# adjacent s_setprio 0 / s_setprio 1 pairs inside the MFMA intervals removed: priority stays raised through all 16 (32) MFMAs of an interval
# baseline (speedup 1.0000x reference)
; #define PG8_STAGE(bufoff, gbase, voff) do { PG8_GLDS((const char*)(gbase), (voff)[0], ldsb + (bufoff)); PG8_GLDS((const char*)(gbase), (voff)[1], ldsb + (bufoff) + 8192u); } while (0)
; #define PG8_STAGEA(bufoff, gbase, o0, o1) do { PG8_GLDS((const char*)(gbase), (o0), ldsb + (bufoff)); PG8_GLDS((const char*)(gbase), (o1), ldsb + (bufoff) + 8192u); } while (0)
; #define PG8_STAGEA1(bufoff, gbase) do { if constexpr (Sched::GATHER) { PG8_STAGEA(bufoff, gbase, vA2, vA3); } else { PG8_STAGEA(bufoff, (gbase) + hstep, vA0, vA1); } } while (0)
; #define PG8_LDA(dst, b, h) do { if constexpr (F8) { _Pragma("unroll") for (int m = 0; m < 4; ++m) dst##8[m] = PG8_LD32(lds + PG8_SA(b, h) + aoff + m * 2048); } else { \
;         _Pragma("unroll") for (int m = 0; m < 4; ++m) _Pragma("unroll") for (int k = 0; k < 2; ++k) dst[m][k] = *(const LAS bf16x8*)(lds + PG8_SA(b, h) + aoff + m * 2048 + k * 1024); } } while (0)
; #define PG8_LDB(dst, b, h) do { if constexpr (F8) { _Pragma("unroll") for (int n = 0; n < 2; ++n) dst##8[n] = PG8_LD32(lds + PG8_SB(b, h) + boff + n * 2048); } else { \
;         _Pragma("unroll") for (int n = 0; n < 2; ++n) _Pragma("unroll") for (int k = 0; k < 2; ++k) dst[n][k] = *(const LAS bf16x8*)(lds + PG8_SB(b, h) + boff + n * 2048 + k * 1024); } } while (0)
; #define PG8_WAIT_VR() PG8_WAIT_V(8)
; #define PG8_WAIT_VX() do { if (relax) asm volatile("s_waitcnt vmcnt(%0)" :: "n"(8 + Epi::RELAX) : "memory"); else PG8_WAIT_V(8); } while (0)
; #define PG8_WAIT_L(n) asm volatile("s_waitcnt lgkmcnt(" #n ")" ::: "memory")
; #define PG8_BAR __builtin_amdgcn_s_barrier()
; template <class Epi, class Sched, bool F8 = false, bool PF = false, bool I8 = false, int PID = -1>
; __device__ __forceinline__ void gemm_phase(LAS unsigned char* lds, LAS unsigned char* xlds, const int RP, const int RPB, const int nt, const Sched& S, const Epi& E, const int stagger_ticks) {
;     ...
;             PG8_LDA(At, 0, 1); PG8_STAGE(PG8_SB(0, 0), b2, voffB); PG8_STAGE(PG8_SB(0, 1), b2 + hstepB, voffB); PG8_STAGEA(PG8_SA(0, 0), a2, vA0, vA1);
;             PG8_WAIT_VX(); PG8_WAIT_L(0); PG8_BAR; PG8_MMA(1, 0, At, B0); PG8_MMA(1, 1, At, B1); PG8_BAR; PG8_SCHED;
;             PG8_LDB(B0, 1, 0); PG8_LDB(B1, 1, 1); PG8_SCHED; PG8_LDA(At, 1, 0); PG8_STAGEA1(PG8_SA(0, 1), a2);
;             PG8_WAIT_VR(); PG8_WAIT_L(0); PG8_BAR; PG8_MMA(0, 0, At, B0); PG8_MMA(0, 1, At, B1); PG8_BAR; PG8_SCHED;
.LBB0_213:
	s_add_u32 s48, s2, 0xfffe0080
	s_addc_u32 s49, s3, -1
	s_cmp_eq_u32 s79, 4
	s_cselect_b32 s62, s10, s48
	s_cselect_b32 s63, s11, s49
	s_cselect_b32 s50, s12, s76
	s_cselect_b32 s51, s13, s77
	s_add_u32 s48, s62, 0x80
	s_addc_u32 s49, s63, 0
	s_add_u32 s60, s50, 0x80
	s_addc_u32 s61, s51, 0
	ds_read_b128 v[122:125], v185 offset:16384
	ds_read_b128 v[126:129], v185 offset:17408
	ds_read_b128 v[138:141], v185 offset:18432
	ds_read_b128 v[142:145], v185 offset:19456
	ds_read_b128 v[186:189], v185 offset:20480
	ds_read_b128 v[190:193], v185 offset:21504
	ds_read_b128 v[194:197], v185 offset:22528
	ds_read_b128 v[198:201], v185 offset:23552
	s_add_i32 s83, s82, 0x10000
	s_mov_b32 m0, s83
	s_nop 0
	global_load_lds_dwordx4 v182, s[50:51]
	s_add_i32 s83, s82, 0x12000
	s_mov_b32 m0, s83
	s_nop 0
	global_load_lds_dwordx4 v183, s[50:51]
	s_add_u32 s86, s50, 0x2000
	s_addc_u32 s87, s51, 0
	s_add_i32 s83, s82, 0x14000
	s_mov_b32 m0, s83
	s_nop 0
	global_load_lds_dwordx4 v182, s[86:87]
	s_add_i32 s83, s82, 0x16000
	s_mov_b32 m0, s83
	s_nop 0
	global_load_lds_dwordx4 v183, s[86:87]
	s_add_i32 s83, s82, 0x2000
	s_mov_b32 m0, s82
	s_nop 0
	global_load_lds_dwordx4 v180, s[62:63]
	s_nop 0
	s_mov_b32 m0, s83
	s_nop 0
	global_load_lds_dwordx4 v181, s[62:63]
	s_waitcnt vmcnt(8)
	s_waitcnt lgkmcnt(0)
	s_barrier
	s_setprio 1
	s_waitcnt lgkmcnt(7)
	v_mfma_i32_16x16x64_i8 v[78:81], v[162:165], v[122:125], v[78:81]
	v_mfma_i32_16x16x64_i8 v[74:77], v[170:173], v[122:125], v[74:77]
	s_waitcnt lgkmcnt(5)
	v_mfma_i32_16x16x64_i8 v[50:53], v[162:165], v[138:141], v[50:53]
	v_mfma_i32_16x16x64_i8 v[42:45], v[170:173], v[138:141], v[42:45]
	s_waitcnt lgkmcnt(3)
	v_mfma_i32_16x16x64_i8 v[30:33], v[162:165], v[186:189], v[30:33]
	v_mfma_i32_16x16x64_i8 v[26:29], v[170:173], v[186:189], v[26:29]
	s_waitcnt lgkmcnt(1)
	v_mfma_i32_16x16x64_i8 v[14:17], v[162:165], v[194:197], v[14:17]
	v_mfma_i32_16x16x64_i8 v[10:13], v[170:173], v[194:197], v[10:13]
	v_mfma_i32_16x16x64_i8 v[78:81], v[166:169], v[126:129], v[78:81]
	v_mfma_i32_16x16x64_i8 v[74:77], v[174:177], v[126:129], v[74:77]
	v_mfma_i32_16x16x64_i8 v[50:53], v[166:169], v[142:145], v[50:53]
	v_mfma_i32_16x16x64_i8 v[42:45], v[174:177], v[142:145], v[42:45]
	v_mfma_i32_16x16x64_i8 v[30:33], v[166:169], v[190:193], v[30:33]
	v_mfma_i32_16x16x64_i8 v[26:29], v[174:177], v[190:193], v[26:29]
	s_waitcnt lgkmcnt(0)
	v_mfma_i32_16x16x64_i8 v[14:17], v[166:169], v[198:201], v[14:17]
	v_mfma_i32_16x16x64_i8 v[10:13], v[174:177], v[198:201], v[10:13]
	v_mfma_i32_16x16x64_i8 v[70:73], v[146:149], v[122:125], v[70:73]
	v_mfma_i32_16x16x64_i8 v[62:65], v[154:157], v[122:125], v[62:65]
	v_mfma_i32_16x16x64_i8 v[38:41], v[146:149], v[138:141], v[38:41]
	v_mfma_i32_16x16x64_i8 v[34:37], v[154:157], v[138:141], v[34:37]
	v_mfma_i32_16x16x64_i8 v[22:25], v[146:149], v[186:189], v[22:25]
	v_mfma_i32_16x16x64_i8 v[18:21], v[154:157], v[186:189], v[18:21]
	v_mfma_i32_16x16x64_i8 v[6:9], v[146:149], v[194:197], v[6:9]
	v_mfma_i32_16x16x64_i8 v[2:5], v[154:157], v[194:197], v[2:5]
	v_mfma_i32_16x16x64_i8 v[70:73], v[150:153], v[126:129], v[70:73]
	v_mfma_i32_16x16x64_i8 v[62:65], v[158:161], v[126:129], v[62:65]
	v_mfma_i32_16x16x64_i8 v[38:41], v[150:153], v[142:145], v[38:41]
	v_mfma_i32_16x16x64_i8 v[34:37], v[158:161], v[142:145], v[34:37]
	v_mfma_i32_16x16x64_i8 v[22:25], v[150:153], v[190:193], v[22:25]
	v_mfma_i32_16x16x64_i8 v[18:21], v[158:161], v[190:193], v[18:21]
	v_mfma_i32_16x16x64_i8 v[6:9], v[150:153], v[198:201], v[6:9]
	v_mfma_i32_16x16x64_i8 v[2:5], v[158:161], v[198:201], v[2:5]
	s_setprio 0
	s_barrier
	v_add_u32_e32 v122, 0x18000, v184
	ds_read_b128 v[146:149], v122
	ds_read_b128 v[150:153], v122 offset:1024
	ds_read_b128 v[154:157], v122 offset:2048
	ds_read_b128 v[158:161], v122 offset:3072
	v_add_u32_e32 v122, 0x1c000, v184
	ds_read_b128 v[162:165], v122
	ds_read_b128 v[166:169], v122 offset:1024
	ds_read_b128 v[170:173], v122 offset:2048
	ds_read_b128 v[174:177], v122 offset:3072
	ds_read_b128 v[186:189], v185 offset:32768
	ds_read_b128 v[190:193], v185 offset:33792
	ds_read_b128 v[194:197], v185 offset:34816
	ds_read_b128 v[198:201], v185 offset:35840
	ds_read_b128 v[202:205], v185 offset:36864
	ds_read_b128 v[206:209], v185 offset:37888
	ds_read_b128 v[210:213], v185 offset:38912
	ds_read_b128 v[214:217], v185 offset:39936
	s_add_u32 s62, s62, 0x20000
	s_addc_u32 s63, s63, 0
	s_add_i32 s83, s82, 0x4000
	s_mov_b32 m0, s83
	s_nop 0
	global_load_lds_dwordx4 v180, s[62:63]
	s_add_i32 s83, s82, 0x6000
	s_mov_b32 m0, s83
	s_nop 0
	global_load_lds_dwordx4 v181, s[62:63]
	s_waitcnt vmcnt(8)
	s_waitcnt lgkmcnt(0)
	s_barrier
; #define PG8_STAGE(bufoff, gbase, voff) do { PG8_GLDS((const char*)(gbase), (voff)[0], ldsb + (bufoff)); PG8_GLDS((const char*)(gbase), (voff)[1], ldsb + (bufoff) + 8192u); } while (0)
; #define PG8_STAGEA(bufoff, gbase, o0, o1) do { PG8_GLDS((const char*)(gbase), (o0), ldsb + (bufoff)); PG8_GLDS((const char*)(gbase), (o1), ldsb + (bufoff) + 8192u); } while (0)
; #define PG8_LDA(dst, b, h) do { if constexpr (F8) { _Pragma("unroll") for (int m = 0; m < 4; ++m) dst##8[m] = PG8_LD32(lds + PG8_SA(b, h) + aoff + m * 2048); } else { \
;         _Pragma("unroll") for (int m = 0; m < 4; ++m) _Pragma("unroll") for (int k = 0; k < 2; ++k) dst[m][k] = *(const LAS bf16x8*)(lds + PG8_SA(b, h) + aoff + m * 2048 + k * 1024); } } while (0)
; #define PG8_WAIT_VR() PG8_WAIT_V(8)
; #define PG8_WAIT_L(n) asm volatile("s_waitcnt lgkmcnt(" #n ")" ::: "memory")
; #define PG8_BAR __builtin_amdgcn_s_barrier()
; #define PG8_SCHED __builtin_amdgcn_sched_barrier(0)
; template <class Epi, class Sched, bool F8 = false, bool PF = false, bool I8 = false, int PID = -1>
; __device__ __forceinline__ void gemm_phase(LAS unsigned char* lds, LAS unsigned char* xlds, const int RP, const int RPB, const int nt, const Sched& S, const Epi& E, const int stagger_ticks) {
;     ...
;             PG8_WAIT_VR(); PG8_WAIT_L(0); PG8_BAR; PG8_MMA(0, 0, At, B0); PG8_MMA(0, 1, At, B1); PG8_BAR; PG8_SCHED;
;             PG8_LDA(At, 1, 1); PG8_STAGE(PG8_SB(1, 0), b3, voffB); PG8_STAGE(PG8_SB(1, 1), b3 + hstepB, voffB); PG8_STAGEA(PG8_SA(1, 0), a3, vA0, vA1);
;             PG8_WAIT_VR(); PG8_WAIT_L(0); PG8_BAR; PG8_MMA(1, 0, At, B0); PG8_MMA(1, 1, At, B1); PG8_BAR; PG8_SCHED;
;         }
	s_setprio 1
	s_waitcnt lgkmcnt(7)
	v_mfma_i32_16x16x64_i8 v[46:49], v[146:149], v[186:189], v[46:49]
	s_waitcnt lgkmcnt(6)
	v_mfma_i32_16x16x64_i8 v[142:145], v[150:153], v[190:193], v[46:49]
	v_mfma_i32_16x16x64_i8 v[46:49], v[154:157], v[186:189], v[54:57]
	v_mfma_i32_16x16x64_i8 v[138:141], v[158:161], v[190:193], v[46:49]
	s_waitcnt lgkmcnt(5)
	v_mfma_i32_16x16x64_i8 v[46:49], v[146:149], v[194:197], v[58:61]
	s_waitcnt lgkmcnt(4)
	v_mfma_i32_16x16x64_i8 v[126:129], v[150:153], v[198:201], v[46:49]
	v_mfma_i32_16x16x64_i8 v[46:49], v[154:157], v[194:197], v[66:69]
	v_mfma_i32_16x16x64_i8 v[122:125], v[158:161], v[198:201], v[46:49]
	s_waitcnt lgkmcnt(3)
	v_mfma_i32_16x16x64_i8 v[46:49], v[146:149], v[202:205], v[110:113]
	s_waitcnt lgkmcnt(2)
	v_mfma_i32_16x16x64_i8 v[110:113], v[150:153], v[206:209], v[46:49]
	v_mfma_i32_16x16x64_i8 v[46:49], v[154:157], v[202:205], v[106:109]
	v_mfma_i32_16x16x64_i8 v[106:109], v[158:161], v[206:209], v[46:49]
	s_waitcnt lgkmcnt(1)
	v_mfma_i32_16x16x64_i8 v[46:49], v[146:149], v[210:213], v[94:97]
	s_waitcnt lgkmcnt(0)
	v_mfma_i32_16x16x64_i8 v[94:97], v[150:153], v[214:217], v[46:49]
	v_mfma_i32_16x16x64_i8 v[46:49], v[154:157], v[210:213], v[90:93]
	v_mfma_i32_16x16x64_i8 v[90:93], v[158:161], v[214:217], v[46:49]
	v_mfma_i32_16x16x64_i8 v[46:49], v[162:165], v[186:189], v[134:137]
	v_mfma_i32_16x16x64_i8 v[134:137], v[166:169], v[190:193], v[46:49]
	v_mfma_i32_16x16x64_i8 v[46:49], v[170:173], v[186:189], v[130:133]
	v_mfma_i32_16x16x64_i8 v[130:133], v[174:177], v[190:193], v[46:49]
	v_mfma_i32_16x16x64_i8 v[46:49], v[162:165], v[194:197], v[118:121]
	v_mfma_i32_16x16x64_i8 v[118:121], v[166:169], v[198:201], v[46:49]
	v_mfma_i32_16x16x64_i8 v[46:49], v[170:173], v[194:197], v[114:117]
	v_mfma_i32_16x16x64_i8 v[114:117], v[174:177], v[198:201], v[46:49]
	v_mfma_i32_16x16x64_i8 v[46:49], v[162:165], v[202:205], v[102:105]
	v_mfma_i32_16x16x64_i8 v[102:105], v[166:169], v[206:209], v[46:49]
	v_mfma_i32_16x16x64_i8 v[46:49], v[170:173], v[202:205], v[98:101]
	v_mfma_i32_16x16x64_i8 v[98:101], v[174:177], v[206:209], v[46:49]
	v_mfma_i32_16x16x64_i8 v[46:49], v[162:165], v[210:213], v[86:89]
	v_mfma_i32_16x16x64_i8 v[86:89], v[166:169], v[214:217], v[46:49]
	v_mfma_i32_16x16x64_i8 v[46:49], v[170:173], v[210:213], v[82:85]
	v_mfma_i32_16x16x64_i8 v[82:85], v[174:177], v[214:217], v[46:49]
	s_setprio 0
	s_barrier
	s_nop 4
	ds_read_b128 v[46:49], v185 offset:49152
	ds_read_b128 v[54:57], v185 offset:50176
	ds_read_b128 v[58:61], v185 offset:51200
	ds_read_b128 v[66:69], v185 offset:52224
	ds_read_b128 v[186:189], v185 offset:53248
	ds_read_b128 v[190:193], v185 offset:54272
	ds_read_b128 v[194:197], v185 offset:55296
	ds_read_b128 v[198:201], v185 offset:56320
	s_add_i32 s62, s82, 0x18000
	s_mov_b32 m0, s62
	s_nop 0
	global_load_lds_dwordx4 v182, s[60:61]
	s_add_i32 s62, s82, 0x1a000
	s_mov_b32 m0, s62
	s_nop 0
	global_load_lds_dwordx4 v183, s[60:61]
	s_add_u32 s50, s50, 0x2080
	s_addc_u32 s51, s51, 0
	s_add_i32 s60, s82, 0x1c000
	s_mov_b32 m0, s60
	s_nop 0
	global_load_lds_dwordx4 v182, s[50:51]
	s_add_i32 s60, s82, 0x1e000
	s_mov_b32 m0, s60
	s_nop 0
	global_load_lds_dwordx4 v183, s[50:51]
	s_add_i32 s50, s82, 0x8000
	s_mov_b32 m0, s50
	s_nop 0
	global_load_lds_dwordx4 v180, s[48:49]
	s_add_i32 s82, s82, 0xa000
	s_mov_b32 m0, s82
	s_nop 0
	global_load_lds_dwordx4 v181, s[48:49]
	s_waitcnt vmcnt(8)
	s_waitcnt lgkmcnt(0)
	s_barrier
	s_setprio 1
	s_waitcnt lgkmcnt(7)
	v_mfma_i32_16x16x64_i8 v[78:81], v[146:149], v[46:49], v[78:81]
	v_mfma_i32_16x16x64_i8 v[74:77], v[154:157], v[46:49], v[74:77]
	s_waitcnt lgkmcnt(5)
	v_mfma_i32_16x16x64_i8 v[50:53], v[146:149], v[58:61], v[50:53]
	v_mfma_i32_16x16x64_i8 v[42:45], v[154:157], v[58:61], v[42:45]
	s_waitcnt lgkmcnt(3)
	v_mfma_i32_16x16x64_i8 v[30:33], v[146:149], v[186:189], v[30:33]
	v_mfma_i32_16x16x64_i8 v[26:29], v[154:157], v[186:189], v[26:29]
	s_waitcnt lgkmcnt(1)
	v_mfma_i32_16x16x64_i8 v[14:17], v[146:149], v[194:197], v[14:17]
	v_mfma_i32_16x16x64_i8 v[10:13], v[154:157], v[194:197], v[10:13]
	v_mfma_i32_16x16x64_i8 v[78:81], v[150:153], v[54:57], v[78:81]
	v_mfma_i32_16x16x64_i8 v[74:77], v[158:161], v[54:57], v[74:77]
	v_mfma_i32_16x16x64_i8 v[50:53], v[150:153], v[66:69], v[50:53]
	v_mfma_i32_16x16x64_i8 v[42:45], v[158:161], v[66:69], v[42:45]
	v_mfma_i32_16x16x64_i8 v[30:33], v[150:153], v[190:193], v[30:33]
	v_mfma_i32_16x16x64_i8 v[26:29], v[158:161], v[190:193], v[26:29]
	s_waitcnt lgkmcnt(0)
	v_mfma_i32_16x16x64_i8 v[14:17], v[150:153], v[198:201], v[14:17]
	v_mfma_i32_16x16x64_i8 v[10:13], v[158:161], v[198:201], v[10:13]
	v_mfma_i32_16x16x64_i8 v[70:73], v[162:165], v[46:49], v[70:73]
	v_mfma_i32_16x16x64_i8 v[46:49], v[170:173], v[46:49], v[62:65]
	v_mfma_i32_16x16x64_i8 v[38:41], v[162:165], v[58:61], v[38:41]
	v_mfma_i32_16x16x64_i8 v[34:37], v[170:173], v[58:61], v[34:37]
	v_mfma_i32_16x16x64_i8 v[22:25], v[162:165], v[186:189], v[22:25]
	v_mfma_i32_16x16x64_i8 v[18:21], v[170:173], v[186:189], v[18:21]
	v_mfma_i32_16x16x64_i8 v[6:9], v[162:165], v[194:197], v[6:9]
	v_mfma_i32_16x16x64_i8 v[2:5], v[170:173], v[194:197], v[2:5]
	v_mfma_i32_16x16x64_i8 v[70:73], v[166:169], v[54:57], v[70:73]
	v_mfma_i32_16x16x64_i8 v[62:65], v[174:177], v[54:57], v[46:49]
	v_mfma_i32_16x16x64_i8 v[38:41], v[166:169], v[66:69], v[38:41]
	v_mfma_i32_16x16x64_i8 v[34:37], v[174:177], v[66:69], v[34:37]
	v_mfma_i32_16x16x64_i8 v[22:25], v[166:169], v[190:193], v[22:25]
	v_mfma_i32_16x16x64_i8 v[18:21], v[174:177], v[190:193], v[18:21]
	v_mfma_i32_16x16x64_i8 v[6:9], v[166:169], v[198:201], v[6:9]
	v_mfma_i32_16x16x64_i8 v[2:5], v[174:177], v[198:201], v[2:5]
	s_setprio 0
	s_barrier
	s_add_i32 s79, s79, 2
	s_add_u32 s76, s76, 0x100
	s_addc_u32 s77, s77, 0
	s_add_u32 s2, s2, 0x100
	s_addc_u32 s3, s3, 0
	s_cmp_gt_u32 s79, 5
	s_cbranch_scc1 .LBB0_216
; #define PG8_STAGE(bufoff, gbase, voff) do { PG8_GLDS((const char*)(gbase), (voff)[0], ldsb + (bufoff)); PG8_GLDS((const char*)(gbase), (voff)[1], ldsb + (bufoff) + 8192u); } while (0)
; #define PG8_STAGEA(bufoff, gbase, o0, o1) do { PG8_GLDS((const char*)(gbase), (o0), ldsb + (bufoff)); PG8_GLDS((const char*)(gbase), (o1), ldsb + (bufoff) + 8192u); } while (0)
; #define PG8_STAGEA1(bufoff, gbase) do { if constexpr (Sched::GATHER) { PG8_STAGEA(bufoff, gbase, vA2, vA3); } else { PG8_STAGEA(bufoff, (gbase) + hstep, vA0, vA1); } } while (0)
; #define PG8_LDA(dst, b, h) do { if constexpr (F8) { _Pragma("unroll") for (int m = 0; m < 4; ++m) dst##8[m] = PG8_LD32(lds + PG8_SA(b, h) + aoff + m * 2048); } else { \
;         _Pragma("unroll") for (int m = 0; m < 4; ++m) _Pragma("unroll") for (int k = 0; k < 2; ++k) dst[m][k] = *(const LAS bf16x8*)(lds + PG8_SA(b, h) + aoff + m * 2048 + k * 1024); } } while (0)
; #define PG8_LDB(dst, b, h) do { if constexpr (F8) { _Pragma("unroll") for (int n = 0; n < 2; ++n) dst##8[n] = PG8_LD32(lds + PG8_SB(b, h) + boff + n * 2048); } else { \
;         _Pragma("unroll") for (int n = 0; n < 2; ++n) _Pragma("unroll") for (int k = 0; k < 2; ++k) dst[n][k] = *(const LAS bf16x8*)(lds + PG8_SB(b, h) + boff + n * 2048 + k * 1024); } } while (0)
; template <class Epi, class Sched, bool F8 = false, bool PF = false, bool I8 = false, int PID = -1>
; __device__ __forceinline__ void gemm_phase(LAS unsigned char* lds, LAS unsigned char* xlds, const int RP, const int RPB, const int nt, const Sched& S, const Epi& E, const int stagger_ticks) {
;     ...
;             PG8_LDB(B0, 0, 0); PG8_LDB(B1, 0, 1); PG8_SCHED; PG8_LDA(At, 0, 0); PG8_STAGEA1(PG8_SA(1, 1), a1);
;             if (Sched::GATHER) { if (last) { const u32x4 nv = *nslot; vA0 = nv.x; vA1 = nv.y; vA2 = nv.z; vA3 = nv.w; } }
;             PG8_WAIT_VX(); PG8_WAIT_L(0); PG8_BAR; PG8_MMA(0, 0, At, B0); PG8_MMA(0, 1, At, B1); PG8_BAR; PG8_SCHED;
;             if constexpr (Epi::BIAS_DMA) { if (t == 0 && has_next) E.bias_dma(nxt, xlds + 8192 + ((ui + 1) & 1) * Epi::BIAS_STRIDE, wid, lane); }
;             PG8_LDA(At, 0, 1); PG8_STAGE(PG8_SB(0, 0), b2, voffB); PG8_STAGE(PG8_SB(0, 1), b2 + hstepB, voffB); PG8_STAGEA(PG8_SA(0, 0), a2, vA0, vA1);
;             PG8_WAIT_VX(); PG8_WAIT_L(0); PG8_BAR; PG8_MMA(1, 0, At, B0); PG8_MMA(1, 1, At, B1); PG8_BAR; PG8_SCHED;
.LBB0_214:
	s_mov_b32 s82, s7
	v_add_u32_e32 v46, 0x10000, v184
	ds_read_b128 v[162:165], v46
	ds_read_b128 v[166:169], v46 offset:1024
	ds_read_b128 v[170:173], v46 offset:2048
	ds_read_b128 v[174:177], v46 offset:3072
	v_add_u32_e32 v46, 0x14000, v184
	ds_read_b128 v[146:149], v46
	ds_read_b128 v[150:153], v46 offset:1024
	ds_read_b128 v[154:157], v46 offset:2048
	ds_read_b128 v[158:161], v46 offset:3072
	ds_read_b128 v[186:189], v185
	ds_read_b128 v[190:193], v185 offset:1024
	ds_read_b128 v[194:197], v185 offset:2048
	ds_read_b128 v[198:201], v185 offset:3072
	ds_read_b128 v[202:205], v185 offset:4096
	ds_read_b128 v[206:209], v185 offset:5120
	ds_read_b128 v[210:213], v185 offset:6144
	ds_read_b128 v[214:217], v185 offset:7168
	s_add_i32 s48, s82, 0xc000
	s_mov_b32 m0, s48
	s_nop 0
	global_load_lds_dwordx4 v180, s[2:3]
	s_add_i32 s48, s82, 0xe000
	s_mov_b32 m0, s48
	s_nop 0
	global_load_lds_dwordx4 v181, s[2:3]
	s_waitcnt vmcnt(8)
	s_waitcnt lgkmcnt(0)
	s_barrier
	s_setprio 1
	s_waitcnt lgkmcnt(7)
	v_mfma_i32_16x16x64_i8 v[46:49], v[162:165], v[186:189], v[142:145]
	v_mfma_i32_16x16x64_i8 v[54:57], v[170:173], v[186:189], v[138:141]
	s_waitcnt lgkmcnt(5)
	v_mfma_i32_16x16x64_i8 v[58:61], v[162:165], v[194:197], v[126:129]
	v_mfma_i32_16x16x64_i8 v[66:69], v[170:173], v[194:197], v[122:125]
	s_waitcnt lgkmcnt(3)
	v_mfma_i32_16x16x64_i8 v[110:113], v[162:165], v[202:205], v[110:113]
	v_mfma_i32_16x16x64_i8 v[106:109], v[170:173], v[202:205], v[106:109]
	s_waitcnt lgkmcnt(1)
	v_mfma_i32_16x16x64_i8 v[94:97], v[162:165], v[210:213], v[94:97]
	v_mfma_i32_16x16x64_i8 v[90:93], v[170:173], v[210:213], v[90:93]
	v_mfma_i32_16x16x64_i8 v[46:49], v[166:169], v[190:193], v[46:49]
	v_mfma_i32_16x16x64_i8 v[54:57], v[174:177], v[190:193], v[54:57]
	v_mfma_i32_16x16x64_i8 v[58:61], v[166:169], v[198:201], v[58:61]
	v_mfma_i32_16x16x64_i8 v[66:69], v[174:177], v[198:201], v[66:69]
	v_mfma_i32_16x16x64_i8 v[110:113], v[166:169], v[206:209], v[110:113]
	v_mfma_i32_16x16x64_i8 v[106:109], v[174:177], v[206:209], v[106:109]
	s_waitcnt lgkmcnt(0)
	v_mfma_i32_16x16x64_i8 v[94:97], v[166:169], v[214:217], v[94:97]
	v_mfma_i32_16x16x64_i8 v[90:93], v[174:177], v[214:217], v[90:93]
	v_mfma_i32_16x16x64_i8 v[122:125], v[146:149], v[186:189], v[134:137]
	v_mfma_i32_16x16x64_i8 v[134:137], v[150:153], v[190:193], v[122:125]
	v_mfma_i32_16x16x64_i8 v[122:125], v[154:157], v[186:189], v[130:133]
	v_mfma_i32_16x16x64_i8 v[118:121], v[146:149], v[194:197], v[118:121]
	v_mfma_i32_16x16x64_i8 v[114:117], v[154:157], v[194:197], v[114:117]
	v_mfma_i32_16x16x64_i8 v[102:105], v[146:149], v[202:205], v[102:105]
	v_mfma_i32_16x16x64_i8 v[98:101], v[154:157], v[202:205], v[98:101]
	v_mfma_i32_16x16x64_i8 v[86:89], v[146:149], v[210:213], v[86:89]
	v_mfma_i32_16x16x64_i8 v[82:85], v[154:157], v[210:213], v[82:85]
	v_mfma_i32_16x16x64_i8 v[130:133], v[158:161], v[190:193], v[122:125]
	v_mfma_i32_16x16x64_i8 v[118:121], v[150:153], v[198:201], v[118:121]
	v_mfma_i32_16x16x64_i8 v[114:117], v[158:161], v[198:201], v[114:117]
	v_mfma_i32_16x16x64_i8 v[102:105], v[150:153], v[206:209], v[102:105]
	v_mfma_i32_16x16x64_i8 v[98:101], v[158:161], v[206:209], v[98:101]
	v_mfma_i32_16x16x64_i8 v[86:89], v[150:153], v[214:217], v[86:89]
	v_mfma_i32_16x16x64_i8 v[82:85], v[158:161], v[214:217], v[82:85]
	s_setprio 0
	s_barrier
	s_cmp_lg_u32 s79, -2
	s_cselect_b64 s[48:49], -1, 0
	s_or_b64 s[48:49], s[46:47], s[48:49]
	s_and_b64 vcc, exec, s[48:49]
	s_cbranch_vccnz .LBB0_213
	s_mov_b32 m0, s78
	s_nop 0
	global_load_lds_dword v1, s[0:1]
	s_branch .LBB0_213
.Lmy_z1t:
	s_mov_b32 s82, s7
	v_add_u32_e32 v46, 0x10000, v184
	ds_read_b128 v[162:165], v46
	ds_read_b128 v[166:169], v46 offset:1024
	ds_read_b128 v[170:173], v46 offset:2048
	ds_read_b128 v[174:177], v46 offset:3072
	v_add_u32_e32 v46, 0x14000, v184
	ds_read_b128 v[146:149], v46
	ds_read_b128 v[150:153], v46 offset:1024
	ds_read_b128 v[154:157], v46 offset:2048
	ds_read_b128 v[158:161], v46 offset:3072
	ds_read_b128 v[186:189], v185
	ds_read_b128 v[190:193], v185 offset:1024
	ds_read_b128 v[194:197], v185 offset:2048
	ds_read_b128 v[198:201], v185 offset:3072
	ds_read_b128 v[202:205], v185 offset:4096
	ds_read_b128 v[206:209], v185 offset:5120
	ds_read_b128 v[210:213], v185 offset:6144
	ds_read_b128 v[214:217], v185 offset:7168
	s_add_i32 s48, s82, 0xc000
	s_mov_b32 m0, s48
	s_nop 0
	global_load_lds_dwordx4 v180, s[2:3]
	s_add_i32 s48, s82, 0xe000
	s_mov_b32 m0, s48
	s_nop 0
	global_load_lds_dwordx4 v181, s[2:3]
	s_waitcnt vmcnt(8)
	s_waitcnt lgkmcnt(0)
	s_barrier
	s_setprio 1
	s_waitcnt lgkmcnt(7)
	v_mfma_i32_16x16x64_i8 v[46:49], v[162:165], v[186:189], 0
	v_mfma_i32_16x16x64_i8 v[54:57], v[170:173], v[186:189], 0
	s_waitcnt lgkmcnt(5)
	v_mfma_i32_16x16x64_i8 v[58:61], v[162:165], v[194:197], 0
	v_mfma_i32_16x16x64_i8 v[66:69], v[170:173], v[194:197], 0
	s_waitcnt lgkmcnt(3)
	v_mfma_i32_16x16x64_i8 v[110:113], v[162:165], v[202:205], 0
	v_mfma_i32_16x16x64_i8 v[106:109], v[170:173], v[202:205], 0
	s_waitcnt lgkmcnt(1)
	v_mfma_i32_16x16x64_i8 v[94:97], v[162:165], v[210:213], 0
	v_mfma_i32_16x16x64_i8 v[90:93], v[170:173], v[210:213], 0
	v_mfma_i32_16x16x64_i8 v[46:49], v[166:169], v[190:193], v[46:49]
	v_mfma_i32_16x16x64_i8 v[54:57], v[174:177], v[190:193], v[54:57]
	v_mfma_i32_16x16x64_i8 v[58:61], v[166:169], v[198:201], v[58:61]
	v_mfma_i32_16x16x64_i8 v[66:69], v[174:177], v[198:201], v[66:69]
	v_mfma_i32_16x16x64_i8 v[110:113], v[166:169], v[206:209], v[110:113]
	v_mfma_i32_16x16x64_i8 v[106:109], v[174:177], v[206:209], v[106:109]
	s_waitcnt lgkmcnt(0)
	v_mfma_i32_16x16x64_i8 v[94:97], v[166:169], v[214:217], v[94:97]
	v_mfma_i32_16x16x64_i8 v[90:93], v[174:177], v[214:217], v[90:93]
	v_mfma_i32_16x16x64_i8 v[122:125], v[146:149], v[186:189], 0
	v_mfma_i32_16x16x64_i8 v[134:137], v[150:153], v[190:193], v[122:125]
	v_mfma_i32_16x16x64_i8 v[122:125], v[154:157], v[186:189], 0
	v_mfma_i32_16x16x64_i8 v[118:121], v[146:149], v[194:197], 0
	v_mfma_i32_16x16x64_i8 v[114:117], v[154:157], v[194:197], 0
	v_mfma_i32_16x16x64_i8 v[102:105], v[146:149], v[202:205], 0
	v_mfma_i32_16x16x64_i8 v[98:101], v[154:157], v[202:205], 0
	v_mfma_i32_16x16x64_i8 v[86:89], v[146:149], v[210:213], 0
	v_mfma_i32_16x16x64_i8 v[82:85], v[154:157], v[210:213], 0
	v_mfma_i32_16x16x64_i8 v[130:133], v[158:161], v[190:193], v[122:125]
	v_mfma_i32_16x16x64_i8 v[118:121], v[150:153], v[198:201], v[118:121]
	v_mfma_i32_16x16x64_i8 v[114:117], v[158:161], v[198:201], v[114:117]
	v_mfma_i32_16x16x64_i8 v[102:105], v[150:153], v[206:209], v[102:105]
	v_mfma_i32_16x16x64_i8 v[98:101], v[158:161], v[206:209], v[98:101]
	v_mfma_i32_16x16x64_i8 v[86:89], v[150:153], v[214:217], v[86:89]
	v_mfma_i32_16x16x64_i8 v[82:85], v[158:161], v[214:217], v[82:85]
	s_setprio 0
	s_barrier
	s_cmp_lg_u32 s79, -2
	s_cselect_b64 s[48:49], -1, 0
	s_or_b64 s[48:49], s[46:47], s[48:49]
	s_and_b64 vcc, exec, s[48:49]
	s_cbranch_vccnz .Lmy_z1b
	s_mov_b32 m0, s78
	s_nop 0
	global_load_lds_dword v1, s[0:1]
	s_branch .Lmy_z1b
; #define PG8_STAGE(bufoff, gbase, voff) do { PG8_GLDS((const char*)(gbase), (voff)[0], ldsb + (bufoff)); PG8_GLDS((const char*)(gbase), (voff)[1], ldsb + (bufoff) + 8192u); } while (0)
; #define PG8_STAGEA(bufoff, gbase, o0, o1) do { PG8_GLDS((const char*)(gbase), (o0), ldsb + (bufoff)); PG8_GLDS((const char*)(gbase), (o1), ldsb + (bufoff) + 8192u); } while (0)
; #define PG8_STAGEA1(bufoff, gbase) do { if constexpr (Sched::GATHER) { PG8_STAGEA(bufoff, gbase, vA2, vA3); } else { PG8_STAGEA(bufoff, (gbase) + hstep, vA0, vA1); } } while (0)
; #define PG8_LDA(dst, b, h) do { if constexpr (F8) { _Pragma("unroll") for (int m = 0; m < 4; ++m) dst##8[m] = PG8_LD32(lds + PG8_SA(b, h) + aoff + m * 2048); } else { \
;         _Pragma("unroll") for (int m = 0; m < 4; ++m) _Pragma("unroll") for (int k = 0; k < 2; ++k) dst[m][k] = *(const LAS bf16x8*)(lds + PG8_SA(b, h) + aoff + m * 2048 + k * 1024); } } while (0)
; #define PG8_LDB(dst, b, h) do { if constexpr (F8) { _Pragma("unroll") for (int n = 0; n < 2; ++n) dst##8[n] = PG8_LD32(lds + PG8_SB(b, h) + boff + n * 2048); } else { \
;         _Pragma("unroll") for (int n = 0; n < 2; ++n) _Pragma("unroll") for (int k = 0; k < 2; ++k) dst[n][k] = *(const LAS bf16x8*)(lds + PG8_SB(b, h) + boff + n * 2048 + k * 1024); } } while (0)
; #define PG8_WAIT_VR() PG8_WAIT_V(8)
; #define PG8_WAIT_VX() do { if (relax) asm volatile("s_waitcnt vmcnt(%0)" :: "n"(8 + Epi::RELAX) : "memory"); else PG8_WAIT_V(8); } while (0)
; #define PG8_WAIT_L(n) asm volatile("s_waitcnt lgkmcnt(" #n ")" ::: "memory")
; #define PG8_BAR __builtin_amdgcn_s_barrier()
; template <class Epi, class Sched, bool F8 = false, bool PF = false, bool I8 = false, int PID = -1>
; __device__ __forceinline__ void gemm_phase(LAS unsigned char* lds, LAS unsigned char* xlds, const int RP, const int RPB, const int nt, const Sched& S, const Epi& E, const int stagger_ticks) {
;     ...
;             PG8_LDA(At, 0, 1); PG8_STAGE(PG8_SB(0, 0), b2, voffB); PG8_STAGE(PG8_SB(0, 1), b2 + hstepB, voffB); PG8_STAGEA(PG8_SA(0, 0), a2, vA0, vA1);
;             PG8_WAIT_VX(); PG8_WAIT_L(0); PG8_BAR; PG8_MMA(1, 0, At, B0); PG8_MMA(1, 1, At, B1); PG8_BAR; PG8_SCHED;
;             PG8_LDB(B0, 1, 0); PG8_LDB(B1, 1, 1); PG8_SCHED; PG8_LDA(At, 1, 0); PG8_STAGEA1(PG8_SA(0, 1), a2);
;             PG8_WAIT_VR(); PG8_WAIT_L(0); PG8_BAR; PG8_MMA(0, 0, At, B0); PG8_MMA(0, 1, At, B1); PG8_BAR; PG8_SCHED;
.Lmy_z1b:
	s_add_u32 s48, s2, 0xfffe0080
	s_addc_u32 s49, s3, -1
	s_cmp_eq_u32 s79, 4
	s_cselect_b32 s62, s10, s48
	s_cselect_b32 s63, s11, s49
	s_cselect_b32 s50, s12, s76
	s_cselect_b32 s51, s13, s77
	s_add_u32 s48, s62, 0x80
	s_addc_u32 s49, s63, 0
	s_add_u32 s60, s50, 0x80
	s_addc_u32 s61, s51, 0
	ds_read_b128 v[122:125], v185 offset:16384
	ds_read_b128 v[126:129], v185 offset:17408
	ds_read_b128 v[138:141], v185 offset:18432
	ds_read_b128 v[142:145], v185 offset:19456
	ds_read_b128 v[186:189], v185 offset:20480
	ds_read_b128 v[190:193], v185 offset:21504
	ds_read_b128 v[194:197], v185 offset:22528
	ds_read_b128 v[198:201], v185 offset:23552
	s_add_i32 s83, s82, 0x10000
	s_mov_b32 m0, s83
	s_nop 0
	global_load_lds_dwordx4 v182, s[50:51]
	s_add_i32 s83, s82, 0x12000
	s_mov_b32 m0, s83
	s_nop 0
	global_load_lds_dwordx4 v183, s[50:51]
	s_add_u32 s86, s50, 0x2000
	s_addc_u32 s87, s51, 0
	s_add_i32 s83, s82, 0x14000
	s_mov_b32 m0, s83
	s_nop 0
	global_load_lds_dwordx4 v182, s[86:87]
	s_add_i32 s83, s82, 0x16000
	s_mov_b32 m0, s83
	s_nop 0
	global_load_lds_dwordx4 v183, s[86:87]
	s_add_i32 s83, s82, 0x2000
	s_mov_b32 m0, s82
	s_nop 0
	global_load_lds_dwordx4 v180, s[62:63]
	s_nop 0
	s_mov_b32 m0, s83
	s_nop 0
	global_load_lds_dwordx4 v181, s[62:63]
	s_waitcnt vmcnt(8)
	s_waitcnt lgkmcnt(0)
	s_barrier
	s_setprio 1
	s_waitcnt lgkmcnt(7)
	v_mfma_i32_16x16x64_i8 v[78:81], v[162:165], v[122:125], 0
	v_mfma_i32_16x16x64_i8 v[74:77], v[170:173], v[122:125], 0
	s_waitcnt lgkmcnt(5)
	v_mfma_i32_16x16x64_i8 v[50:53], v[162:165], v[138:141], 0
	v_mfma_i32_16x16x64_i8 v[42:45], v[170:173], v[138:141], 0
	s_waitcnt lgkmcnt(3)
	v_mfma_i32_16x16x64_i8 v[30:33], v[162:165], v[186:189], 0
	v_mfma_i32_16x16x64_i8 v[26:29], v[170:173], v[186:189], 0
	s_waitcnt lgkmcnt(1)
	v_mfma_i32_16x16x64_i8 v[14:17], v[162:165], v[194:197], 0
	v_mfma_i32_16x16x64_i8 v[10:13], v[170:173], v[194:197], 0
	v_mfma_i32_16x16x64_i8 v[78:81], v[166:169], v[126:129], v[78:81]
	v_mfma_i32_16x16x64_i8 v[74:77], v[174:177], v[126:129], v[74:77]
	v_mfma_i32_16x16x64_i8 v[50:53], v[166:169], v[142:145], v[50:53]
	v_mfma_i32_16x16x64_i8 v[42:45], v[174:177], v[142:145], v[42:45]
	v_mfma_i32_16x16x64_i8 v[30:33], v[166:169], v[190:193], v[30:33]
	v_mfma_i32_16x16x64_i8 v[26:29], v[174:177], v[190:193], v[26:29]
	s_waitcnt lgkmcnt(0)
	v_mfma_i32_16x16x64_i8 v[14:17], v[166:169], v[198:201], v[14:17]
	v_mfma_i32_16x16x64_i8 v[10:13], v[174:177], v[198:201], v[10:13]
	v_mfma_i32_16x16x64_i8 v[70:73], v[146:149], v[122:125], 0
	v_mfma_i32_16x16x64_i8 v[62:65], v[154:157], v[122:125], 0
	v_mfma_i32_16x16x64_i8 v[38:41], v[146:149], v[138:141], 0
	v_mfma_i32_16x16x64_i8 v[34:37], v[154:157], v[138:141], 0
	v_mfma_i32_16x16x64_i8 v[22:25], v[146:149], v[186:189], 0
	v_mfma_i32_16x16x64_i8 v[18:21], v[154:157], v[186:189], 0
	v_mfma_i32_16x16x64_i8 v[6:9], v[146:149], v[194:197], 0
	v_mfma_i32_16x16x64_i8 v[2:5], v[154:157], v[194:197], 0
	v_mfma_i32_16x16x64_i8 v[70:73], v[150:153], v[126:129], v[70:73]
	v_mfma_i32_16x16x64_i8 v[62:65], v[158:161], v[126:129], v[62:65]
	v_mfma_i32_16x16x64_i8 v[38:41], v[150:153], v[142:145], v[38:41]
	v_mfma_i32_16x16x64_i8 v[34:37], v[158:161], v[142:145], v[34:37]
	v_mfma_i32_16x16x64_i8 v[22:25], v[150:153], v[190:193], v[22:25]
	v_mfma_i32_16x16x64_i8 v[18:21], v[158:161], v[190:193], v[18:21]
	v_mfma_i32_16x16x64_i8 v[6:9], v[150:153], v[198:201], v[6:9]
	v_mfma_i32_16x16x64_i8 v[2:5], v[158:161], v[198:201], v[2:5]
	s_setprio 0
	s_barrier
	v_add_u32_e32 v122, 0x18000, v184
	ds_read_b128 v[146:149], v122
	ds_read_b128 v[150:153], v122 offset:1024
	ds_read_b128 v[154:157], v122 offset:2048
	ds_read_b128 v[158:161], v122 offset:3072
	v_add_u32_e32 v122, 0x1c000, v184
	ds_read_b128 v[162:165], v122
	ds_read_b128 v[166:169], v122 offset:1024
	ds_read_b128 v[170:173], v122 offset:2048
	ds_read_b128 v[174:177], v122 offset:3072
	ds_read_b128 v[186:189], v185 offset:32768
	ds_read_b128 v[190:193], v185 offset:33792
	ds_read_b128 v[194:197], v185 offset:34816
	ds_read_b128 v[198:201], v185 offset:35840
	ds_read_b128 v[202:205], v185 offset:36864
	ds_read_b128 v[206:209], v185 offset:37888
	ds_read_b128 v[210:213], v185 offset:38912
	ds_read_b128 v[214:217], v185 offset:39936
	s_add_u32 s62, s62, 0x20000
	s_addc_u32 s63, s63, 0
	s_add_i32 s83, s82, 0x4000
	s_mov_b32 m0, s83
	s_nop 0
	global_load_lds_dwordx4 v180, s[62:63]
	s_add_i32 s83, s82, 0x6000
	s_mov_b32 m0, s83
	s_nop 0
	global_load_lds_dwordx4 v181, s[62:63]
	s_waitcnt vmcnt(8)
	s_waitcnt lgkmcnt(0)
	s_barrier
; #define PG8_STAGE(bufoff, gbase, voff) do { PG8_GLDS((const char*)(gbase), (voff)[0], ldsb + (bufoff)); PG8_GLDS((const char*)(gbase), (voff)[1], ldsb + (bufoff) + 8192u); } while (0)
; #define PG8_STAGEA(bufoff, gbase, o0, o1) do { PG8_GLDS((const char*)(gbase), (o0), ldsb + (bufoff)); PG8_GLDS((const char*)(gbase), (o1), ldsb + (bufoff) + 8192u); } while (0)
; #define PG8_LDA(dst, b, h) do { if constexpr (F8) { _Pragma("unroll") for (int m = 0; m < 4; ++m) dst##8[m] = PG8_LD32(lds + PG8_SA(b, h) + aoff + m * 2048); } else { \
;         _Pragma("unroll") for (int m = 0; m < 4; ++m) _Pragma("unroll") for (int k = 0; k < 2; ++k) dst[m][k] = *(const LAS bf16x8*)(lds + PG8_SA(b, h) + aoff + m * 2048 + k * 1024); } } while (0)
; #define PG8_WAIT_VR() PG8_WAIT_V(8)
; #define PG8_WAIT_L(n) asm volatile("s_waitcnt lgkmcnt(" #n ")" ::: "memory")
; #define PG8_BAR __builtin_amdgcn_s_barrier()
; #define PG8_SCHED __builtin_amdgcn_sched_barrier(0)
; template <class Epi, class Sched, bool F8 = false, bool PF = false, bool I8 = false, int PID = -1>
; __device__ __forceinline__ void gemm_phase(LAS unsigned char* lds, LAS unsigned char* xlds, const int RP, const int RPB, const int nt, const Sched& S, const Epi& E, const int stagger_ticks) {
;     ...
;             PG8_WAIT_VR(); PG8_WAIT_L(0); PG8_BAR; PG8_MMA(0, 0, At, B0); PG8_MMA(0, 1, At, B1); PG8_BAR; PG8_SCHED;
;             PG8_LDA(At, 1, 1); PG8_STAGE(PG8_SB(1, 0), b3, voffB); PG8_STAGE(PG8_SB(1, 1), b3 + hstepB, voffB); PG8_STAGEA(PG8_SA(1, 0), a3, vA0, vA1);
;             PG8_WAIT_VR(); PG8_WAIT_L(0); PG8_BAR; PG8_MMA(1, 0, At, B0); PG8_MMA(1, 1, At, B1); PG8_BAR; PG8_SCHED;
;         }
	s_setprio 1
	s_waitcnt lgkmcnt(7)
	v_mfma_i32_16x16x64_i8 v[46:49], v[146:149], v[186:189], v[46:49]
	s_waitcnt lgkmcnt(6)
	v_mfma_i32_16x16x64_i8 v[142:145], v[150:153], v[190:193], v[46:49]
	v_mfma_i32_16x16x64_i8 v[46:49], v[154:157], v[186:189], v[54:57]
	v_mfma_i32_16x16x64_i8 v[138:141], v[158:161], v[190:193], v[46:49]
	s_waitcnt lgkmcnt(5)
	v_mfma_i32_16x16x64_i8 v[46:49], v[146:149], v[194:197], v[58:61]
	s_waitcnt lgkmcnt(4)
	v_mfma_i32_16x16x64_i8 v[126:129], v[150:153], v[198:201], v[46:49]
	v_mfma_i32_16x16x64_i8 v[46:49], v[154:157], v[194:197], v[66:69]
	v_mfma_i32_16x16x64_i8 v[122:125], v[158:161], v[198:201], v[46:49]
	s_waitcnt lgkmcnt(3)
	v_mfma_i32_16x16x64_i8 v[46:49], v[146:149], v[202:205], v[110:113]
	s_waitcnt lgkmcnt(2)
	v_mfma_i32_16x16x64_i8 v[110:113], v[150:153], v[206:209], v[46:49]
	v_mfma_i32_16x16x64_i8 v[46:49], v[154:157], v[202:205], v[106:109]
	v_mfma_i32_16x16x64_i8 v[106:109], v[158:161], v[206:209], v[46:49]
	s_waitcnt lgkmcnt(1)
	v_mfma_i32_16x16x64_i8 v[46:49], v[146:149], v[210:213], v[94:97]
	s_waitcnt lgkmcnt(0)
	v_mfma_i32_16x16x64_i8 v[94:97], v[150:153], v[214:217], v[46:49]
	v_mfma_i32_16x16x64_i8 v[46:49], v[154:157], v[210:213], v[90:93]
	v_mfma_i32_16x16x64_i8 v[90:93], v[158:161], v[214:217], v[46:49]
	v_mfma_i32_16x16x64_i8 v[46:49], v[162:165], v[186:189], v[134:137]
	v_mfma_i32_16x16x64_i8 v[134:137], v[166:169], v[190:193], v[46:49]
	v_mfma_i32_16x16x64_i8 v[46:49], v[170:173], v[186:189], v[130:133]
	v_mfma_i32_16x16x64_i8 v[130:133], v[174:177], v[190:193], v[46:49]
	v_mfma_i32_16x16x64_i8 v[46:49], v[162:165], v[194:197], v[118:121]
	v_mfma_i32_16x16x64_i8 v[118:121], v[166:169], v[198:201], v[46:49]
	v_mfma_i32_16x16x64_i8 v[46:49], v[170:173], v[194:197], v[114:117]
	v_mfma_i32_16x16x64_i8 v[114:117], v[174:177], v[198:201], v[46:49]
	v_mfma_i32_16x16x64_i8 v[46:49], v[162:165], v[202:205], v[102:105]
	v_mfma_i32_16x16x64_i8 v[102:105], v[166:169], v[206:209], v[46:49]
	v_mfma_i32_16x16x64_i8 v[46:49], v[170:173], v[202:205], v[98:101]
	v_mfma_i32_16x16x64_i8 v[98:101], v[174:177], v[206:209], v[46:49]
	v_mfma_i32_16x16x64_i8 v[46:49], v[162:165], v[210:213], v[86:89]
	v_mfma_i32_16x16x64_i8 v[86:89], v[166:169], v[214:217], v[46:49]
	v_mfma_i32_16x16x64_i8 v[46:49], v[170:173], v[210:213], v[82:85]
	v_mfma_i32_16x16x64_i8 v[82:85], v[174:177], v[214:217], v[46:49]
	s_setprio 0
	s_barrier
	s_nop 4
	ds_read_b128 v[46:49], v185 offset:49152
	ds_read_b128 v[54:57], v185 offset:50176
	ds_read_b128 v[58:61], v185 offset:51200
	ds_read_b128 v[66:69], v185 offset:52224
	ds_read_b128 v[186:189], v185 offset:53248
	ds_read_b128 v[190:193], v185 offset:54272
	ds_read_b128 v[194:197], v185 offset:55296
	ds_read_b128 v[198:201], v185 offset:56320
	s_add_i32 s62, s82, 0x18000
	s_mov_b32 m0, s62
	s_nop 0
	global_load_lds_dwordx4 v182, s[60:61]
	s_add_i32 s62, s82, 0x1a000
	s_mov_b32 m0, s62
	s_nop 0
	global_load_lds_dwordx4 v183, s[60:61]
	s_add_u32 s50, s50, 0x2080
	s_addc_u32 s51, s51, 0
	s_add_i32 s60, s82, 0x1c000
	s_mov_b32 m0, s60
	s_nop 0
	global_load_lds_dwordx4 v182, s[50:51]
	s_add_i32 s60, s82, 0x1e000
	s_mov_b32 m0, s60
	s_nop 0
	global_load_lds_dwordx4 v183, s[50:51]
	s_add_i32 s50, s82, 0x8000
	s_mov_b32 m0, s50
	s_nop 0
	global_load_lds_dwordx4 v180, s[48:49]
	s_add_i32 s82, s82, 0xa000
	s_mov_b32 m0, s82
	s_nop 0
	global_load_lds_dwordx4 v181, s[48:49]
	s_waitcnt vmcnt(8)
	s_waitcnt lgkmcnt(0)
	s_barrier
	s_setprio 1
	s_waitcnt lgkmcnt(7)
	v_mfma_i32_16x16x64_i8 v[78:81], v[146:149], v[46:49], v[78:81]
	v_mfma_i32_16x16x64_i8 v[74:77], v[154:157], v[46:49], v[74:77]
	s_waitcnt lgkmcnt(5)
	v_mfma_i32_16x16x64_i8 v[50:53], v[146:149], v[58:61], v[50:53]
	v_mfma_i32_16x16x64_i8 v[42:45], v[154:157], v[58:61], v[42:45]
	s_waitcnt lgkmcnt(3)
	v_mfma_i32_16x16x64_i8 v[30:33], v[146:149], v[186:189], v[30:33]
	v_mfma_i32_16x16x64_i8 v[26:29], v[154:157], v[186:189], v[26:29]
	s_waitcnt lgkmcnt(1)
	v_mfma_i32_16x16x64_i8 v[14:17], v[146:149], v[194:197], v[14:17]
	v_mfma_i32_16x16x64_i8 v[10:13], v[154:157], v[194:197], v[10:13]
	v_mfma_i32_16x16x64_i8 v[78:81], v[150:153], v[54:57], v[78:81]
	v_mfma_i32_16x16x64_i8 v[74:77], v[158:161], v[54:57], v[74:77]
	v_mfma_i32_16x16x64_i8 v[50:53], v[150:153], v[66:69], v[50:53]
	v_mfma_i32_16x16x64_i8 v[42:45], v[158:161], v[66:69], v[42:45]
	v_mfma_i32_16x16x64_i8 v[30:33], v[150:153], v[190:193], v[30:33]
	v_mfma_i32_16x16x64_i8 v[26:29], v[158:161], v[190:193], v[26:29]
	s_waitcnt lgkmcnt(0)
	v_mfma_i32_16x16x64_i8 v[14:17], v[150:153], v[198:201], v[14:17]
	v_mfma_i32_16x16x64_i8 v[10:13], v[158:161], v[198:201], v[10:13]
	v_mfma_i32_16x16x64_i8 v[70:73], v[162:165], v[46:49], v[70:73]
	v_mfma_i32_16x16x64_i8 v[46:49], v[170:173], v[46:49], v[62:65]
	v_mfma_i32_16x16x64_i8 v[38:41], v[162:165], v[58:61], v[38:41]
	v_mfma_i32_16x16x64_i8 v[34:37], v[170:173], v[58:61], v[34:37]
	v_mfma_i32_16x16x64_i8 v[22:25], v[162:165], v[186:189], v[22:25]
	v_mfma_i32_16x16x64_i8 v[18:21], v[170:173], v[186:189], v[18:21]
	v_mfma_i32_16x16x64_i8 v[6:9], v[162:165], v[194:197], v[6:9]
	v_mfma_i32_16x16x64_i8 v[2:5], v[170:173], v[194:197], v[2:5]
	v_mfma_i32_16x16x64_i8 v[70:73], v[166:169], v[54:57], v[70:73]
	v_mfma_i32_16x16x64_i8 v[62:65], v[174:177], v[54:57], v[46:49]
	v_mfma_i32_16x16x64_i8 v[38:41], v[166:169], v[66:69], v[38:41]
	v_mfma_i32_16x16x64_i8 v[34:37], v[174:177], v[66:69], v[34:37]
	v_mfma_i32_16x16x64_i8 v[22:25], v[166:169], v[190:193], v[22:25]
	v_mfma_i32_16x16x64_i8 v[18:21], v[174:177], v[190:193], v[18:21]
	v_mfma_i32_16x16x64_i8 v[6:9], v[166:169], v[198:201], v[6:9]
	v_mfma_i32_16x16x64_i8 v[2:5], v[174:177], v[198:201], v[2:5]
	s_setprio 0
	s_barrier
	s_add_i32 s79, s79, 2
	s_add_u32 s76, s76, 0x100
	s_addc_u32 s77, s77, 0
	s_add_u32 s2, s2, 0x100
	s_addc_u32 s3, s3, 0
	s_cmp_gt_u32 s79, 5
	s_branch .LBB0_214

; #define PG8_STAGE(bufoff, gbase, voff) do { PG8_GLDS((const char*)(gbase), (voff)[0], ldsb + (bufoff)); PG8_GLDS((const char*)(gbase), (voff)[1], ldsb + (bufoff) + 8192u); } while (0)
; #define PG8_STAGEA(bufoff, gbase, o0, o1) do { PG8_GLDS((const char*)(gbase), (o0), ldsb + (bufoff)); PG8_GLDS((const char*)(gbase), (o1), ldsb + (bufoff) + 8192u); } while (0)
; #define PG8_STAGEA1(bufoff, gbase) do { if constexpr (Sched::GATHER) { PG8_STAGEA(bufoff, gbase, vA2, vA3); } else { PG8_STAGEA(bufoff, (gbase) + hstep, vA0, vA1); } } while (0)
; #define PG8_LDA(dst, b, h) do { if constexpr (F8) { _Pragma("unroll") for (int m = 0; m < 4; ++m) dst##8[m] = PG8_LD32(lds + PG8_SA(b, h) + aoff + m * 2048); } else { \
;         _Pragma("unroll") for (int m = 0; m < 4; ++m) _Pragma("unroll") for (int k = 0; k < 2; ++k) dst[m][k] = *(const LAS bf16x8*)(lds + PG8_SA(b, h) + aoff + m * 2048 + k * 1024); } } while (0)
; #define PG8_LDB(dst, b, h) do { if constexpr (F8) { _Pragma("unroll") for (int n = 0; n < 2; ++n) dst##8[n] = PG8_LD32(lds + PG8_SB(b, h) + boff + n * 2048); } else { \
;         _Pragma("unroll") for (int n = 0; n < 2; ++n) _Pragma("unroll") for (int k = 0; k < 2; ++k) dst[n][k] = *(const LAS bf16x8*)(lds + PG8_SB(b, h) + boff + n * 2048 + k * 1024); } } while (0)
; template <class Epi, class Sched, bool F8 = false, bool PF = false, bool I8 = false, int PID = -1>
; __device__ __forceinline__ void gemm_phase(LAS unsigned char* lds, LAS unsigned char* xlds, const int RP, const int RPB, const int nt, const Sched& S, const Epi& E, const int stagger_ticks) {
;     ...
;             PG8_LDB(B0, 0, 0); PG8_LDB(B1, 0, 1); PG8_SCHED; PG8_LDA(At, 0, 0); PG8_STAGEA1(PG8_SA(1, 1), a1);
;             if (Sched::GATHER) { if (last) { const u32x4 nv = *nslot; vA0 = nv.x; vA1 = nv.y; vA2 = nv.z; vA3 = nv.w; } }
;             PG8_WAIT_VX(); PG8_WAIT_L(0); PG8_BAR; PG8_MMA(0, 0, At, B0); PG8_MMA(0, 1, At, B1); PG8_BAR; PG8_SCHED;
;             if constexpr (Epi::BIAS_DMA) { if (t == 0 && has_next) E.bias_dma(nxt, xlds + 8192 + ((ui + 1) & 1) * Epi::BIAS_STRIDE, wid, lane); }
;             PG8_LDA(At, 0, 1); PG8_STAGE(PG8_SB(0, 0), b2, voffB); PG8_STAGE(PG8_SB(0, 1), b2 + hstepB, voffB); PG8_STAGEA(PG8_SA(0, 0), a2, vA0, vA1);
;             PG8_WAIT_VX(); PG8_WAIT_L(0); PG8_BAR; PG8_MMA(1, 0, At, B0); PG8_MMA(1, 1, At, B1); PG8_BAR; PG8_SCHED;
.LBB0_448:
	s_add_u32 s29, s30, s36
	s_addc_u32 s42, s31, s37
	s_add_u32 s43, s29, 0x100
	s_addc_u32 s44, s42, 0
	s_and_b64 s[40:41], s[38:39], exec
	s_cselect_b32 s45, s9, s44
	s_cselect_b32 s44, s8, s43
	s_add_u32 s36, s34, s36
	s_addc_u32 s37, s35, s37
	s_add_u32 s40, s36, 0x100
	s_addc_u32 s41, s37, 0
	s_add_u32 s36, s44, 0x80
	s_addc_u32 s37, s45, 0
	s_and_b64 s[38:39], s[38:39], exec
	s_mov_b32 s82, s67
	s_cselect_b32 s47, s11, s41
	s_cselect_b32 s46, s10, s40
	s_add_u32 s78, s29, 0x80080
	v_add_u32_e32 v130, 0x10000, v135
	s_addc_u32 s79, s42, 0
	s_add_i32 s83, s82, 0xc000
	s_add_i32 s86, s82, 0xe000
	s_add_i32 s87, s82, 0x10000
	s_add_i32 s90, s82, 0x12000
	ds_read_b128 v[138:141], v130
	ds_read_b128 v[142:145], v130 offset:1024
	ds_read_b128 v[146:149], v130 offset:2048
	ds_read_b128 v[150:153], v130 offset:3072
	v_add_u32_e32 v130, 0x14000, v135
	s_add_u32 s48, s46, 0x4000
	ds_read_b128 v[154:157], v130
	ds_read_b128 v[158:161], v130 offset:1024
	ds_read_b128 v[162:165], v130 offset:2048
	ds_read_b128 v[166:169], v130 offset:3072
	s_addc_u32 s49, s47, 0
	s_add_i32 s91, s82, 0x14000
	s_add_i32 s94, s82, 0x16000
	s_add_i32 s95, s82, 0x2000
	s_add_u32 s42, s44, 0x80000
	s_addc_u32 s43, s45, 0
	s_add_i32 s77, s82, 0x4000
	s_add_i32 s76, s82, 0x6000
	s_add_u32 s38, s46, 0x80
	s_addc_u32 s39, s47, 0
	s_add_i32 s73, s82, 0x18000
	s_add_i32 s72, s82, 0x1a000
	s_add_u32 s40, s46, 0x4080
	s_addc_u32 s41, s47, 0
	s_add_i32 s75, s82, 0x1c000
	s_add_i32 s74, s82, 0x1e000
	s_add_i32 s71, s82, 0x8000
	s_add_i32 s29, s82, 0xa000
	ds_read_b128 v[170:173], v136
	ds_read_b128 v[174:177], v136 offset:1024
	ds_read_b128 v[178:181], v136 offset:2048
	ds_read_b128 v[182:185], v136 offset:3072
	ds_read_b128 v[186:189], v136 offset:4096
	ds_read_b128 v[190:193], v136 offset:5120
	ds_read_b128 v[194:197], v136 offset:6144
	ds_read_b128 v[198:201], v136 offset:7168
	s_mov_b32 m0, s83
	s_nop 0
	global_load_lds_dwordx4 v1, s[78:79]
	s_nop 0
	s_mov_b32 m0, s86
	s_nop 0
	global_load_lds_dwordx4 v132, s[78:79]
	s_waitcnt vmcnt(8)
	s_waitcnt lgkmcnt(0)
	s_barrier
	s_setprio 1
	s_waitcnt lgkmcnt(7)
	v_mfma_f32_16x16x32_bf16 v[118:121], v[138:141], v[170:173], v[118:121]
	v_mfma_f32_16x16x32_bf16 v[114:117], v[146:149], v[170:173], v[114:117]
	s_waitcnt lgkmcnt(5)
	v_mfma_f32_16x16x32_bf16 v[102:105], v[138:141], v[178:181], v[102:105]
	v_mfma_f32_16x16x32_bf16 v[98:101], v[146:149], v[178:181], v[98:101]
	s_waitcnt lgkmcnt(3)
	v_mfma_f32_16x16x32_bf16 v[86:89], v[138:141], v[186:189], v[86:89]
	v_mfma_f32_16x16x32_bf16 v[82:85], v[146:149], v[186:189], v[82:85]
	s_waitcnt lgkmcnt(1)
	v_mfma_f32_16x16x32_bf16 v[66:69], v[138:141], v[194:197], v[66:69]
	v_mfma_f32_16x16x32_bf16 v[58:61], v[146:149], v[194:197], v[58:61]
	v_mfma_f32_16x16x32_bf16 v[118:121], v[142:145], v[174:177], v[118:121]
	v_mfma_f32_16x16x32_bf16 v[114:117], v[150:153], v[174:177], v[114:117]
	v_mfma_f32_16x16x32_bf16 v[102:105], v[142:145], v[182:185], v[102:105]
	v_mfma_f32_16x16x32_bf16 v[98:101], v[150:153], v[182:185], v[98:101]
	v_mfma_f32_16x16x32_bf16 v[86:89], v[142:145], v[190:193], v[86:89]
	v_mfma_f32_16x16x32_bf16 v[82:85], v[150:153], v[190:193], v[82:85]
	s_waitcnt lgkmcnt(0)
	v_mfma_f32_16x16x32_bf16 v[66:69], v[142:145], v[198:201], v[66:69]
	v_mfma_f32_16x16x32_bf16 v[58:61], v[150:153], v[198:201], v[58:61]
	v_mfma_f32_16x16x32_bf16 v[126:129], v[154:157], v[170:173], v[126:129]
	v_mfma_f32_16x16x32_bf16 v[122:125], v[162:165], v[170:173], v[122:125]
	v_mfma_f32_16x16x32_bf16 v[110:113], v[154:157], v[178:181], v[110:113]
	v_mfma_f32_16x16x32_bf16 v[106:109], v[162:165], v[178:181], v[106:109]
	v_mfma_f32_16x16x32_bf16 v[94:97], v[154:157], v[186:189], v[94:97]
	v_mfma_f32_16x16x32_bf16 v[90:93], v[162:165], v[186:189], v[90:93]
	v_mfma_f32_16x16x32_bf16 v[78:81], v[154:157], v[194:197], v[78:81]
	v_mfma_f32_16x16x32_bf16 v[74:77], v[162:165], v[194:197], v[74:77]
	v_mfma_f32_16x16x32_bf16 v[126:129], v[158:161], v[174:177], v[126:129]
	v_mfma_f32_16x16x32_bf16 v[122:125], v[166:169], v[174:177], v[122:125]
	v_mfma_f32_16x16x32_bf16 v[110:113], v[158:161], v[182:185], v[110:113]
	v_mfma_f32_16x16x32_bf16 v[106:109], v[166:169], v[182:185], v[106:109]
	v_mfma_f32_16x16x32_bf16 v[94:97], v[158:161], v[190:193], v[94:97]
	v_mfma_f32_16x16x32_bf16 v[90:93], v[166:169], v[190:193], v[90:93]
	v_mfma_f32_16x16x32_bf16 v[78:81], v[158:161], v[198:201], v[78:81]
	v_mfma_f32_16x16x32_bf16 v[74:77], v[166:169], v[198:201], v[74:77]
	s_setprio 0
	s_barrier
	ds_read_b128 v[170:173], v136 offset:16384
	ds_read_b128 v[174:177], v136 offset:17408
	ds_read_b128 v[178:181], v136 offset:18432
	ds_read_b128 v[182:185], v136 offset:19456
	ds_read_b128 v[186:189], v136 offset:20480
	ds_read_b128 v[190:193], v136 offset:21504
	ds_read_b128 v[194:197], v136 offset:22528
	ds_read_b128 v[198:201], v136 offset:23552
	s_mov_b32 m0, s87
	s_nop 0
	global_load_lds_dwordx4 v133, s[46:47]
	s_nop 0
	s_mov_b32 m0, s90
	s_nop 0
	global_load_lds_dwordx4 v134, s[46:47]
	s_nop 0
	s_mov_b32 m0, s91
	s_nop 0
	global_load_lds_dwordx4 v133, s[48:49]
	s_nop 0
	s_mov_b32 m0, s94
	s_nop 0
	global_load_lds_dwordx4 v134, s[48:49]
	s_nop 0
	s_mov_b32 m0, s82
	s_nop 0
	global_load_lds_dwordx4 v1, s[44:45]
	s_nop 0
	s_mov_b32 m0, s95
	s_nop 0
	global_load_lds_dwordx4 v132, s[44:45]
	s_waitcnt vmcnt(8)
	s_waitcnt lgkmcnt(0)
	s_barrier
; #define PG8_STAGEA1(bufoff, gbase) do { if constexpr (Sched::GATHER) { PG8_STAGEA(bufoff, gbase, vA2, vA3); } else { PG8_STAGEA(bufoff, (gbase) + hstep, vA0, vA1); } } while (0)
; #define PG8_LDA(dst, b, h) do { if constexpr (F8) { _Pragma("unroll") for (int m = 0; m < 4; ++m) dst##8[m] = PG8_LD32(lds + PG8_SA(b, h) + aoff + m * 2048); } else { \
;         _Pragma("unroll") for (int m = 0; m < 4; ++m) _Pragma("unroll") for (int k = 0; k < 2; ++k) dst[m][k] = *(const LAS bf16x8*)(lds + PG8_SA(b, h) + aoff + m * 2048 + k * 1024); } } while (0)
; #define PG8_LDB(dst, b, h) do { if constexpr (F8) { _Pragma("unroll") for (int n = 0; n < 2; ++n) dst##8[n] = PG8_LD32(lds + PG8_SB(b, h) + boff + n * 2048); } else { \
;         _Pragma("unroll") for (int n = 0; n < 2; ++n) _Pragma("unroll") for (int k = 0; k < 2; ++k) dst[n][k] = *(const LAS bf16x8*)(lds + PG8_SB(b, h) + boff + n * 2048 + k * 1024); } } while (0)
; #define PG8_WAIT_VR() PG8_WAIT_V(8)
; #define PG8_WAIT_VX() do { if (relax) asm volatile("s_waitcnt vmcnt(%0)" :: "n"(8 + Epi::RELAX) : "memory"); else PG8_WAIT_V(8); } while (0)
; #define PG8_WAIT_L(n) asm volatile("s_waitcnt lgkmcnt(" #n ")" ::: "memory")
; #define PG8_BAR __builtin_amdgcn_s_barrier()
; #define PG8_SCHED __builtin_amdgcn_sched_barrier(0)
; template <class Epi, class Sched, bool F8 = false, bool PF = false, bool I8 = false, int PID = -1>
; __device__ __forceinline__ void gemm_phase(LAS unsigned char* lds, LAS unsigned char* xlds, const int RP, const int RPB, const int nt, const Sched& S, const Epi& E, const int stagger_ticks) {
;     ...
;             PG8_WAIT_VX(); PG8_WAIT_L(0); PG8_BAR; PG8_MMA(1, 0, At, B0); PG8_MMA(1, 1, At, B1); PG8_BAR; PG8_SCHED;
;             PG8_LDB(B0, 1, 0); PG8_LDB(B1, 1, 1); PG8_SCHED; PG8_LDA(At, 1, 0); PG8_STAGEA1(PG8_SA(0, 1), a2);
;             PG8_WAIT_VR(); PG8_WAIT_L(0); PG8_BAR; PG8_MMA(0, 0, At, B0); PG8_MMA(0, 1, At, B1); PG8_BAR; PG8_SCHED;
	s_setprio 1
	s_waitcnt lgkmcnt(7)
	v_mfma_f32_16x16x32_bf16 v[54:57], v[138:141], v[170:173], v[54:57]
	v_mfma_f32_16x16x32_bf16 v[50:53], v[146:149], v[170:173], v[50:53]
	s_waitcnt lgkmcnt(5)
	v_mfma_f32_16x16x32_bf16 v[38:41], v[138:141], v[178:181], v[38:41]
	v_mfma_f32_16x16x32_bf16 v[34:37], v[146:149], v[178:181], v[34:37]
	s_waitcnt lgkmcnt(3)
	v_mfma_f32_16x16x32_bf16 v[22:25], v[138:141], v[186:189], v[22:25]
	v_mfma_f32_16x16x32_bf16 v[18:21], v[146:149], v[186:189], v[18:21]
	s_waitcnt lgkmcnt(1)
	v_mfma_f32_16x16x32_bf16 v[6:9], v[138:141], v[194:197], v[6:9]
	v_mfma_f32_16x16x32_bf16 v[2:5], v[146:149], v[194:197], v[2:5]
	v_mfma_f32_16x16x32_bf16 v[54:57], v[142:145], v[174:177], v[54:57]
	v_mfma_f32_16x16x32_bf16 v[50:53], v[150:153], v[174:177], v[50:53]
	v_mfma_f32_16x16x32_bf16 v[38:41], v[142:145], v[182:185], v[38:41]
	v_mfma_f32_16x16x32_bf16 v[34:37], v[150:153], v[182:185], v[34:37]
	v_mfma_f32_16x16x32_bf16 v[22:25], v[142:145], v[190:193], v[22:25]
	v_mfma_f32_16x16x32_bf16 v[18:21], v[150:153], v[190:193], v[18:21]
	s_waitcnt lgkmcnt(0)
	v_mfma_f32_16x16x32_bf16 v[6:9], v[142:145], v[198:201], v[6:9]
	v_mfma_f32_16x16x32_bf16 v[2:5], v[150:153], v[198:201], v[2:5]
	v_mfma_f32_16x16x32_bf16 v[70:73], v[154:157], v[170:173], v[70:73]
	v_mfma_f32_16x16x32_bf16 v[62:65], v[162:165], v[170:173], v[62:65]
	v_mfma_f32_16x16x32_bf16 v[46:49], v[154:157], v[178:181], v[46:49]
	v_mfma_f32_16x16x32_bf16 v[42:45], v[162:165], v[178:181], v[42:45]
	v_mfma_f32_16x16x32_bf16 v[30:33], v[154:157], v[186:189], v[30:33]
	v_mfma_f32_16x16x32_bf16 v[26:29], v[162:165], v[186:189], v[26:29]
	v_mfma_f32_16x16x32_bf16 v[14:17], v[154:157], v[194:197], v[14:17]
	v_mfma_f32_16x16x32_bf16 v[10:13], v[162:165], v[194:197], v[10:13]
	v_mfma_f32_16x16x32_bf16 v[70:73], v[158:161], v[174:177], v[70:73]
	v_mfma_f32_16x16x32_bf16 v[62:65], v[166:169], v[174:177], v[62:65]
	v_mfma_f32_16x16x32_bf16 v[46:49], v[158:161], v[182:185], v[46:49]
	v_mfma_f32_16x16x32_bf16 v[42:45], v[166:169], v[182:185], v[42:45]
	v_mfma_f32_16x16x32_bf16 v[30:33], v[158:161], v[190:193], v[30:33]
	v_mfma_f32_16x16x32_bf16 v[26:29], v[166:169], v[190:193], v[26:29]
	v_mfma_f32_16x16x32_bf16 v[14:17], v[158:161], v[198:201], v[14:17]
	v_mfma_f32_16x16x32_bf16 v[10:13], v[166:169], v[198:201], v[10:13]
	s_setprio 0
	s_barrier
	v_add_u32_e32 v130, 0x18000, v135
	ds_read_b128 v[138:141], v130
	ds_read_b128 v[142:145], v130 offset:1024
	ds_read_b128 v[146:149], v130 offset:2048
	ds_read_b128 v[150:153], v130 offset:3072
	v_add_u32_e32 v130, 0x1c000, v135
	ds_read_b128 v[154:157], v130
	ds_read_b128 v[158:161], v130 offset:1024
	ds_read_b128 v[162:165], v130 offset:2048
	ds_read_b128 v[166:169], v130 offset:3072
	ds_read_b128 v[170:173], v136 offset:32768
	ds_read_b128 v[174:177], v136 offset:33792
	ds_read_b128 v[178:181], v136 offset:34816
	ds_read_b128 v[182:185], v136 offset:35840
	ds_read_b128 v[186:189], v136 offset:36864
	ds_read_b128 v[190:193], v136 offset:37888
	ds_read_b128 v[194:197], v136 offset:38912
	ds_read_b128 v[198:201], v136 offset:39936
	s_mov_b32 m0, s77
	s_nop 0
	global_load_lds_dwordx4 v1, s[42:43]
	s_nop 0
	s_mov_b32 m0, s76
	s_nop 0
	global_load_lds_dwordx4 v132, s[42:43]
	s_waitcnt vmcnt(8)
	s_waitcnt lgkmcnt(0)
	s_barrier
	s_setprio 1
	s_waitcnt lgkmcnt(7)
	v_mfma_f32_16x16x32_bf16 v[118:121], v[138:141], v[170:173], v[118:121]
	v_mfma_f32_16x16x32_bf16 v[114:117], v[146:149], v[170:173], v[114:117]
	s_waitcnt lgkmcnt(5)
	v_mfma_f32_16x16x32_bf16 v[102:105], v[138:141], v[178:181], v[102:105]
	v_mfma_f32_16x16x32_bf16 v[98:101], v[146:149], v[178:181], v[98:101]
	s_waitcnt lgkmcnt(3)
	v_mfma_f32_16x16x32_bf16 v[86:89], v[138:141], v[186:189], v[86:89]
	v_mfma_f32_16x16x32_bf16 v[82:85], v[146:149], v[186:189], v[82:85]
	s_waitcnt lgkmcnt(1)
	v_mfma_f32_16x16x32_bf16 v[66:69], v[138:141], v[194:197], v[66:69]
	v_mfma_f32_16x16x32_bf16 v[58:61], v[146:149], v[194:197], v[58:61]
	v_mfma_f32_16x16x32_bf16 v[118:121], v[142:145], v[174:177], v[118:121]
	v_mfma_f32_16x16x32_bf16 v[114:117], v[150:153], v[174:177], v[114:117]
	v_mfma_f32_16x16x32_bf16 v[102:105], v[142:145], v[182:185], v[102:105]
	v_mfma_f32_16x16x32_bf16 v[98:101], v[150:153], v[182:185], v[98:101]
	v_mfma_f32_16x16x32_bf16 v[86:89], v[142:145], v[190:193], v[86:89]
	v_mfma_f32_16x16x32_bf16 v[82:85], v[150:153], v[190:193], v[82:85]
	s_waitcnt lgkmcnt(0)
	v_mfma_f32_16x16x32_bf16 v[66:69], v[142:145], v[198:201], v[66:69]
	v_mfma_f32_16x16x32_bf16 v[58:61], v[150:153], v[198:201], v[58:61]
	v_mfma_f32_16x16x32_bf16 v[126:129], v[154:157], v[170:173], v[126:129]
	v_mfma_f32_16x16x32_bf16 v[122:125], v[162:165], v[170:173], v[122:125]
	v_mfma_f32_16x16x32_bf16 v[110:113], v[154:157], v[178:181], v[110:113]
	v_mfma_f32_16x16x32_bf16 v[106:109], v[162:165], v[178:181], v[106:109]
	v_mfma_f32_16x16x32_bf16 v[94:97], v[154:157], v[186:189], v[94:97]
	v_mfma_f32_16x16x32_bf16 v[90:93], v[162:165], v[186:189], v[90:93]
	v_mfma_f32_16x16x32_bf16 v[78:81], v[154:157], v[194:197], v[78:81]
	v_mfma_f32_16x16x32_bf16 v[74:77], v[162:165], v[194:197], v[74:77]
	v_mfma_f32_16x16x32_bf16 v[126:129], v[158:161], v[174:177], v[126:129]
	v_mfma_f32_16x16x32_bf16 v[122:125], v[166:169], v[174:177], v[122:125]
	v_mfma_f32_16x16x32_bf16 v[110:113], v[158:161], v[182:185], v[110:113]
	v_mfma_f32_16x16x32_bf16 v[106:109], v[166:169], v[182:185], v[106:109]
	v_mfma_f32_16x16x32_bf16 v[94:97], v[158:161], v[190:193], v[94:97]
	v_mfma_f32_16x16x32_bf16 v[90:93], v[166:169], v[190:193], v[90:93]
	v_mfma_f32_16x16x32_bf16 v[78:81], v[158:161], v[198:201], v[78:81]
	v_mfma_f32_16x16x32_bf16 v[74:77], v[166:169], v[198:201], v[74:77]
	s_setprio 0
	s_barrier
; #define PG8_STAGE(bufoff, gbase, voff) do { PG8_GLDS((const char*)(gbase), (voff)[0], ldsb + (bufoff)); PG8_GLDS((const char*)(gbase), (voff)[1], ldsb + (bufoff) + 8192u); } while (0)
; #define PG8_STAGEA(bufoff, gbase, o0, o1) do { PG8_GLDS((const char*)(gbase), (o0), ldsb + (bufoff)); PG8_GLDS((const char*)(gbase), (o1), ldsb + (bufoff) + 8192u); } while (0)
; #define PG8_LDA(dst, b, h) do { if constexpr (F8) { _Pragma("unroll") for (int m = 0; m < 4; ++m) dst##8[m] = PG8_LD32(lds + PG8_SA(b, h) + aoff + m * 2048); } else { \
;         _Pragma("unroll") for (int m = 0; m < 4; ++m) _Pragma("unroll") for (int k = 0; k < 2; ++k) dst[m][k] = *(const LAS bf16x8*)(lds + PG8_SA(b, h) + aoff + m * 2048 + k * 1024); } } while (0)
; #define PG8_WAIT_VR() PG8_WAIT_V(8)
; #define PG8_WAIT_L(n) asm volatile("s_waitcnt lgkmcnt(" #n ")" ::: "memory")
; #define PG8_BAR __builtin_amdgcn_s_barrier()
; #define PG8_SCHED __builtin_amdgcn_sched_barrier(0)
; #define PROF_BEGIN(sel) do { if constexpr (PROF && PROF_SEL == (sel)) prof_t0 = (unsigned)__builtin_amdgcn_s_memrealtime(); } while (0)
; #define PROF_END(sel) do { if constexpr (PROF && PROF_SEL == (sel)) prof_acc += (unsigned)__builtin_amdgcn_s_memrealtime() - prof_t0; } while (0)
; template <class Epi, class Sched, bool F8 = false, bool PF = false, bool I8 = false, int PID = -1>
; __device__ __forceinline__ void gemm_phase(LAS unsigned char* lds, LAS unsigned char* xlds, const int RP, const int RPB, const int nt, const Sched& S, const Epi& E, const int stagger_ticks) {
;     ...
;             PG8_LDA(At, 1, 1); PG8_STAGE(PG8_SB(1, 0), b3, voffB); PG8_STAGE(PG8_SB(1, 1), b3 + hstepB, voffB); PG8_STAGEA(PG8_SA(1, 0), a3, vA0, vA1);
;             PG8_WAIT_VR(); PG8_WAIT_L(0); PG8_BAR; PG8_MMA(1, 0, At, B0); PG8_MMA(1, 1, At, B1); PG8_BAR; PG8_SCHED;
;         }
;         PROF_END(1); PROF_BEGIN(3);
;         if (wr == 0) PG8_BAR;
	ds_read_b128 v[170:173], v136 offset:49152
	ds_read_b128 v[174:177], v136 offset:50176
	ds_read_b128 v[178:181], v136 offset:51200
	ds_read_b128 v[182:185], v136 offset:52224
	ds_read_b128 v[186:189], v136 offset:53248
	ds_read_b128 v[190:193], v136 offset:54272
	ds_read_b128 v[194:197], v136 offset:55296
	ds_read_b128 v[198:201], v136 offset:56320
	s_mov_b32 m0, s73
	s_nop 0
	global_load_lds_dwordx4 v133, s[38:39]
	s_nop 0
	s_mov_b32 m0, s72
	s_nop 0
	global_load_lds_dwordx4 v134, s[38:39]
	s_nop 0
	s_mov_b32 m0, s75
	s_nop 0
	global_load_lds_dwordx4 v133, s[40:41]
	s_nop 0
	s_mov_b32 m0, s74
	s_nop 0
	global_load_lds_dwordx4 v134, s[40:41]
	s_nop 0
	s_mov_b32 m0, s71
	s_nop 0
	global_load_lds_dwordx4 v1, s[36:37]
	s_nop 0
	s_mov_b32 m0, s29
	s_nop 0
	global_load_lds_dwordx4 v132, s[36:37]
	s_waitcnt vmcnt(8)
	s_waitcnt lgkmcnt(0)
	s_barrier
	s_setprio 1
	s_waitcnt lgkmcnt(7)
	v_mfma_f32_16x16x32_bf16 v[54:57], v[138:141], v[170:173], v[54:57]
	v_mfma_f32_16x16x32_bf16 v[50:53], v[146:149], v[170:173], v[50:53]
	s_waitcnt lgkmcnt(5)
	v_mfma_f32_16x16x32_bf16 v[38:41], v[138:141], v[178:181], v[38:41]
	v_mfma_f32_16x16x32_bf16 v[34:37], v[146:149], v[178:181], v[34:37]
	s_waitcnt lgkmcnt(3)
	v_mfma_f32_16x16x32_bf16 v[22:25], v[138:141], v[186:189], v[22:25]
	v_mfma_f32_16x16x32_bf16 v[18:21], v[146:149], v[186:189], v[18:21]
	s_waitcnt lgkmcnt(1)
	v_mfma_f32_16x16x32_bf16 v[6:9], v[138:141], v[194:197], v[6:9]
	v_mfma_f32_16x16x32_bf16 v[2:5], v[146:149], v[194:197], v[2:5]
	v_mfma_f32_16x16x32_bf16 v[54:57], v[142:145], v[174:177], v[54:57]
	v_mfma_f32_16x16x32_bf16 v[50:53], v[150:153], v[174:177], v[50:53]
	v_mfma_f32_16x16x32_bf16 v[38:41], v[142:145], v[182:185], v[38:41]
	v_mfma_f32_16x16x32_bf16 v[34:37], v[150:153], v[182:185], v[34:37]
	v_mfma_f32_16x16x32_bf16 v[22:25], v[142:145], v[190:193], v[22:25]
	v_mfma_f32_16x16x32_bf16 v[18:21], v[150:153], v[190:193], v[18:21]
	s_waitcnt lgkmcnt(0)
	v_mfma_f32_16x16x32_bf16 v[6:9], v[142:145], v[198:201], v[6:9]
	v_mfma_f32_16x16x32_bf16 v[2:5], v[150:153], v[198:201], v[2:5]
	v_mfma_f32_16x16x32_bf16 v[70:73], v[154:157], v[170:173], v[70:73]
	v_mfma_f32_16x16x32_bf16 v[62:65], v[162:165], v[170:173], v[62:65]
	v_mfma_f32_16x16x32_bf16 v[46:49], v[154:157], v[178:181], v[46:49]
	v_mfma_f32_16x16x32_bf16 v[42:45], v[162:165], v[178:181], v[42:45]
	v_mfma_f32_16x16x32_bf16 v[30:33], v[154:157], v[186:189], v[30:33]
	v_mfma_f32_16x16x32_bf16 v[26:29], v[162:165], v[186:189], v[26:29]
	v_mfma_f32_16x16x32_bf16 v[14:17], v[154:157], v[194:197], v[14:17]
	v_mfma_f32_16x16x32_bf16 v[10:13], v[162:165], v[194:197], v[10:13]
	v_mfma_f32_16x16x32_bf16 v[70:73], v[158:161], v[174:177], v[70:73]
	v_mfma_f32_16x16x32_bf16 v[62:65], v[166:169], v[174:177], v[62:65]
	v_mfma_f32_16x16x32_bf16 v[46:49], v[158:161], v[182:185], v[46:49]
	v_mfma_f32_16x16x32_bf16 v[42:45], v[166:169], v[182:185], v[42:45]
	v_mfma_f32_16x16x32_bf16 v[30:33], v[158:161], v[190:193], v[30:33]
	v_mfma_f32_16x16x32_bf16 v[26:29], v[166:169], v[190:193], v[26:29]
	v_mfma_f32_16x16x32_bf16 v[14:17], v[158:161], v[198:201], v[14:17]
	v_mfma_f32_16x16x32_bf16 v[10:13], v[166:169], v[198:201], v[10:13]
	s_setprio 0
	s_barrier
	s_andn2_b64 vcc, exec, s[2:3]
	s_mov_b64 s[38:39], -1
	s_mov_b64 s[2:3], 0
	s_mov_b64 s[36:37], 0x100
	s_cbranch_vccz .LBB0_448
	s_and_b64 vcc, exec, s[24:25]
	s_cbranch_vccz .LBB0_451
	s_barrier

; #define PG8_STAGE(bufoff, gbase, voff) do { PG8_GLDS((const char*)(gbase), (voff)[0], ldsb + (bufoff)); PG8_GLDS((const char*)(gbase), (voff)[1], ldsb + (bufoff) + 8192u); } while (0)
; #define PG8_STAGEA(bufoff, gbase, o0, o1) do { PG8_GLDS((const char*)(gbase), (o0), ldsb + (bufoff)); PG8_GLDS((const char*)(gbase), (o1), ldsb + (bufoff) + 8192u); } while (0)
; #define PG8_STAGEA1(bufoff, gbase) do { if constexpr (Sched::GATHER) { PG8_STAGEA(bufoff, gbase, vA2, vA3); } else { PG8_STAGEA(bufoff, (gbase) + hstep, vA0, vA1); } } while (0)
; #define PG8_LDA(dst, b, h) do { if constexpr (F8) { _Pragma("unroll") for (int m = 0; m < 4; ++m) dst##8[m] = PG8_LD32(lds + PG8_SA(b, h) + aoff + m * 2048); } else { \
;         _Pragma("unroll") for (int m = 0; m < 4; ++m) _Pragma("unroll") for (int k = 0; k < 2; ++k) dst[m][k] = *(const LAS bf16x8*)(lds + PG8_SA(b, h) + aoff + m * 2048 + k * 1024); } } while (0)
; #define PG8_LDB(dst, b, h) do { if constexpr (F8) { _Pragma("unroll") for (int n = 0; n < 2; ++n) dst##8[n] = PG8_LD32(lds + PG8_SB(b, h) + boff + n * 2048); } else { \
;         _Pragma("unroll") for (int n = 0; n < 2; ++n) _Pragma("unroll") for (int k = 0; k < 2; ++k) dst[n][k] = *(const LAS bf16x8*)(lds + PG8_SB(b, h) + boff + n * 2048 + k * 1024); } } while (0)
; template <class Epi, class Sched, bool F8 = false, bool PF = false, bool I8 = false, int PID = -1>
; __device__ __forceinline__ void gemm_phase(LAS unsigned char* lds, LAS unsigned char* xlds, const int RP, const int RPB, const int nt, const Sched& S, const Epi& E, const int stagger_ticks) {
;     ...
;             PG8_LDB(B0, 0, 0); PG8_LDB(B1, 0, 1); PG8_SCHED; PG8_LDA(At, 0, 0); PG8_STAGEA1(PG8_SA(1, 1), a1);
;             if (Sched::GATHER) { if (last) { const u32x4 nv = *nslot; vA0 = nv.x; vA1 = nv.y; vA2 = nv.z; vA3 = nv.w; } }
;             PG8_WAIT_VX(); PG8_WAIT_L(0); PG8_BAR; PG8_MMA(0, 0, At, B0); PG8_MMA(0, 1, At, B1); PG8_BAR; PG8_SCHED;
;             if constexpr (Epi::BIAS_DMA) { if (t == 0 && has_next) E.bias_dma(nxt, xlds + 8192 + ((ui + 1) & 1) * Epi::BIAS_STRIDE, wid, lane); }
;             PG8_LDA(At, 0, 1); PG8_STAGE(PG8_SB(0, 0), b2, voffB); PG8_STAGE(PG8_SB(0, 1), b2 + hstepB, voffB); PG8_STAGEA(PG8_SA(0, 0), a2, vA0, vA1);
;             PG8_WAIT_VX(); PG8_WAIT_L(0); PG8_BAR; PG8_MMA(1, 0, At, B0); PG8_MMA(1, 1, At, B1); PG8_BAR; PG8_SCHED;
.LBB0_469:
	s_add_u32 s25, s26, s30
	s_addc_u32 s38, s27, s31
	s_add_u32 s39, s25, 0x100
	s_addc_u32 s40, s38, 0
	s_and_b64 s[36:37], s[34:35], exec
	s_cselect_b32 s41, s7, s40
	s_cselect_b32 s40, s6, s39
	s_add_u32 s30, s28, s30
	s_addc_u32 s31, s29, s31
	s_add_u32 s36, s30, 0x100
	s_addc_u32 s37, s31, 0
	s_add_u32 s30, s40, 0x80
	s_addc_u32 s31, s41, 0
	s_and_b64 s[34:35], s[34:35], exec
	s_mov_b32 s77, s61
	s_cselect_b32 s43, s9, s37
	s_cselect_b32 s42, s8, s36
	s_add_u32 s78, s25, 0x40080
	v_add_u32_e32 v130, 0x10000, v135
	s_addc_u32 s79, s38, 0
	s_add_i32 s82, s77, 0xc000
	s_add_i32 s83, s77, 0xe000
	s_add_i32 s86, s77, 0x10000
	s_add_i32 s87, s77, 0x12000
	ds_read_b128 v[138:141], v130
	ds_read_b128 v[142:145], v130 offset:1024
	ds_read_b128 v[146:149], v130 offset:2048
	ds_read_b128 v[150:153], v130 offset:3072
	v_add_u32_e32 v130, 0x14000, v135
	s_add_u32 s44, s42, 0x8000
	ds_read_b128 v[154:157], v130
	ds_read_b128 v[158:161], v130 offset:1024
	ds_read_b128 v[162:165], v130 offset:2048
	ds_read_b128 v[166:169], v130 offset:3072
	s_addc_u32 s45, s43, 0
	s_add_i32 s90, s77, 0x14000
	s_add_i32 s91, s77, 0x16000
	s_add_i32 s94, s77, 0x2000
	s_add_u32 s38, s40, 0x40000
	s_addc_u32 s39, s41, 0
	s_add_i32 s76, s77, 0x4000
	s_add_i32 s75, s77, 0x6000
	s_add_u32 s34, s42, 0x80
	s_addc_u32 s35, s43, 0
	s_add_i32 s72, s77, 0x18000
	s_add_i32 s71, s77, 0x1a000
	s_add_u32 s36, s42, 0x8080
	s_addc_u32 s37, s43, 0
	s_add_i32 s74, s77, 0x1c000
	s_add_i32 s73, s77, 0x1e000
	s_add_i32 s70, s77, 0x8000
	s_add_i32 s25, s77, 0xa000
	ds_read_b128 v[170:173], v136
	ds_read_b128 v[174:177], v136 offset:1024
	ds_read_b128 v[178:181], v136 offset:2048
	ds_read_b128 v[182:185], v136 offset:3072
	ds_read_b128 v[186:189], v136 offset:4096
	ds_read_b128 v[190:193], v136 offset:5120
	ds_read_b128 v[194:197], v136 offset:6144
	ds_read_b128 v[198:201], v136 offset:7168
	s_mov_b32 m0, s82
	s_nop 0
	global_load_lds_dwordx4 v1, s[78:79]
	s_nop 0
	s_mov_b32 m0, s83
	s_nop 0
	global_load_lds_dwordx4 v132, s[78:79]
	s_waitcnt vmcnt(8)
	s_waitcnt lgkmcnt(0)
	s_barrier
	s_setprio 1
	s_waitcnt lgkmcnt(7)
	v_mfma_f32_16x16x32_bf16 v[106:109], v[138:141], v[170:173], v[106:109]
	v_mfma_f32_16x16x32_bf16 v[114:117], v[146:149], v[170:173], v[114:117]
	s_waitcnt lgkmcnt(5)
	v_mfma_f32_16x16x32_bf16 v[94:97], v[138:141], v[178:181], v[94:97]
	v_mfma_f32_16x16x32_bf16 v[102:105], v[146:149], v[178:181], v[102:105]
	s_waitcnt lgkmcnt(3)
	v_mfma_f32_16x16x32_bf16 v[74:77], v[138:141], v[186:189], v[74:77]
	v_mfma_f32_16x16x32_bf16 v[86:89], v[146:149], v[186:189], v[86:89]
	s_waitcnt lgkmcnt(1)
	v_mfma_f32_16x16x32_bf16 v[42:45], v[138:141], v[194:197], v[42:45]
	v_mfma_f32_16x16x32_bf16 v[58:61], v[146:149], v[194:197], v[58:61]
	v_mfma_f32_16x16x32_bf16 v[106:109], v[142:145], v[174:177], v[106:109]
	v_mfma_f32_16x16x32_bf16 v[114:117], v[150:153], v[174:177], v[114:117]
	v_mfma_f32_16x16x32_bf16 v[94:97], v[142:145], v[182:185], v[94:97]
	v_mfma_f32_16x16x32_bf16 v[102:105], v[150:153], v[182:185], v[102:105]
	v_mfma_f32_16x16x32_bf16 v[74:77], v[142:145], v[190:193], v[74:77]
	v_mfma_f32_16x16x32_bf16 v[86:89], v[150:153], v[190:193], v[86:89]
	s_waitcnt lgkmcnt(0)
	v_mfma_f32_16x16x32_bf16 v[42:45], v[142:145], v[198:201], v[42:45]
	v_mfma_f32_16x16x32_bf16 v[58:61], v[150:153], v[198:201], v[58:61]
	v_mfma_f32_16x16x32_bf16 v[122:125], v[154:157], v[170:173], v[122:125]
	v_mfma_f32_16x16x32_bf16 v[126:129], v[162:165], v[170:173], v[126:129]
	v_mfma_f32_16x16x32_bf16 v[110:113], v[154:157], v[178:181], v[110:113]
	v_mfma_f32_16x16x32_bf16 v[118:121], v[162:165], v[178:181], v[118:121]
	v_mfma_f32_16x16x32_bf16 v[90:93], v[154:157], v[186:189], v[90:93]
	v_mfma_f32_16x16x32_bf16 v[98:101], v[162:165], v[186:189], v[98:101]
	v_mfma_f32_16x16x32_bf16 v[66:69], v[154:157], v[194:197], v[66:69]
	v_mfma_f32_16x16x32_bf16 v[78:81], v[162:165], v[194:197], v[78:81]
	v_mfma_f32_16x16x32_bf16 v[122:125], v[158:161], v[174:177], v[122:125]
	v_mfma_f32_16x16x32_bf16 v[126:129], v[166:169], v[174:177], v[126:129]
	v_mfma_f32_16x16x32_bf16 v[110:113], v[158:161], v[182:185], v[110:113]
	v_mfma_f32_16x16x32_bf16 v[118:121], v[166:169], v[182:185], v[118:121]
	v_mfma_f32_16x16x32_bf16 v[90:93], v[158:161], v[190:193], v[90:93]
	v_mfma_f32_16x16x32_bf16 v[98:101], v[166:169], v[190:193], v[98:101]
	v_mfma_f32_16x16x32_bf16 v[66:69], v[158:161], v[198:201], v[66:69]
	v_mfma_f32_16x16x32_bf16 v[78:81], v[166:169], v[198:201], v[78:81]
	s_setprio 0
	s_barrier
	ds_read_b128 v[170:173], v136 offset:16384
	ds_read_b128 v[174:177], v136 offset:17408
	ds_read_b128 v[178:181], v136 offset:18432
	ds_read_b128 v[182:185], v136 offset:19456
	ds_read_b128 v[186:189], v136 offset:20480
	ds_read_b128 v[190:193], v136 offset:21504
	ds_read_b128 v[194:197], v136 offset:22528
	ds_read_b128 v[198:201], v136 offset:23552
	s_mov_b32 m0, s86
	s_nop 0
	global_load_lds_dwordx4 v133, s[42:43]
	s_nop 0
	s_mov_b32 m0, s87
	s_nop 0
	global_load_lds_dwordx4 v134, s[42:43]
	s_nop 0
	s_mov_b32 m0, s90
	s_nop 0
	global_load_lds_dwordx4 v133, s[44:45]
	s_nop 0
	s_mov_b32 m0, s91
	s_nop 0
	global_load_lds_dwordx4 v134, s[44:45]
	s_nop 0
	s_mov_b32 m0, s77
	s_nop 0
	global_load_lds_dwordx4 v1, s[40:41]
	s_nop 0
	s_mov_b32 m0, s94
	s_nop 0
	global_load_lds_dwordx4 v132, s[40:41]
	s_waitcnt vmcnt(8)
	s_waitcnt lgkmcnt(0)
	s_barrier
; #define PG8_STAGEA1(bufoff, gbase) do { if constexpr (Sched::GATHER) { PG8_STAGEA(bufoff, gbase, vA2, vA3); } else { PG8_STAGEA(bufoff, (gbase) + hstep, vA0, vA1); } } while (0)
; #define PG8_LDA(dst, b, h) do { if constexpr (F8) { _Pragma("unroll") for (int m = 0; m < 4; ++m) dst##8[m] = PG8_LD32(lds + PG8_SA(b, h) + aoff + m * 2048); } else { \
;         _Pragma("unroll") for (int m = 0; m < 4; ++m) _Pragma("unroll") for (int k = 0; k < 2; ++k) dst[m][k] = *(const LAS bf16x8*)(lds + PG8_SA(b, h) + aoff + m * 2048 + k * 1024); } } while (0)
; #define PG8_LDB(dst, b, h) do { if constexpr (F8) { _Pragma("unroll") for (int n = 0; n < 2; ++n) dst##8[n] = PG8_LD32(lds + PG8_SB(b, h) + boff + n * 2048); } else { \
;         _Pragma("unroll") for (int n = 0; n < 2; ++n) _Pragma("unroll") for (int k = 0; k < 2; ++k) dst[n][k] = *(const LAS bf16x8*)(lds + PG8_SB(b, h) + boff + n * 2048 + k * 1024); } } while (0)
; #define PG8_WAIT_VR() PG8_WAIT_V(8)
; #define PG8_WAIT_VX() do { if (relax) asm volatile("s_waitcnt vmcnt(%0)" :: "n"(8 + Epi::RELAX) : "memory"); else PG8_WAIT_V(8); } while (0)
; #define PG8_WAIT_L(n) asm volatile("s_waitcnt lgkmcnt(" #n ")" ::: "memory")
; #define PG8_BAR __builtin_amdgcn_s_barrier()
; #define PG8_SCHED __builtin_amdgcn_sched_barrier(0)
; template <class Epi, class Sched, bool F8 = false, bool PF = false, bool I8 = false, int PID = -1>
; __device__ __forceinline__ void gemm_phase(LAS unsigned char* lds, LAS unsigned char* xlds, const int RP, const int RPB, const int nt, const Sched& S, const Epi& E, const int stagger_ticks) {
;     ...
;             PG8_WAIT_VX(); PG8_WAIT_L(0); PG8_BAR; PG8_MMA(1, 0, At, B0); PG8_MMA(1, 1, At, B1); PG8_BAR; PG8_SCHED;
;             PG8_LDB(B0, 1, 0); PG8_LDB(B1, 1, 1); PG8_SCHED; PG8_LDA(At, 1, 0); PG8_STAGEA1(PG8_SA(0, 1), a2);
;             PG8_WAIT_VR(); PG8_WAIT_L(0); PG8_BAR; PG8_MMA(0, 0, At, B0); PG8_MMA(0, 1, At, B1); PG8_BAR; PG8_SCHED;
	s_setprio 1
	s_waitcnt lgkmcnt(7)
	v_mfma_f32_16x16x32_bf16 v[46:49], v[138:141], v[170:173], v[46:49]
	v_mfma_f32_16x16x32_bf16 v[62:65], v[146:149], v[170:173], v[62:65]
	s_waitcnt lgkmcnt(5)
	v_mfma_f32_16x16x32_bf16 v[26:29], v[138:141], v[178:181], v[26:29]
	v_mfma_f32_16x16x32_bf16 v[38:41], v[146:149], v[178:181], v[38:41]
	s_waitcnt lgkmcnt(3)
	v_mfma_f32_16x16x32_bf16 v[14:17], v[138:141], v[186:189], v[14:17]
	v_mfma_f32_16x16x32_bf16 v[22:25], v[146:149], v[186:189], v[22:25]
	s_waitcnt lgkmcnt(1)
	v_mfma_f32_16x16x32_bf16 v[2:5], v[138:141], v[194:197], v[2:5]
	v_mfma_f32_16x16x32_bf16 v[6:9], v[146:149], v[194:197], v[6:9]
	v_mfma_f32_16x16x32_bf16 v[46:49], v[142:145], v[174:177], v[46:49]
	v_mfma_f32_16x16x32_bf16 v[62:65], v[150:153], v[174:177], v[62:65]
	v_mfma_f32_16x16x32_bf16 v[26:29], v[142:145], v[182:185], v[26:29]
	v_mfma_f32_16x16x32_bf16 v[38:41], v[150:153], v[182:185], v[38:41]
	v_mfma_f32_16x16x32_bf16 v[14:17], v[142:145], v[190:193], v[14:17]
	v_mfma_f32_16x16x32_bf16 v[22:25], v[150:153], v[190:193], v[22:25]
	s_waitcnt lgkmcnt(0)
	v_mfma_f32_16x16x32_bf16 v[2:5], v[142:145], v[198:201], v[2:5]
	v_mfma_f32_16x16x32_bf16 v[6:9], v[150:153], v[198:201], v[6:9]
	v_mfma_f32_16x16x32_bf16 v[70:73], v[154:157], v[170:173], v[70:73]
	v_mfma_f32_16x16x32_bf16 v[82:85], v[162:165], v[170:173], v[82:85]
	v_mfma_f32_16x16x32_bf16 v[50:53], v[154:157], v[178:181], v[50:53]
	v_mfma_f32_16x16x32_bf16 v[54:57], v[162:165], v[178:181], v[54:57]
	v_mfma_f32_16x16x32_bf16 v[30:33], v[154:157], v[186:189], v[30:33]
	v_mfma_f32_16x16x32_bf16 v[34:37], v[162:165], v[186:189], v[34:37]
	v_mfma_f32_16x16x32_bf16 v[10:13], v[154:157], v[194:197], v[10:13]
	v_mfma_f32_16x16x32_bf16 v[18:21], v[162:165], v[194:197], v[18:21]
	v_mfma_f32_16x16x32_bf16 v[70:73], v[158:161], v[174:177], v[70:73]
	v_mfma_f32_16x16x32_bf16 v[82:85], v[166:169], v[174:177], v[82:85]
	v_mfma_f32_16x16x32_bf16 v[50:53], v[158:161], v[182:185], v[50:53]
	v_mfma_f32_16x16x32_bf16 v[54:57], v[166:169], v[182:185], v[54:57]
	v_mfma_f32_16x16x32_bf16 v[30:33], v[158:161], v[190:193], v[30:33]
	v_mfma_f32_16x16x32_bf16 v[34:37], v[166:169], v[190:193], v[34:37]
	v_mfma_f32_16x16x32_bf16 v[10:13], v[158:161], v[198:201], v[10:13]
	v_mfma_f32_16x16x32_bf16 v[18:21], v[166:169], v[198:201], v[18:21]
	s_setprio 0
	s_barrier
	v_add_u32_e32 v130, 0x18000, v135
	ds_read_b128 v[138:141], v130
	ds_read_b128 v[142:145], v130 offset:1024
	ds_read_b128 v[146:149], v130 offset:2048
	ds_read_b128 v[150:153], v130 offset:3072
	v_add_u32_e32 v130, 0x1c000, v135
	ds_read_b128 v[154:157], v130
	ds_read_b128 v[158:161], v130 offset:1024
	ds_read_b128 v[162:165], v130 offset:2048
	ds_read_b128 v[166:169], v130 offset:3072
	ds_read_b128 v[170:173], v136 offset:32768
	ds_read_b128 v[174:177], v136 offset:33792
	ds_read_b128 v[178:181], v136 offset:34816
	ds_read_b128 v[182:185], v136 offset:35840
	ds_read_b128 v[186:189], v136 offset:36864
	ds_read_b128 v[190:193], v136 offset:37888
	ds_read_b128 v[194:197], v136 offset:38912
	ds_read_b128 v[198:201], v136 offset:39936
	s_mov_b32 m0, s76
	s_nop 0
	global_load_lds_dwordx4 v1, s[38:39]
	s_nop 0
	s_mov_b32 m0, s75
	s_nop 0
	global_load_lds_dwordx4 v132, s[38:39]
	s_waitcnt vmcnt(8)
	s_waitcnt lgkmcnt(0)
	s_barrier
	s_setprio 1
	s_waitcnt lgkmcnt(7)
	v_mfma_f32_16x16x32_bf16 v[106:109], v[138:141], v[170:173], v[106:109]
	v_mfma_f32_16x16x32_bf16 v[114:117], v[146:149], v[170:173], v[114:117]
	s_waitcnt lgkmcnt(5)
	v_mfma_f32_16x16x32_bf16 v[94:97], v[138:141], v[178:181], v[94:97]
	v_mfma_f32_16x16x32_bf16 v[102:105], v[146:149], v[178:181], v[102:105]
	s_waitcnt lgkmcnt(3)
	v_mfma_f32_16x16x32_bf16 v[74:77], v[138:141], v[186:189], v[74:77]
	v_mfma_f32_16x16x32_bf16 v[86:89], v[146:149], v[186:189], v[86:89]
	s_waitcnt lgkmcnt(1)
	v_mfma_f32_16x16x32_bf16 v[42:45], v[138:141], v[194:197], v[42:45]
	v_mfma_f32_16x16x32_bf16 v[58:61], v[146:149], v[194:197], v[58:61]
	v_mfma_f32_16x16x32_bf16 v[106:109], v[142:145], v[174:177], v[106:109]
	v_mfma_f32_16x16x32_bf16 v[114:117], v[150:153], v[174:177], v[114:117]
	v_mfma_f32_16x16x32_bf16 v[94:97], v[142:145], v[182:185], v[94:97]
	v_mfma_f32_16x16x32_bf16 v[102:105], v[150:153], v[182:185], v[102:105]
	v_mfma_f32_16x16x32_bf16 v[74:77], v[142:145], v[190:193], v[74:77]
	v_mfma_f32_16x16x32_bf16 v[86:89], v[150:153], v[190:193], v[86:89]
	s_waitcnt lgkmcnt(0)
	v_mfma_f32_16x16x32_bf16 v[42:45], v[142:145], v[198:201], v[42:45]
	v_mfma_f32_16x16x32_bf16 v[58:61], v[150:153], v[198:201], v[58:61]
	v_mfma_f32_16x16x32_bf16 v[122:125], v[154:157], v[170:173], v[122:125]
	v_mfma_f32_16x16x32_bf16 v[126:129], v[162:165], v[170:173], v[126:129]
	v_mfma_f32_16x16x32_bf16 v[110:113], v[154:157], v[178:181], v[110:113]
	v_mfma_f32_16x16x32_bf16 v[118:121], v[162:165], v[178:181], v[118:121]
	v_mfma_f32_16x16x32_bf16 v[90:93], v[154:157], v[186:189], v[90:93]
	v_mfma_f32_16x16x32_bf16 v[98:101], v[162:165], v[186:189], v[98:101]
	v_mfma_f32_16x16x32_bf16 v[66:69], v[154:157], v[194:197], v[66:69]
	v_mfma_f32_16x16x32_bf16 v[78:81], v[162:165], v[194:197], v[78:81]
	v_mfma_f32_16x16x32_bf16 v[122:125], v[158:161], v[174:177], v[122:125]
	v_mfma_f32_16x16x32_bf16 v[126:129], v[166:169], v[174:177], v[126:129]
	v_mfma_f32_16x16x32_bf16 v[110:113], v[158:161], v[182:185], v[110:113]
	v_mfma_f32_16x16x32_bf16 v[118:121], v[166:169], v[182:185], v[118:121]
	v_mfma_f32_16x16x32_bf16 v[90:93], v[158:161], v[190:193], v[90:93]
	v_mfma_f32_16x16x32_bf16 v[98:101], v[166:169], v[190:193], v[98:101]
	v_mfma_f32_16x16x32_bf16 v[66:69], v[158:161], v[198:201], v[66:69]
	v_mfma_f32_16x16x32_bf16 v[78:81], v[166:169], v[198:201], v[78:81]
	s_setprio 0
	s_barrier
; #define PG8_STAGE(bufoff, gbase, voff) do { PG8_GLDS((const char*)(gbase), (voff)[0], ldsb + (bufoff)); PG8_GLDS((const char*)(gbase), (voff)[1], ldsb + (bufoff) + 8192u); } while (0)
; #define PG8_STAGEA(bufoff, gbase, o0, o1) do { PG8_GLDS((const char*)(gbase), (o0), ldsb + (bufoff)); PG8_GLDS((const char*)(gbase), (o1), ldsb + (bufoff) + 8192u); } while (0)
; #define PG8_LDA(dst, b, h) do { if constexpr (F8) { _Pragma("unroll") for (int m = 0; m < 4; ++m) dst##8[m] = PG8_LD32(lds + PG8_SA(b, h) + aoff + m * 2048); } else { \
;         _Pragma("unroll") for (int m = 0; m < 4; ++m) _Pragma("unroll") for (int k = 0; k < 2; ++k) dst[m][k] = *(const LAS bf16x8*)(lds + PG8_SA(b, h) + aoff + m * 2048 + k * 1024); } } while (0)
; #define PG8_WAIT_VR() PG8_WAIT_V(8)
; #define PG8_WAIT_L(n) asm volatile("s_waitcnt lgkmcnt(" #n ")" ::: "memory")
; #define PG8_BAR __builtin_amdgcn_s_barrier()
; #define PG8_SCHED __builtin_amdgcn_sched_barrier(0)
; #define PROF_BEGIN(sel) do { if constexpr (PROF && PROF_SEL == (sel)) prof_t0 = (unsigned)__builtin_amdgcn_s_memrealtime(); } while (0)
; #define PROF_END(sel) do { if constexpr (PROF && PROF_SEL == (sel)) prof_acc += (unsigned)__builtin_amdgcn_s_memrealtime() - prof_t0; } while (0)
; template <class Epi, class Sched, bool F8 = false, bool PF = false, bool I8 = false, int PID = -1>
; __device__ __forceinline__ void gemm_phase(LAS unsigned char* lds, LAS unsigned char* xlds, const int RP, const int RPB, const int nt, const Sched& S, const Epi& E, const int stagger_ticks) {
;     ...
;             PG8_LDA(At, 1, 1); PG8_STAGE(PG8_SB(1, 0), b3, voffB); PG8_STAGE(PG8_SB(1, 1), b3 + hstepB, voffB); PG8_STAGEA(PG8_SA(1, 0), a3, vA0, vA1);
;             PG8_WAIT_VR(); PG8_WAIT_L(0); PG8_BAR; PG8_MMA(1, 0, At, B0); PG8_MMA(1, 1, At, B1); PG8_BAR; PG8_SCHED;
;         }
;         PROF_END(1); PROF_BEGIN(3);
;         if (wr == 0) PG8_BAR;
	ds_read_b128 v[170:173], v136 offset:49152
	ds_read_b128 v[174:177], v136 offset:50176
	ds_read_b128 v[178:181], v136 offset:51200
	ds_read_b128 v[182:185], v136 offset:52224
	ds_read_b128 v[186:189], v136 offset:53248
	ds_read_b128 v[190:193], v136 offset:54272
	ds_read_b128 v[194:197], v136 offset:55296
	ds_read_b128 v[198:201], v136 offset:56320
	s_mov_b32 m0, s72
	s_nop 0
	global_load_lds_dwordx4 v133, s[34:35]
	s_nop 0
	s_mov_b32 m0, s71
	s_nop 0
	global_load_lds_dwordx4 v134, s[34:35]
	s_nop 0
	s_mov_b32 m0, s74
	s_nop 0
	global_load_lds_dwordx4 v133, s[36:37]
	s_nop 0
	s_mov_b32 m0, s73
	s_nop 0
	global_load_lds_dwordx4 v134, s[36:37]
	s_nop 0
	s_mov_b32 m0, s70
	s_nop 0
	global_load_lds_dwordx4 v1, s[30:31]
	s_nop 0
	s_mov_b32 m0, s25
	s_nop 0
	global_load_lds_dwordx4 v132, s[30:31]
	s_waitcnt vmcnt(8)
	s_waitcnt lgkmcnt(0)
	s_barrier
	s_setprio 1
	s_waitcnt lgkmcnt(7)
	v_mfma_f32_16x16x32_bf16 v[46:49], v[138:141], v[170:173], v[46:49]
	v_mfma_f32_16x16x32_bf16 v[62:65], v[146:149], v[170:173], v[62:65]
	s_waitcnt lgkmcnt(5)
	v_mfma_f32_16x16x32_bf16 v[26:29], v[138:141], v[178:181], v[26:29]
	v_mfma_f32_16x16x32_bf16 v[38:41], v[146:149], v[178:181], v[38:41]
	s_waitcnt lgkmcnt(3)
	v_mfma_f32_16x16x32_bf16 v[14:17], v[138:141], v[186:189], v[14:17]
	v_mfma_f32_16x16x32_bf16 v[22:25], v[146:149], v[186:189], v[22:25]
	s_waitcnt lgkmcnt(1)
	v_mfma_f32_16x16x32_bf16 v[2:5], v[138:141], v[194:197], v[2:5]
	v_mfma_f32_16x16x32_bf16 v[6:9], v[146:149], v[194:197], v[6:9]
	v_mfma_f32_16x16x32_bf16 v[46:49], v[142:145], v[174:177], v[46:49]
	v_mfma_f32_16x16x32_bf16 v[62:65], v[150:153], v[174:177], v[62:65]
	v_mfma_f32_16x16x32_bf16 v[26:29], v[142:145], v[182:185], v[26:29]
	v_mfma_f32_16x16x32_bf16 v[38:41], v[150:153], v[182:185], v[38:41]
	v_mfma_f32_16x16x32_bf16 v[14:17], v[142:145], v[190:193], v[14:17]
	v_mfma_f32_16x16x32_bf16 v[22:25], v[150:153], v[190:193], v[22:25]
	s_waitcnt lgkmcnt(0)
	v_mfma_f32_16x16x32_bf16 v[2:5], v[142:145], v[198:201], v[2:5]
	v_mfma_f32_16x16x32_bf16 v[6:9], v[150:153], v[198:201], v[6:9]
	v_mfma_f32_16x16x32_bf16 v[70:73], v[154:157], v[170:173], v[70:73]
	v_mfma_f32_16x16x32_bf16 v[82:85], v[162:165], v[170:173], v[82:85]
	v_mfma_f32_16x16x32_bf16 v[50:53], v[154:157], v[178:181], v[50:53]
	v_mfma_f32_16x16x32_bf16 v[54:57], v[162:165], v[178:181], v[54:57]
	v_mfma_f32_16x16x32_bf16 v[30:33], v[154:157], v[186:189], v[30:33]
	v_mfma_f32_16x16x32_bf16 v[34:37], v[162:165], v[186:189], v[34:37]
	v_mfma_f32_16x16x32_bf16 v[10:13], v[154:157], v[194:197], v[10:13]
	v_mfma_f32_16x16x32_bf16 v[18:21], v[162:165], v[194:197], v[18:21]
	v_mfma_f32_16x16x32_bf16 v[70:73], v[158:161], v[174:177], v[70:73]
	v_mfma_f32_16x16x32_bf16 v[82:85], v[166:169], v[174:177], v[82:85]
	v_mfma_f32_16x16x32_bf16 v[50:53], v[158:161], v[182:185], v[50:53]
	v_mfma_f32_16x16x32_bf16 v[54:57], v[166:169], v[182:185], v[54:57]
	v_mfma_f32_16x16x32_bf16 v[30:33], v[158:161], v[190:193], v[30:33]
	v_mfma_f32_16x16x32_bf16 v[34:37], v[166:169], v[190:193], v[34:37]
	v_mfma_f32_16x16x32_bf16 v[10:13], v[158:161], v[198:201], v[10:13]
	v_mfma_f32_16x16x32_bf16 v[18:21], v[166:169], v[198:201], v[18:21]
	s_setprio 0
	s_barrier
	s_andn2_b64 vcc, exec, s[2:3]
	s_mov_b64 s[34:35], -1
	s_mov_b64 s[2:3], 0
	s_mov_b64 s[30:31], 0x100
	s_cbranch_vccz .LBB0_469
	s_and_b64 vcc, exec, s[22:23]
	s_cbranch_vccz .LBB0_472
	s_barrier

; #define PG8_STAGE(bufoff, gbase, voff) do { PG8_GLDS((const char*)(gbase), (voff)[0], ldsb + (bufoff)); PG8_GLDS((const char*)(gbase), (voff)[1], ldsb + (bufoff) + 8192u); } while (0)
; #define PG8_STAGEA(bufoff, gbase, o0, o1) do { PG8_GLDS((const char*)(gbase), (o0), ldsb + (bufoff)); PG8_GLDS((const char*)(gbase), (o1), ldsb + (bufoff) + 8192u); } while (0)
; #define PG8_STAGEA1(bufoff, gbase) do { if constexpr (Sched::GATHER) { PG8_STAGEA(bufoff, gbase, vA2, vA3); } else { PG8_STAGEA(bufoff, (gbase) + hstep, vA0, vA1); } } while (0)
; #define PG8_LDA(dst, b, h) do { if constexpr (F8) { _Pragma("unroll") for (int m = 0; m < 4; ++m) dst##8[m] = PG8_LD32(lds + PG8_SA(b, h) + aoff + m * 2048); } else { \
;         _Pragma("unroll") for (int m = 0; m < 4; ++m) _Pragma("unroll") for (int k = 0; k < 2; ++k) dst[m][k] = *(const LAS bf16x8*)(lds + PG8_SA(b, h) + aoff + m * 2048 + k * 1024); } } while (0)
; #define PG8_LDB(dst, b, h) do { if constexpr (F8) { _Pragma("unroll") for (int n = 0; n < 2; ++n) dst##8[n] = PG8_LD32(lds + PG8_SB(b, h) + boff + n * 2048); } else { \
;         _Pragma("unroll") for (int n = 0; n < 2; ++n) _Pragma("unroll") for (int k = 0; k < 2; ++k) dst[n][k] = *(const LAS bf16x8*)(lds + PG8_SB(b, h) + boff + n * 2048 + k * 1024); } } while (0)
; #define PG8_WAIT_VX() do { if (relax) asm volatile("s_waitcnt vmcnt(%0)" :: "n"(8 + Epi::RELAX) : "memory"); else PG8_WAIT_V(8); } while (0)
; template <class Epi, class Sched, bool F8 = false, bool PF = false, bool I8 = false, int PID = -1>
; __device__ __forceinline__ void gemm_phase(LAS unsigned char* lds, LAS unsigned char* xlds, const int RP, const int RPB, const int nt, const Sched& S, const Epi& E, const int stagger_ticks) {
;     ...
;             PG8_LDB(B0, 0, 0); PG8_LDB(B1, 0, 1); PG8_SCHED; PG8_LDA(At, 0, 0); PG8_STAGEA1(PG8_SA(1, 1), a1);
;             if (Sched::GATHER) { if (last) { const u32x4 nv = *nslot; vA0 = nv.x; vA1 = nv.y; vA2 = nv.z; vA3 = nv.w; } }
;             PG8_WAIT_VX(); PG8_WAIT_L(0); PG8_BAR; PG8_MMA(0, 0, At, B0); PG8_MMA(0, 1, At, B1); PG8_BAR; PG8_SCHED;
;             if constexpr (Epi::BIAS_DMA) { if (t == 0 && has_next) E.bias_dma(nxt, xlds + 8192 + ((ui + 1) & 1) * Epi::BIAS_STRIDE, wid, lane); }
;             PG8_LDA(At, 0, 1); PG8_STAGE(PG8_SB(0, 0), b2, voffB); PG8_STAGE(PG8_SB(0, 1), b2 + hstepB, voffB); PG8_STAGEA(PG8_SA(0, 0), a2, vA0, vA1);
.LBB0_546:
	s_mov_b64 s[36:37], s[10:11]
	s_add_u32 s20, s36, 0x100
	s_mov_b64 s[34:35], s[8:9]
	s_addc_u32 s45, s37, 0
	s_mov_b64 s[8:9], s[0:1]
	s_add_u32 s0, s34, 0x40080
	s_mov_b64 s[10:11], s[2:3]
	s_mov_b32 s15, s4
	s_mov_b32 s19, s6
	s_mov_b32 s6, s18
	s_mov_b32 s4, s14
	s_addc_u32 s1, s35, 0
	s_mov_b32 s46, -2
	s_mov_b32 s47, s5
	v_add_u32_e32 v142, 0x10000, v195
	v_add_u32_e32 v158, 0x14000, v195
	ds_read_b128 v[130:133], v142
	ds_read_b128 v[134:137], v142 offset:1024
	ds_read_b128 v[138:141], v142 offset:2048
	ds_read_b128 v[142:145], v142 offset:3072
	ds_read_b128 v[146:149], v158
	ds_read_b128 v[150:153], v158 offset:1024
	ds_read_b128 v[154:157], v158 offset:2048
	ds_read_b128 v[158:161], v158 offset:3072
	s_add_u32 s2, s0, 0xfffc0080
	s_addc_u32 s3, s1, -1
	s_cmp_eq_u32 s46, 12
	s_cselect_b32 s36, s8, s2
	s_cselect_b32 s37, s9, s3
	s_cselect_b32 s34, s10, s20
	s_cselect_b32 s35, s11, s45
	s_add_u32 s2, s36, 0x80
	s_addc_u32 s3, s37, 0
	ds_read_b128 v[162:165], v196
	ds_read_b128 v[166:169], v196 offset:1024
	ds_read_b128 v[170:173], v196 offset:2048
	ds_read_b128 v[174:177], v196 offset:3072
	ds_read_b128 v[180:183], v196 offset:4096
	ds_read_b128 v[184:187], v196 offset:5120
	ds_read_b128 v[188:191], v196 offset:6144
	ds_read_b128 v[198:201], v196 offset:7168
	s_add_i32 s48, s47, 0xc000
	s_mov_b32 m0, s48
	s_nop 0
	global_load_lds_dwordx4 v1, s[0:1]
	s_add_i32 s48, s47, 0xe000
	s_mov_b32 m0, s48
	s_nop 0
	global_load_lds_dwordx4 v192, s[0:1]
	s_waitcnt vmcnt(8)
	s_waitcnt lgkmcnt(0)
	s_barrier
	s_setprio 1
	s_waitcnt lgkmcnt(7)
	v_mfma_f32_16x16x32_bf16 v[114:117], v[130:133], v[162:165], 0
	v_mfma_f32_16x16x32_bf16 v[118:121], v[138:141], v[162:165], 0
	s_waitcnt lgkmcnt(5)
	v_mfma_f32_16x16x32_bf16 v[110:113], v[130:133], v[170:173], 0
	v_mfma_f32_16x16x32_bf16 v[106:109], v[138:141], v[170:173], 0
	s_waitcnt lgkmcnt(3)
	v_mfma_f32_16x16x32_bf16 v[94:97], v[130:133], v[180:183], 0
	v_mfma_f32_16x16x32_bf16 v[90:93], v[138:141], v[180:183], 0
	s_waitcnt lgkmcnt(1)
	v_mfma_f32_16x16x32_bf16 v[78:81], v[130:133], v[188:191], 0
	v_mfma_f32_16x16x32_bf16 v[74:77], v[138:141], v[188:191], 0
	v_mfma_f32_16x16x32_bf16 v[114:117], v[134:137], v[166:169], v[114:117]
	v_mfma_f32_16x16x32_bf16 v[118:121], v[142:145], v[166:169], v[118:121]
	v_mfma_f32_16x16x32_bf16 v[110:113], v[134:137], v[174:177], v[110:113]
	v_mfma_f32_16x16x32_bf16 v[106:109], v[142:145], v[174:177], v[106:109]
	v_mfma_f32_16x16x32_bf16 v[94:97], v[134:137], v[184:187], v[94:97]
	v_mfma_f32_16x16x32_bf16 v[90:93], v[142:145], v[184:187], v[90:93]
	s_waitcnt lgkmcnt(0)
	v_mfma_f32_16x16x32_bf16 v[78:81], v[134:137], v[198:201], v[78:81]
	v_mfma_f32_16x16x32_bf16 v[74:77], v[142:145], v[198:201], v[74:77]
	v_mfma_f32_16x16x32_bf16 v[126:129], v[146:149], v[162:165], 0
	v_mfma_f32_16x16x32_bf16 v[122:125], v[154:157], v[162:165], 0
	v_mfma_f32_16x16x32_bf16 v[102:105], v[146:149], v[170:173], 0
	v_mfma_f32_16x16x32_bf16 v[98:101], v[154:157], v[170:173], 0
	v_mfma_f32_16x16x32_bf16 v[86:89], v[146:149], v[180:183], 0
	v_mfma_f32_16x16x32_bf16 v[82:85], v[154:157], v[180:183], 0
	v_mfma_f32_16x16x32_bf16 v[70:73], v[146:149], v[188:191], 0
	v_mfma_f32_16x16x32_bf16 v[66:69], v[154:157], v[188:191], 0
	v_mfma_f32_16x16x32_bf16 v[126:129], v[150:153], v[166:169], v[126:129]
	v_mfma_f32_16x16x32_bf16 v[122:125], v[158:161], v[166:169], v[122:125]
	v_mfma_f32_16x16x32_bf16 v[102:105], v[150:153], v[174:177], v[102:105]
	v_mfma_f32_16x16x32_bf16 v[98:101], v[158:161], v[174:177], v[98:101]
	v_mfma_f32_16x16x32_bf16 v[86:89], v[150:153], v[184:187], v[86:89]
	v_mfma_f32_16x16x32_bf16 v[82:85], v[158:161], v[184:187], v[82:85]
	v_mfma_f32_16x16x32_bf16 v[70:73], v[150:153], v[198:201], v[70:73]
	v_mfma_f32_16x16x32_bf16 v[66:69], v[158:161], v[198:201], v[66:69]
	s_setprio 0
	s_barrier
	ds_read_b128 v[162:165], v196 offset:16384
	ds_read_b128 v[166:169], v196 offset:17408
	ds_read_b128 v[170:173], v196 offset:18432
	ds_read_b128 v[174:177], v196 offset:19456
	ds_read_b128 v[180:183], v196 offset:20480
	ds_read_b128 v[184:187], v196 offset:21504
	ds_read_b128 v[188:191], v196 offset:22528
	ds_read_b128 v[198:201], v196 offset:23552
	s_add_i32 s48, s47, 0x10000
	s_mov_b32 m0, s48
	s_nop 0
	global_load_lds_dwordx4 v193, s[34:35]
	s_add_i32 s48, s47, 0x12000
	s_mov_b32 m0, s48
	s_nop 0
	global_load_lds_dwordx4 v194, s[34:35]
	s_add_u32 s48, s34, 0x4000
	s_addc_u32 s49, s35, 0
	s_add_i32 s50, s47, 0x14000
	s_mov_b32 m0, s50
	s_nop 0
	global_load_lds_dwordx4 v193, s[48:49]
	s_add_i32 s50, s47, 0x16000
	s_mov_b32 m0, s50
	s_nop 0
	global_load_lds_dwordx4 v194, s[48:49]
	s_add_i32 s48, s47, 0x2000
	s_mov_b32 m0, s47
	s_nop 0
	global_load_lds_dwordx4 v1, s[36:37]
	s_nop 0
	s_mov_b32 m0, s48
	s_nop 0
	global_load_lds_dwordx4 v192, s[36:37]
	s_waitcnt vmcnt(8)
	s_waitcnt lgkmcnt(0)
	s_barrier
; #define PG8_STAGE(bufoff, gbase, voff) do { PG8_GLDS((const char*)(gbase), (voff)[0], ldsb + (bufoff)); PG8_GLDS((const char*)(gbase), (voff)[1], ldsb + (bufoff) + 8192u); } while (0)
; #define PG8_STAGEA(bufoff, gbase, o0, o1) do { PG8_GLDS((const char*)(gbase), (o0), ldsb + (bufoff)); PG8_GLDS((const char*)(gbase), (o1), ldsb + (bufoff) + 8192u); } while (0)
; #define PG8_STAGEA1(bufoff, gbase) do { if constexpr (Sched::GATHER) { PG8_STAGEA(bufoff, gbase, vA2, vA3); } else { PG8_STAGEA(bufoff, (gbase) + hstep, vA0, vA1); } } while (0)
; #define PG8_WAIT_VR() PG8_WAIT_V(8)
; #define PG8_WAIT_VX() do { if (relax) asm volatile("s_waitcnt vmcnt(%0)" :: "n"(8 + Epi::RELAX) : "memory"); else PG8_WAIT_V(8); } while (0)
; #define PG8_WAIT_L(n) asm volatile("s_waitcnt lgkmcnt(" #n ")" ::: "memory")
; template <class Epi, class Sched, bool F8 = false, bool PF = false, bool I8 = false, int PID = -1>
; __device__ __forceinline__ void gemm_phase(LAS unsigned char* lds, LAS unsigned char* xlds, const int RP, const int RPB, const int nt, const Sched& S, const Epi& E, const int stagger_ticks) {
;     ...
;             PG8_LDB(B0, 0, 0); PG8_LDB(B1, 0, 1); PG8_SCHED; PG8_LDA(At, 0, 0); PG8_STAGEA1(PG8_SA(1, 1), a1);
;             if (Sched::GATHER) { if (last) { const u32x4 nv = *nslot; vA0 = nv.x; vA1 = nv.y; vA2 = nv.z; vA3 = nv.w; } }
;             PG8_WAIT_VX(); PG8_WAIT_L(0); PG8_BAR; PG8_MMA(0, 0, At, B0); PG8_MMA(0, 1, At, B1); PG8_BAR; PG8_SCHED;
;             if constexpr (Epi::BIAS_DMA) { if (t == 0 && has_next) E.bias_dma(nxt, xlds + 8192 + ((ui + 1) & 1) * Epi::BIAS_STRIDE, wid, lane); }
;             PG8_LDA(At, 0, 1); PG8_STAGE(PG8_SB(0, 0), b2, voffB); PG8_STAGE(PG8_SB(0, 1), b2 + hstepB, voffB); PG8_STAGEA(PG8_SA(0, 0), a2, vA0, vA1);
;             PG8_WAIT_VX(); PG8_WAIT_L(0); PG8_BAR; PG8_MMA(1, 0, At, B0); PG8_MMA(1, 1, At, B1); PG8_BAR; PG8_SCHED;
;             PG8_LDB(B0, 1, 0); PG8_LDB(B1, 1, 1); PG8_SCHED; PG8_LDA(At, 1, 0); PG8_STAGEA1(PG8_SA(0, 1), a2);
;             PG8_WAIT_VR(); PG8_WAIT_L(0); PG8_BAR; PG8_MMA(0, 0, At, B0); PG8_MMA(0, 1, At, B1); PG8_BAR; PG8_SCHED;
;             PG8_LDA(At, 1, 1); PG8_STAGE(PG8_SB(1, 0), b3, voffB); PG8_STAGE(PG8_SB(1, 1), b3 + hstepB, voffB); PG8_STAGEA(PG8_SA(1, 0), a3, vA0, vA1);
;             PG8_WAIT_VR(); PG8_WAIT_L(0); PG8_BAR; PG8_MMA(1, 0, At, B0); PG8_MMA(1, 1, At, B1); PG8_BAR; PG8_SCHED;
	s_setprio 1
	s_waitcnt lgkmcnt(7)
	v_mfma_f32_16x16x32_bf16 v[50:53], v[130:133], v[162:165], 0
	v_mfma_f32_16x16x32_bf16 v[54:57], v[138:141], v[162:165], 0
	s_waitcnt lgkmcnt(5)
	v_mfma_f32_16x16x32_bf16 v[46:49], v[130:133], v[170:173], 0
	v_mfma_f32_16x16x32_bf16 v[42:45], v[138:141], v[170:173], 0
	s_waitcnt lgkmcnt(3)
	v_mfma_f32_16x16x32_bf16 v[30:33], v[130:133], v[180:183], 0
	v_mfma_f32_16x16x32_bf16 v[26:29], v[138:141], v[180:183], 0
	s_waitcnt lgkmcnt(1)
	v_mfma_f32_16x16x32_bf16 v[14:17], v[130:133], v[188:191], 0
	v_mfma_f32_16x16x32_bf16 v[10:13], v[138:141], v[188:191], 0
	v_mfma_f32_16x16x32_bf16 v[50:53], v[134:137], v[166:169], v[50:53]
	v_mfma_f32_16x16x32_bf16 v[54:57], v[142:145], v[166:169], v[54:57]
	v_mfma_f32_16x16x32_bf16 v[46:49], v[134:137], v[174:177], v[46:49]
	v_mfma_f32_16x16x32_bf16 v[42:45], v[142:145], v[174:177], v[42:45]
	v_mfma_f32_16x16x32_bf16 v[30:33], v[134:137], v[184:187], v[30:33]
	v_mfma_f32_16x16x32_bf16 v[26:29], v[142:145], v[184:187], v[26:29]
	s_waitcnt lgkmcnt(0)
	v_mfma_f32_16x16x32_bf16 v[14:17], v[134:137], v[198:201], v[14:17]
	v_mfma_f32_16x16x32_bf16 v[10:13], v[142:145], v[198:201], v[10:13]
	v_mfma_f32_16x16x32_bf16 v[58:61], v[146:149], v[162:165], 0
	v_mfma_f32_16x16x32_bf16 v[62:65], v[154:157], v[162:165], 0
	v_mfma_f32_16x16x32_bf16 v[38:41], v[146:149], v[170:173], 0
	v_mfma_f32_16x16x32_bf16 v[34:37], v[154:157], v[170:173], 0
	v_mfma_f32_16x16x32_bf16 v[22:25], v[146:149], v[180:183], 0
	v_mfma_f32_16x16x32_bf16 v[18:21], v[154:157], v[180:183], 0
	v_mfma_f32_16x16x32_bf16 v[6:9], v[146:149], v[188:191], 0
	v_mfma_f32_16x16x32_bf16 v[2:5], v[154:157], v[188:191], 0
	v_mfma_f32_16x16x32_bf16 v[58:61], v[150:153], v[166:169], v[58:61]
	v_mfma_f32_16x16x32_bf16 v[62:65], v[158:161], v[166:169], v[62:65]
	v_mfma_f32_16x16x32_bf16 v[38:41], v[150:153], v[174:177], v[38:41]
	v_mfma_f32_16x16x32_bf16 v[34:37], v[158:161], v[174:177], v[34:37]
	v_mfma_f32_16x16x32_bf16 v[22:25], v[150:153], v[184:187], v[22:25]
	v_mfma_f32_16x16x32_bf16 v[18:21], v[158:161], v[184:187], v[18:21]
	v_mfma_f32_16x16x32_bf16 v[6:9], v[150:153], v[198:201], v[6:9]
	v_mfma_f32_16x16x32_bf16 v[2:5], v[158:161], v[198:201], v[2:5]
	s_setprio 0
	s_barrier
	v_add_u32_e32 v142, 0x18000, v195
	v_add_u32_e32 v158, 0x1c000, v195
	ds_read_b128 v[130:133], v142
	ds_read_b128 v[134:137], v142 offset:1024
	ds_read_b128 v[138:141], v142 offset:2048
	ds_read_b128 v[142:145], v142 offset:3072
	ds_read_b128 v[146:149], v158
	ds_read_b128 v[150:153], v158 offset:1024
	ds_read_b128 v[154:157], v158 offset:2048
	ds_read_b128 v[158:161], v158 offset:3072
	ds_read_b128 v[162:165], v196 offset:32768
	ds_read_b128 v[166:169], v196 offset:33792
	ds_read_b128 v[170:173], v196 offset:34816
	ds_read_b128 v[174:177], v196 offset:35840
	ds_read_b128 v[180:183], v196 offset:36864
	ds_read_b128 v[184:187], v196 offset:37888
	ds_read_b128 v[188:191], v196 offset:38912
	ds_read_b128 v[198:201], v196 offset:39936
	s_add_u32 s36, s36, 0x40000
	s_addc_u32 s37, s37, 0
	s_add_i32 s48, s47, 0x4000
	s_mov_b32 m0, s48
	s_nop 0
	global_load_lds_dwordx4 v1, s[36:37]
	s_add_i32 s48, s47, 0x6000
	s_mov_b32 m0, s48
	s_nop 0
	global_load_lds_dwordx4 v192, s[36:37]
	s_waitcnt vmcnt(8)
	s_waitcnt lgkmcnt(0)
	s_barrier
	s_setprio 1
	s_waitcnt lgkmcnt(7)
	v_mfma_f32_16x16x32_bf16 v[114:117], v[130:133], v[162:165], v[114:117]
	v_mfma_f32_16x16x32_bf16 v[118:121], v[138:141], v[162:165], v[118:121]
	s_waitcnt lgkmcnt(5)
	v_mfma_f32_16x16x32_bf16 v[110:113], v[130:133], v[170:173], v[110:113]
	v_mfma_f32_16x16x32_bf16 v[106:109], v[138:141], v[170:173], v[106:109]
	s_waitcnt lgkmcnt(3)
	v_mfma_f32_16x16x32_bf16 v[94:97], v[130:133], v[180:183], v[94:97]
	v_mfma_f32_16x16x32_bf16 v[90:93], v[138:141], v[180:183], v[90:93]
	s_waitcnt lgkmcnt(1)
	v_mfma_f32_16x16x32_bf16 v[78:81], v[130:133], v[188:191], v[78:81]
	v_mfma_f32_16x16x32_bf16 v[74:77], v[138:141], v[188:191], v[74:77]
	v_mfma_f32_16x16x32_bf16 v[114:117], v[134:137], v[166:169], v[114:117]
	v_mfma_f32_16x16x32_bf16 v[118:121], v[142:145], v[166:169], v[118:121]
	v_mfma_f32_16x16x32_bf16 v[110:113], v[134:137], v[174:177], v[110:113]
	v_mfma_f32_16x16x32_bf16 v[106:109], v[142:145], v[174:177], v[106:109]
	v_mfma_f32_16x16x32_bf16 v[94:97], v[134:137], v[184:187], v[94:97]
	v_mfma_f32_16x16x32_bf16 v[90:93], v[142:145], v[184:187], v[90:93]
	s_waitcnt lgkmcnt(0)
	v_mfma_f32_16x16x32_bf16 v[78:81], v[134:137], v[198:201], v[78:81]
	v_mfma_f32_16x16x32_bf16 v[74:77], v[142:145], v[198:201], v[74:77]
	v_mfma_f32_16x16x32_bf16 v[126:129], v[146:149], v[162:165], v[126:129]
	v_mfma_f32_16x16x32_bf16 v[122:125], v[154:157], v[162:165], v[122:125]
	v_mfma_f32_16x16x32_bf16 v[102:105], v[146:149], v[170:173], v[102:105]
	v_mfma_f32_16x16x32_bf16 v[98:101], v[154:157], v[170:173], v[98:101]
	v_mfma_f32_16x16x32_bf16 v[86:89], v[146:149], v[180:183], v[86:89]
	v_mfma_f32_16x16x32_bf16 v[82:85], v[154:157], v[180:183], v[82:85]
	v_mfma_f32_16x16x32_bf16 v[70:73], v[146:149], v[188:191], v[70:73]
	v_mfma_f32_16x16x32_bf16 v[66:69], v[154:157], v[188:191], v[66:69]
	v_mfma_f32_16x16x32_bf16 v[126:129], v[150:153], v[166:169], v[126:129]
	v_mfma_f32_16x16x32_bf16 v[122:125], v[158:161], v[166:169], v[122:125]
	v_mfma_f32_16x16x32_bf16 v[102:105], v[150:153], v[174:177], v[102:105]
	v_mfma_f32_16x16x32_bf16 v[98:101], v[158:161], v[174:177], v[98:101]
	v_mfma_f32_16x16x32_bf16 v[86:89], v[150:153], v[184:187], v[86:89]
	v_mfma_f32_16x16x32_bf16 v[82:85], v[158:161], v[184:187], v[82:85]
	v_mfma_f32_16x16x32_bf16 v[70:73], v[150:153], v[198:201], v[70:73]
	v_mfma_f32_16x16x32_bf16 v[66:69], v[158:161], v[198:201], v[66:69]
	s_setprio 0
	s_barrier
; #define PG8_WAIT_VR() PG8_WAIT_V(8)
; template <class Epi, class Sched, bool F8 = false, bool PF = false, bool I8 = false, int PID = -1>
; __device__ __forceinline__ void gemm_phase(LAS unsigned char* lds, LAS unsigned char* xlds, const int RP, const int RPB, const int nt, const Sched& S, const Epi& E, const int stagger_ticks) {
;     ...
;         for (int t = 0; t < nt; t += 2) {
;             const bool last = (t == nt - 2);
;             unsigned ldsb = ldsb0; asm volatile("" : "+s"(ldsb));
;             const char* a1 = cA + (size_t)(t + 1) * kstep;
;             const char* a2 = last ? nA : cA + (size_t)(t + 2) * kstep; const char* b2 = last ? nB : cB + (size_t)(t + 2) * kstep;
;             const char* a3 = a2 + kstep; const char* b3 = b2 + kstep;
;             if constexpr (PF) { const char* pfa = (t + 4 < nt) ? cA + (size_t)(t + 4) * kstep : nA + (size_t)(t + 4 - nt) * kstep;
;                 asm volatile("s_mov_b32 m0, %2\n\ts_nop 0\n\tglobal_load_lds_dword %0, %1" :: "v"(voffP), "s"(pfa), "s"(ldsP) : "memory", "m0"); }
;             const bool relax = (Epi::RELAX > 0) && (t == 0) && epi_ran;
;             PG8_LDB(B0, 0, 0); PG8_LDB(B1, 0, 1); PG8_SCHED; PG8_LDA(At, 0, 0); PG8_STAGEA1(PG8_SA(1, 1), a1);
;             if (Sched::GATHER) { if (last) { const u32x4 nv = *nslot; vA0 = nv.x; vA1 = nv.y; vA2 = nv.z; vA3 = nv.w; } }
;             PG8_WAIT_VX(); PG8_WAIT_L(0); PG8_BAR; PG8_MMA(0, 0, At, B0); PG8_MMA(0, 1, At, B1); PG8_BAR; PG8_SCHED;
;             if constexpr (Epi::BIAS_DMA) { if (t == 0 && has_next) E.bias_dma(nxt, xlds + 8192 + ((ui + 1) & 1) * Epi::BIAS_STRIDE, wid, lane); }
;             PG8_LDA(At, 0, 1); PG8_STAGE(PG8_SB(0, 0), b2, voffB); PG8_STAGE(PG8_SB(0, 1), b2 + hstepB, voffB); PG8_STAGEA(PG8_SA(0, 0), a2, vA0, vA1);
;             PG8_WAIT_VX(); PG8_WAIT_L(0); PG8_BAR; PG8_MMA(1, 0, At, B0); PG8_MMA(1, 1, At, B1); PG8_BAR; PG8_SCHED;
;             PG8_LDB(B0, 1, 0); PG8_LDB(B1, 1, 1); PG8_SCHED; PG8_LDA(At, 1, 0); PG8_STAGEA1(PG8_SA(0, 1), a2);
;             PG8_WAIT_VR(); PG8_WAIT_L(0); PG8_BAR; PG8_MMA(0, 0, At, B0); PG8_MMA(0, 1, At, B1); PG8_BAR; PG8_SCHED;
;             PG8_LDA(At, 1, 1); PG8_STAGE(PG8_SB(1, 0), b3, voffB); PG8_STAGE(PG8_SB(1, 1), b3 + hstepB, voffB); PG8_STAGEA(PG8_SA(1, 0), a3, vA0, vA1);
;             PG8_WAIT_VR(); PG8_WAIT_L(0); PG8_BAR; PG8_MMA(1, 0, At, B0); PG8_MMA(1, 1, At, B1); PG8_BAR; PG8_SCHED;
	s_add_u32 s36, s34, 0x80
	ds_read_b128 v[162:165], v196 offset:49152
	ds_read_b128 v[166:169], v196 offset:50176
	ds_read_b128 v[170:173], v196 offset:51200
	ds_read_b128 v[174:177], v196 offset:52224
	ds_read_b128 v[180:183], v196 offset:53248
	ds_read_b128 v[184:187], v196 offset:54272
	ds_read_b128 v[188:191], v196 offset:55296
	ds_read_b128 v[198:201], v196 offset:56320
	s_addc_u32 s37, s35, 0
	s_add_i32 s48, s47, 0x18000
	s_mov_b32 m0, s48
	s_nop 0
	global_load_lds_dwordx4 v193, s[36:37]
	s_add_i32 s48, s47, 0x1a000
	s_mov_b32 m0, s48
	s_nop 0
	global_load_lds_dwordx4 v194, s[36:37]
	s_add_u32 s34, s34, 0x4080
	s_addc_u32 s35, s35, 0
	s_add_i32 s36, s47, 0x1c000
	s_mov_b32 m0, s36
	s_nop 0
	global_load_lds_dwordx4 v193, s[34:35]
	s_add_i32 s36, s47, 0x1e000
	s_mov_b32 m0, s36
	s_nop 0
	global_load_lds_dwordx4 v194, s[34:35]
	s_add_i32 s34, s47, 0x8000
	s_mov_b32 m0, s34
	s_nop 0
	global_load_lds_dwordx4 v1, s[2:3]
	s_add_i32 s47, s47, 0xa000
	s_mov_b32 m0, s47
	s_nop 0
	global_load_lds_dwordx4 v192, s[2:3]
	s_waitcnt vmcnt(8)
	s_waitcnt lgkmcnt(0)
	s_barrier
	s_setprio 1
	s_waitcnt lgkmcnt(7)
	v_mfma_f32_16x16x32_bf16 v[50:53], v[130:133], v[162:165], v[50:53]
	v_mfma_f32_16x16x32_bf16 v[54:57], v[138:141], v[162:165], v[54:57]
	s_waitcnt lgkmcnt(5)
	v_mfma_f32_16x16x32_bf16 v[46:49], v[130:133], v[170:173], v[46:49]
	v_mfma_f32_16x16x32_bf16 v[42:45], v[138:141], v[170:173], v[42:45]
	s_waitcnt lgkmcnt(3)
	v_mfma_f32_16x16x32_bf16 v[30:33], v[130:133], v[180:183], v[30:33]
	v_mfma_f32_16x16x32_bf16 v[26:29], v[138:141], v[180:183], v[26:29]
	s_waitcnt lgkmcnt(1)
	v_mfma_f32_16x16x32_bf16 v[14:17], v[130:133], v[188:191], v[14:17]
	v_mfma_f32_16x16x32_bf16 v[10:13], v[138:141], v[188:191], v[10:13]
	v_mfma_f32_16x16x32_bf16 v[50:53], v[134:137], v[166:169], v[50:53]
	v_mfma_f32_16x16x32_bf16 v[54:57], v[142:145], v[166:169], v[54:57]
	v_mfma_f32_16x16x32_bf16 v[46:49], v[134:137], v[174:177], v[46:49]
	v_mfma_f32_16x16x32_bf16 v[42:45], v[142:145], v[174:177], v[42:45]
	v_mfma_f32_16x16x32_bf16 v[30:33], v[134:137], v[184:187], v[30:33]
	v_mfma_f32_16x16x32_bf16 v[26:29], v[142:145], v[184:187], v[26:29]
	s_waitcnt lgkmcnt(0)
	v_mfma_f32_16x16x32_bf16 v[14:17], v[134:137], v[198:201], v[14:17]
	v_mfma_f32_16x16x32_bf16 v[10:13], v[142:145], v[198:201], v[10:13]
	v_mfma_f32_16x16x32_bf16 v[58:61], v[146:149], v[162:165], v[58:61]
	v_mfma_f32_16x16x32_bf16 v[62:65], v[154:157], v[162:165], v[62:65]
	v_mfma_f32_16x16x32_bf16 v[38:41], v[146:149], v[170:173], v[38:41]
	v_mfma_f32_16x16x32_bf16 v[34:37], v[154:157], v[170:173], v[34:37]
	v_mfma_f32_16x16x32_bf16 v[22:25], v[146:149], v[180:183], v[22:25]
	v_mfma_f32_16x16x32_bf16 v[18:21], v[154:157], v[180:183], v[18:21]
	v_mfma_f32_16x16x32_bf16 v[6:9], v[146:149], v[188:191], v[6:9]
	v_mfma_f32_16x16x32_bf16 v[2:5], v[154:157], v[188:191], v[2:5]
	v_mfma_f32_16x16x32_bf16 v[58:61], v[150:153], v[166:169], v[58:61]
	v_mfma_f32_16x16x32_bf16 v[62:65], v[158:161], v[166:169], v[62:65]
	v_mfma_f32_16x16x32_bf16 v[38:41], v[150:153], v[174:177], v[38:41]
	v_mfma_f32_16x16x32_bf16 v[34:37], v[158:161], v[174:177], v[34:37]
	v_mfma_f32_16x16x32_bf16 v[22:25], v[150:153], v[184:187], v[22:25]
	v_mfma_f32_16x16x32_bf16 v[18:21], v[158:161], v[184:187], v[18:21]
	v_mfma_f32_16x16x32_bf16 v[6:9], v[150:153], v[198:201], v[6:9]
	v_mfma_f32_16x16x32_bf16 v[2:5], v[158:161], v[198:201], v[2:5]
	s_setprio 0
	s_barrier
	s_add_i32 s46, s46, 2
	s_add_u32 s20, s20, 0x100
	s_addc_u32 s45, s45, 0
	s_add_u32 s0, s0, 0x100
	s_addc_u32 s1, s1, 0
	s_cmp_gt_u32 s46, 13
.LBB0_547:
	s_mov_b32 s47, s5
	v_add_u32_e32 v142, 0x10000, v195
	v_add_u32_e32 v158, 0x14000, v195
	ds_read_b128 v[130:133], v142
	ds_read_b128 v[134:137], v142 offset:1024
	ds_read_b128 v[138:141], v142 offset:2048
	ds_read_b128 v[142:145], v142 offset:3072
	ds_read_b128 v[146:149], v158
	ds_read_b128 v[150:153], v158 offset:1024
	ds_read_b128 v[154:157], v158 offset:2048
	ds_read_b128 v[158:161], v158 offset:3072
	s_add_u32 s2, s0, 0xfffc0080
	s_addc_u32 s3, s1, -1
	s_cmp_eq_u32 s46, 12
	s_cselect_b32 s36, s8, s2
	s_cselect_b32 s37, s9, s3
	s_cselect_b32 s34, s10, s20
	s_cselect_b32 s35, s11, s45
	s_add_u32 s2, s36, 0x80
	s_addc_u32 s3, s37, 0
	ds_read_b128 v[162:165], v196
	ds_read_b128 v[166:169], v196 offset:1024
	ds_read_b128 v[170:173], v196 offset:2048
	ds_read_b128 v[174:177], v196 offset:3072
	ds_read_b128 v[180:183], v196 offset:4096
	ds_read_b128 v[184:187], v196 offset:5120
	ds_read_b128 v[188:191], v196 offset:6144
	ds_read_b128 v[198:201], v196 offset:7168
	s_add_i32 s48, s47, 0xc000
	s_mov_b32 m0, s48
	s_nop 0
	global_load_lds_dwordx4 v1, s[0:1]
	s_add_i32 s48, s47, 0xe000
	s_mov_b32 m0, s48
	s_nop 0
	global_load_lds_dwordx4 v192, s[0:1]
	s_waitcnt vmcnt(8)
	s_waitcnt lgkmcnt(0)
	s_barrier
; #define PG8_STAGE(bufoff, gbase, voff) do { PG8_GLDS((const char*)(gbase), (voff)[0], ldsb + (bufoff)); PG8_GLDS((const char*)(gbase), (voff)[1], ldsb + (bufoff) + 8192u); } while (0)
; #define PG8_STAGEA(bufoff, gbase, o0, o1) do { PG8_GLDS((const char*)(gbase), (o0), ldsb + (bufoff)); PG8_GLDS((const char*)(gbase), (o1), ldsb + (bufoff) + 8192u); } while (0)
; #define PG8_STAGEA1(bufoff, gbase) do { if constexpr (Sched::GATHER) { PG8_STAGEA(bufoff, gbase, vA2, vA3); } else { PG8_STAGEA(bufoff, (gbase) + hstep, vA0, vA1); } } while (0)
; #define PG8_WAIT_VR() PG8_WAIT_V(8)
; #define PG8_WAIT_VX() do { if (relax) asm volatile("s_waitcnt vmcnt(%0)" :: "n"(8 + Epi::RELAX) : "memory"); else PG8_WAIT_V(8); } while (0)
; #define PG8_WAIT_L(n) asm volatile("s_waitcnt lgkmcnt(" #n ")" ::: "memory")
; template <class Epi, class Sched, bool F8 = false, bool PF = false, bool I8 = false, int PID = -1>
; __device__ __forceinline__ void gemm_phase(LAS unsigned char* lds, LAS unsigned char* xlds, const int RP, const int RPB, const int nt, const Sched& S, const Epi& E, const int stagger_ticks) {
;     ...
;             PG8_LDB(B0, 0, 0); PG8_LDB(B1, 0, 1); PG8_SCHED; PG8_LDA(At, 0, 0); PG8_STAGEA1(PG8_SA(1, 1), a1);
;             if (Sched::GATHER) { if (last) { const u32x4 nv = *nslot; vA0 = nv.x; vA1 = nv.y; vA2 = nv.z; vA3 = nv.w; } }
;             PG8_WAIT_VX(); PG8_WAIT_L(0); PG8_BAR; PG8_MMA(0, 0, At, B0); PG8_MMA(0, 1, At, B1); PG8_BAR; PG8_SCHED;
;             if constexpr (Epi::BIAS_DMA) { if (t == 0 && has_next) E.bias_dma(nxt, xlds + 8192 + ((ui + 1) & 1) * Epi::BIAS_STRIDE, wid, lane); }
;             PG8_LDA(At, 0, 1); PG8_STAGE(PG8_SB(0, 0), b2, voffB); PG8_STAGE(PG8_SB(0, 1), b2 + hstepB, voffB); PG8_STAGEA(PG8_SA(0, 0), a2, vA0, vA1);
;             PG8_WAIT_VX(); PG8_WAIT_L(0); PG8_BAR; PG8_MMA(1, 0, At, B0); PG8_MMA(1, 1, At, B1); PG8_BAR; PG8_SCHED;
;             PG8_LDB(B0, 1, 0); PG8_LDB(B1, 1, 1); PG8_SCHED; PG8_LDA(At, 1, 0); PG8_STAGEA1(PG8_SA(0, 1), a2);
;             PG8_WAIT_VR(); PG8_WAIT_L(0); PG8_BAR; PG8_MMA(0, 0, At, B0); PG8_MMA(0, 1, At, B1); PG8_BAR; PG8_SCHED;
;             PG8_LDA(At, 1, 1); PG8_STAGE(PG8_SB(1, 0), b3, voffB); PG8_STAGE(PG8_SB(1, 1), b3 + hstepB, voffB); PG8_STAGEA(PG8_SA(1, 0), a3, vA0, vA1);
;             PG8_WAIT_VR(); PG8_WAIT_L(0); PG8_BAR; PG8_MMA(1, 0, At, B0); PG8_MMA(1, 1, At, B1); PG8_BAR; PG8_SCHED;
	s_setprio 1
	s_waitcnt lgkmcnt(7)
	v_mfma_f32_16x16x32_bf16 v[114:117], v[130:133], v[162:165], v[114:117]
	v_mfma_f32_16x16x32_bf16 v[118:121], v[138:141], v[162:165], v[118:121]
	s_waitcnt lgkmcnt(5)
	v_mfma_f32_16x16x32_bf16 v[110:113], v[130:133], v[170:173], v[110:113]
	v_mfma_f32_16x16x32_bf16 v[106:109], v[138:141], v[170:173], v[106:109]
	s_waitcnt lgkmcnt(3)
	v_mfma_f32_16x16x32_bf16 v[94:97], v[130:133], v[180:183], v[94:97]
	v_mfma_f32_16x16x32_bf16 v[90:93], v[138:141], v[180:183], v[90:93]
	s_waitcnt lgkmcnt(1)
	v_mfma_f32_16x16x32_bf16 v[78:81], v[130:133], v[188:191], v[78:81]
	v_mfma_f32_16x16x32_bf16 v[74:77], v[138:141], v[188:191], v[74:77]
	v_mfma_f32_16x16x32_bf16 v[114:117], v[134:137], v[166:169], v[114:117]
	v_mfma_f32_16x16x32_bf16 v[118:121], v[142:145], v[166:169], v[118:121]
	v_mfma_f32_16x16x32_bf16 v[110:113], v[134:137], v[174:177], v[110:113]
	v_mfma_f32_16x16x32_bf16 v[106:109], v[142:145], v[174:177], v[106:109]
	v_mfma_f32_16x16x32_bf16 v[94:97], v[134:137], v[184:187], v[94:97]
	v_mfma_f32_16x16x32_bf16 v[90:93], v[142:145], v[184:187], v[90:93]
	s_waitcnt lgkmcnt(0)
	v_mfma_f32_16x16x32_bf16 v[78:81], v[134:137], v[198:201], v[78:81]
	v_mfma_f32_16x16x32_bf16 v[74:77], v[142:145], v[198:201], v[74:77]
	v_mfma_f32_16x16x32_bf16 v[126:129], v[146:149], v[162:165], v[126:129]
	v_mfma_f32_16x16x32_bf16 v[122:125], v[154:157], v[162:165], v[122:125]
	v_mfma_f32_16x16x32_bf16 v[102:105], v[146:149], v[170:173], v[102:105]
	v_mfma_f32_16x16x32_bf16 v[98:101], v[154:157], v[170:173], v[98:101]
	v_mfma_f32_16x16x32_bf16 v[86:89], v[146:149], v[180:183], v[86:89]
	v_mfma_f32_16x16x32_bf16 v[82:85], v[154:157], v[180:183], v[82:85]
	v_mfma_f32_16x16x32_bf16 v[70:73], v[146:149], v[188:191], v[70:73]
	v_mfma_f32_16x16x32_bf16 v[66:69], v[154:157], v[188:191], v[66:69]
	v_mfma_f32_16x16x32_bf16 v[126:129], v[150:153], v[166:169], v[126:129]
	v_mfma_f32_16x16x32_bf16 v[122:125], v[158:161], v[166:169], v[122:125]
	v_mfma_f32_16x16x32_bf16 v[102:105], v[150:153], v[174:177], v[102:105]
	v_mfma_f32_16x16x32_bf16 v[98:101], v[158:161], v[174:177], v[98:101]
	v_mfma_f32_16x16x32_bf16 v[86:89], v[150:153], v[184:187], v[86:89]
	v_mfma_f32_16x16x32_bf16 v[82:85], v[158:161], v[184:187], v[82:85]
	v_mfma_f32_16x16x32_bf16 v[70:73], v[150:153], v[198:201], v[70:73]
	v_mfma_f32_16x16x32_bf16 v[66:69], v[158:161], v[198:201], v[66:69]
	s_setprio 0
	s_barrier
	ds_read_b128 v[162:165], v196 offset:16384
	ds_read_b128 v[166:169], v196 offset:17408
	ds_read_b128 v[170:173], v196 offset:18432
	ds_read_b128 v[174:177], v196 offset:19456
	ds_read_b128 v[180:183], v196 offset:20480
	ds_read_b128 v[184:187], v196 offset:21504
	ds_read_b128 v[188:191], v196 offset:22528
	ds_read_b128 v[198:201], v196 offset:23552
	s_add_i32 s48, s47, 0x10000
	s_mov_b32 m0, s48
	s_nop 0
	global_load_lds_dwordx4 v193, s[34:35]
	s_add_i32 s48, s47, 0x12000
	s_mov_b32 m0, s48
	s_nop 0
	global_load_lds_dwordx4 v194, s[34:35]
	s_add_u32 s48, s34, 0x4000
	s_addc_u32 s49, s35, 0
	s_add_i32 s50, s47, 0x14000
	s_mov_b32 m0, s50
	s_nop 0
	global_load_lds_dwordx4 v193, s[48:49]
	s_add_i32 s50, s47, 0x16000
	s_mov_b32 m0, s50
	s_nop 0
	global_load_lds_dwordx4 v194, s[48:49]
	s_add_i32 s48, s47, 0x2000
	s_mov_b32 m0, s47
	s_nop 0
	global_load_lds_dwordx4 v1, s[36:37]
	s_nop 0
	s_mov_b32 m0, s48
	s_nop 0
	global_load_lds_dwordx4 v192, s[36:37]
	s_waitcnt vmcnt(8)
	s_waitcnt lgkmcnt(0)
	s_barrier
	s_setprio 1
	s_waitcnt lgkmcnt(7)
	v_mfma_f32_16x16x32_bf16 v[50:53], v[130:133], v[162:165], v[50:53]
	v_mfma_f32_16x16x32_bf16 v[54:57], v[138:141], v[162:165], v[54:57]
	s_waitcnt lgkmcnt(5)
	v_mfma_f32_16x16x32_bf16 v[46:49], v[130:133], v[170:173], v[46:49]
	v_mfma_f32_16x16x32_bf16 v[42:45], v[138:141], v[170:173], v[42:45]
	s_waitcnt lgkmcnt(3)
	v_mfma_f32_16x16x32_bf16 v[30:33], v[130:133], v[180:183], v[30:33]
	v_mfma_f32_16x16x32_bf16 v[26:29], v[138:141], v[180:183], v[26:29]
	s_waitcnt lgkmcnt(1)
	v_mfma_f32_16x16x32_bf16 v[14:17], v[130:133], v[188:191], v[14:17]
	v_mfma_f32_16x16x32_bf16 v[10:13], v[138:141], v[188:191], v[10:13]
	v_mfma_f32_16x16x32_bf16 v[50:53], v[134:137], v[166:169], v[50:53]
	v_mfma_f32_16x16x32_bf16 v[54:57], v[142:145], v[166:169], v[54:57]
	v_mfma_f32_16x16x32_bf16 v[46:49], v[134:137], v[174:177], v[46:49]
	v_mfma_f32_16x16x32_bf16 v[42:45], v[142:145], v[174:177], v[42:45]
	v_mfma_f32_16x16x32_bf16 v[30:33], v[134:137], v[184:187], v[30:33]
	v_mfma_f32_16x16x32_bf16 v[26:29], v[142:145], v[184:187], v[26:29]
	s_waitcnt lgkmcnt(0)
	v_mfma_f32_16x16x32_bf16 v[14:17], v[134:137], v[198:201], v[14:17]
	v_mfma_f32_16x16x32_bf16 v[10:13], v[142:145], v[198:201], v[10:13]
	v_mfma_f32_16x16x32_bf16 v[58:61], v[146:149], v[162:165], v[58:61]
	v_mfma_f32_16x16x32_bf16 v[62:65], v[154:157], v[162:165], v[62:65]
	v_mfma_f32_16x16x32_bf16 v[38:41], v[146:149], v[170:173], v[38:41]
	v_mfma_f32_16x16x32_bf16 v[34:37], v[154:157], v[170:173], v[34:37]
	v_mfma_f32_16x16x32_bf16 v[22:25], v[146:149], v[180:183], v[22:25]
	v_mfma_f32_16x16x32_bf16 v[18:21], v[154:157], v[180:183], v[18:21]
	v_mfma_f32_16x16x32_bf16 v[6:9], v[146:149], v[188:191], v[6:9]
	v_mfma_f32_16x16x32_bf16 v[2:5], v[154:157], v[188:191], v[2:5]
	v_mfma_f32_16x16x32_bf16 v[58:61], v[150:153], v[166:169], v[58:61]
	v_mfma_f32_16x16x32_bf16 v[62:65], v[158:161], v[166:169], v[62:65]
	v_mfma_f32_16x16x32_bf16 v[38:41], v[150:153], v[174:177], v[38:41]
	v_mfma_f32_16x16x32_bf16 v[34:37], v[158:161], v[174:177], v[34:37]
	v_mfma_f32_16x16x32_bf16 v[22:25], v[150:153], v[184:187], v[22:25]
	v_mfma_f32_16x16x32_bf16 v[18:21], v[158:161], v[184:187], v[18:21]
	v_mfma_f32_16x16x32_bf16 v[6:9], v[150:153], v[198:201], v[6:9]
	v_mfma_f32_16x16x32_bf16 v[2:5], v[158:161], v[198:201], v[2:5]
	s_setprio 0
	s_barrier
; #define PG8_STAGE(bufoff, gbase, voff) do { PG8_GLDS((const char*)(gbase), (voff)[0], ldsb + (bufoff)); PG8_GLDS((const char*)(gbase), (voff)[1], ldsb + (bufoff) + 8192u); } while (0)
; #define PG8_STAGEA(bufoff, gbase, o0, o1) do { PG8_GLDS((const char*)(gbase), (o0), ldsb + (bufoff)); PG8_GLDS((const char*)(gbase), (o1), ldsb + (bufoff) + 8192u); } while (0)
; #define PG8_LDA(dst, b, h) do { if constexpr (F8) { _Pragma("unroll") for (int m = 0; m < 4; ++m) dst##8[m] = PG8_LD32(lds + PG8_SA(b, h) + aoff + m * 2048); } else { \
;         _Pragma("unroll") for (int m = 0; m < 4; ++m) _Pragma("unroll") for (int k = 0; k < 2; ++k) dst[m][k] = *(const LAS bf16x8*)(lds + PG8_SA(b, h) + aoff + m * 2048 + k * 1024); } } while (0)
; #define PG8_WAIT_VR() PG8_WAIT_V(8)
; #define PG8_WAIT_L(n) asm volatile("s_waitcnt lgkmcnt(" #n ")" ::: "memory")
; #define PG8_BAR __builtin_amdgcn_s_barrier()
; #define PG8_SCHED __builtin_amdgcn_sched_barrier(0)
; template <class Epi, class Sched, bool F8 = false, bool PF = false, bool I8 = false, int PID = -1>
; __device__ __forceinline__ void gemm_phase(LAS unsigned char* lds, LAS unsigned char* xlds, const int RP, const int RPB, const int nt, const Sched& S, const Epi& E, const int stagger_ticks) {
;     ...
;             PG8_WAIT_VR(); PG8_WAIT_L(0); PG8_BAR; PG8_MMA(0, 0, At, B0); PG8_MMA(0, 1, At, B1); PG8_BAR; PG8_SCHED;
;             PG8_LDA(At, 1, 1); PG8_STAGE(PG8_SB(1, 0), b3, voffB); PG8_STAGE(PG8_SB(1, 1), b3 + hstepB, voffB); PG8_STAGEA(PG8_SA(1, 0), a3, vA0, vA1);
;             PG8_WAIT_VR(); PG8_WAIT_L(0); PG8_BAR; PG8_MMA(1, 0, At, B0); PG8_MMA(1, 1, At, B1); PG8_BAR; PG8_SCHED;
	v_add_u32_e32 v142, 0x18000, v195
	v_add_u32_e32 v158, 0x1c000, v195
	ds_read_b128 v[130:133], v142
	ds_read_b128 v[134:137], v142 offset:1024
	ds_read_b128 v[138:141], v142 offset:2048
	ds_read_b128 v[142:145], v142 offset:3072
	ds_read_b128 v[146:149], v158
	ds_read_b128 v[150:153], v158 offset:1024
	ds_read_b128 v[154:157], v158 offset:2048
	ds_read_b128 v[158:161], v158 offset:3072
	ds_read_b128 v[162:165], v196 offset:32768
	ds_read_b128 v[166:169], v196 offset:33792
	ds_read_b128 v[170:173], v196 offset:34816
	ds_read_b128 v[174:177], v196 offset:35840
	ds_read_b128 v[180:183], v196 offset:36864
	ds_read_b128 v[184:187], v196 offset:37888
	ds_read_b128 v[188:191], v196 offset:38912
	ds_read_b128 v[198:201], v196 offset:39936
	s_add_u32 s36, s36, 0x40000
	s_addc_u32 s37, s37, 0
	s_add_i32 s48, s47, 0x4000
	s_mov_b32 m0, s48
	s_nop 0
	global_load_lds_dwordx4 v1, s[36:37]
	s_add_i32 s48, s47, 0x6000
	s_mov_b32 m0, s48
	s_nop 0
	global_load_lds_dwordx4 v192, s[36:37]
	s_waitcnt vmcnt(8)
	s_waitcnt lgkmcnt(0)
	s_barrier
	s_setprio 1
	s_waitcnt lgkmcnt(7)
	v_mfma_f32_16x16x32_bf16 v[114:117], v[130:133], v[162:165], v[114:117]
	v_mfma_f32_16x16x32_bf16 v[118:121], v[138:141], v[162:165], v[118:121]
	s_waitcnt lgkmcnt(5)
	v_mfma_f32_16x16x32_bf16 v[110:113], v[130:133], v[170:173], v[110:113]
	v_mfma_f32_16x16x32_bf16 v[106:109], v[138:141], v[170:173], v[106:109]
	s_waitcnt lgkmcnt(3)
	v_mfma_f32_16x16x32_bf16 v[94:97], v[130:133], v[180:183], v[94:97]
	v_mfma_f32_16x16x32_bf16 v[90:93], v[138:141], v[180:183], v[90:93]
	s_waitcnt lgkmcnt(1)
	v_mfma_f32_16x16x32_bf16 v[78:81], v[130:133], v[188:191], v[78:81]
	v_mfma_f32_16x16x32_bf16 v[74:77], v[138:141], v[188:191], v[74:77]
	v_mfma_f32_16x16x32_bf16 v[114:117], v[134:137], v[166:169], v[114:117]
	v_mfma_f32_16x16x32_bf16 v[118:121], v[142:145], v[166:169], v[118:121]
	v_mfma_f32_16x16x32_bf16 v[110:113], v[134:137], v[174:177], v[110:113]
	v_mfma_f32_16x16x32_bf16 v[106:109], v[142:145], v[174:177], v[106:109]
	v_mfma_f32_16x16x32_bf16 v[94:97], v[134:137], v[184:187], v[94:97]
	v_mfma_f32_16x16x32_bf16 v[90:93], v[142:145], v[184:187], v[90:93]
	s_waitcnt lgkmcnt(0)
	v_mfma_f32_16x16x32_bf16 v[78:81], v[134:137], v[198:201], v[78:81]
	v_mfma_f32_16x16x32_bf16 v[74:77], v[142:145], v[198:201], v[74:77]
	v_mfma_f32_16x16x32_bf16 v[126:129], v[146:149], v[162:165], v[126:129]
	v_mfma_f32_16x16x32_bf16 v[122:125], v[154:157], v[162:165], v[122:125]
	v_mfma_f32_16x16x32_bf16 v[102:105], v[146:149], v[170:173], v[102:105]
	v_mfma_f32_16x16x32_bf16 v[98:101], v[154:157], v[170:173], v[98:101]
	v_mfma_f32_16x16x32_bf16 v[86:89], v[146:149], v[180:183], v[86:89]
	v_mfma_f32_16x16x32_bf16 v[82:85], v[154:157], v[180:183], v[82:85]
	v_mfma_f32_16x16x32_bf16 v[70:73], v[146:149], v[188:191], v[70:73]
	v_mfma_f32_16x16x32_bf16 v[66:69], v[154:157], v[188:191], v[66:69]
	v_mfma_f32_16x16x32_bf16 v[126:129], v[150:153], v[166:169], v[126:129]
	v_mfma_f32_16x16x32_bf16 v[122:125], v[158:161], v[166:169], v[122:125]
	v_mfma_f32_16x16x32_bf16 v[102:105], v[150:153], v[174:177], v[102:105]
	v_mfma_f32_16x16x32_bf16 v[98:101], v[158:161], v[174:177], v[98:101]
	v_mfma_f32_16x16x32_bf16 v[86:89], v[150:153], v[184:187], v[86:89]
	v_mfma_f32_16x16x32_bf16 v[82:85], v[158:161], v[184:187], v[82:85]
	v_mfma_f32_16x16x32_bf16 v[70:73], v[150:153], v[198:201], v[70:73]
	v_mfma_f32_16x16x32_bf16 v[66:69], v[158:161], v[198:201], v[66:69]
	s_setprio 0
	s_barrier
; #define PG8_STAGE(bufoff, gbase, voff) do { PG8_GLDS((const char*)(gbase), (voff)[0], ldsb + (bufoff)); PG8_GLDS((const char*)(gbase), (voff)[1], ldsb + (bufoff) + 8192u); } while (0)
; #define PG8_STAGEA(bufoff, gbase, o0, o1) do { PG8_GLDS((const char*)(gbase), (o0), ldsb + (bufoff)); PG8_GLDS((const char*)(gbase), (o1), ldsb + (bufoff) + 8192u); } while (0)
; #define PG8_STAGEA1(bufoff, gbase) do { if constexpr (Sched::GATHER) { PG8_STAGEA(bufoff, gbase, vA2, vA3); } else { PG8_STAGEA(bufoff, (gbase) + hstep, vA0, vA1); } } while (0)
; #define PG8_WAIT_VR() PG8_WAIT_V(8)
; #define PG8_WAIT_VX() do { if (relax) asm volatile("s_waitcnt vmcnt(%0)" :: "n"(8 + Epi::RELAX) : "memory"); else PG8_WAIT_V(8); } while (0)
; template <class Epi, class Sched, bool F8 = false, bool PF = false, bool I8 = false, int PID = -1>
; __device__ __forceinline__ void gemm_phase(LAS unsigned char* lds, LAS unsigned char* xlds, const int RP, const int RPB, const int nt, const Sched& S, const Epi& E, const int stagger_ticks) {
;     ...
;             PG8_LDB(B0, 0, 0); PG8_LDB(B1, 0, 1); PG8_SCHED; PG8_LDA(At, 0, 0); PG8_STAGEA1(PG8_SA(1, 1), a1);
;             if (Sched::GATHER) { if (last) { const u32x4 nv = *nslot; vA0 = nv.x; vA1 = nv.y; vA2 = nv.z; vA3 = nv.w; } }
;             PG8_WAIT_VX(); PG8_WAIT_L(0); PG8_BAR; PG8_MMA(0, 0, At, B0); PG8_MMA(0, 1, At, B1); PG8_BAR; PG8_SCHED;
;             if constexpr (Epi::BIAS_DMA) { if (t == 0 && has_next) E.bias_dma(nxt, xlds + 8192 + ((ui + 1) & 1) * Epi::BIAS_STRIDE, wid, lane); }
;             PG8_LDA(At, 0, 1); PG8_STAGE(PG8_SB(0, 0), b2, voffB); PG8_STAGE(PG8_SB(0, 1), b2 + hstepB, voffB); PG8_STAGEA(PG8_SA(0, 0), a2, vA0, vA1);
;             PG8_WAIT_VX(); PG8_WAIT_L(0); PG8_BAR; PG8_MMA(1, 0, At, B0); PG8_MMA(1, 1, At, B1); PG8_BAR; PG8_SCHED;
;             PG8_LDB(B0, 1, 0); PG8_LDB(B1, 1, 1); PG8_SCHED; PG8_LDA(At, 1, 0); PG8_STAGEA1(PG8_SA(0, 1), a2);
;             PG8_WAIT_VR(); PG8_WAIT_L(0); PG8_BAR; PG8_MMA(0, 0, At, B0); PG8_MMA(0, 1, At, B1); PG8_BAR; PG8_SCHED;
;             PG8_LDA(At, 1, 1); PG8_STAGE(PG8_SB(1, 0), b3, voffB); PG8_STAGE(PG8_SB(1, 1), b3 + hstepB, voffB); PG8_STAGEA(PG8_SA(1, 0), a3, vA0, vA1);
;             PG8_WAIT_VR(); PG8_WAIT_L(0); PG8_BAR; PG8_MMA(1, 0, At, B0); PG8_MMA(1, 1, At, B1); PG8_BAR; PG8_SCHED;
;         }
;         PROF_END(1); PROF_BEGIN(3);
;         if (wr == 0) PG8_BAR;
	s_add_u32 s36, s34, 0x80
	ds_read_b128 v[162:165], v196 offset:49152
	ds_read_b128 v[166:169], v196 offset:50176
	ds_read_b128 v[170:173], v196 offset:51200
	ds_read_b128 v[174:177], v196 offset:52224
	ds_read_b128 v[180:183], v196 offset:53248
	ds_read_b128 v[184:187], v196 offset:54272
	ds_read_b128 v[188:191], v196 offset:55296
	ds_read_b128 v[198:201], v196 offset:56320
	s_addc_u32 s37, s35, 0
	s_add_i32 s48, s47, 0x18000
	s_mov_b32 m0, s48
	s_nop 0
	global_load_lds_dwordx4 v193, s[36:37]
	s_add_i32 s48, s47, 0x1a000
	s_mov_b32 m0, s48
	s_nop 0
	global_load_lds_dwordx4 v194, s[36:37]
	s_add_u32 s34, s34, 0x4080
	s_addc_u32 s35, s35, 0
	s_add_i32 s36, s47, 0x1c000
	s_mov_b32 m0, s36
	s_nop 0
	global_load_lds_dwordx4 v193, s[34:35]
	s_add_i32 s36, s47, 0x1e000
	s_mov_b32 m0, s36
	s_nop 0
	global_load_lds_dwordx4 v194, s[34:35]
	s_add_i32 s34, s47, 0x8000
	s_mov_b32 m0, s34
	s_nop 0
	global_load_lds_dwordx4 v1, s[2:3]
	s_add_i32 s47, s47, 0xa000
	s_mov_b32 m0, s47
	s_nop 0
	global_load_lds_dwordx4 v192, s[2:3]
	s_waitcnt vmcnt(8)
	s_waitcnt lgkmcnt(0)
	s_barrier
	s_setprio 1
	s_waitcnt lgkmcnt(7)
	v_mfma_f32_16x16x32_bf16 v[50:53], v[130:133], v[162:165], v[50:53]
	v_mfma_f32_16x16x32_bf16 v[54:57], v[138:141], v[162:165], v[54:57]
	s_waitcnt lgkmcnt(5)
	v_mfma_f32_16x16x32_bf16 v[46:49], v[130:133], v[170:173], v[46:49]
	v_mfma_f32_16x16x32_bf16 v[42:45], v[138:141], v[170:173], v[42:45]
	s_waitcnt lgkmcnt(3)
	v_mfma_f32_16x16x32_bf16 v[30:33], v[130:133], v[180:183], v[30:33]
	v_mfma_f32_16x16x32_bf16 v[26:29], v[138:141], v[180:183], v[26:29]
	s_waitcnt lgkmcnt(1)
	v_mfma_f32_16x16x32_bf16 v[14:17], v[130:133], v[188:191], v[14:17]
	v_mfma_f32_16x16x32_bf16 v[10:13], v[138:141], v[188:191], v[10:13]
	v_mfma_f32_16x16x32_bf16 v[50:53], v[134:137], v[166:169], v[50:53]
	v_mfma_f32_16x16x32_bf16 v[54:57], v[142:145], v[166:169], v[54:57]
	v_mfma_f32_16x16x32_bf16 v[46:49], v[134:137], v[174:177], v[46:49]
	v_mfma_f32_16x16x32_bf16 v[42:45], v[142:145], v[174:177], v[42:45]
	v_mfma_f32_16x16x32_bf16 v[30:33], v[134:137], v[184:187], v[30:33]
	v_mfma_f32_16x16x32_bf16 v[26:29], v[142:145], v[184:187], v[26:29]
	s_waitcnt lgkmcnt(0)
	v_mfma_f32_16x16x32_bf16 v[14:17], v[134:137], v[198:201], v[14:17]
	v_mfma_f32_16x16x32_bf16 v[10:13], v[142:145], v[198:201], v[10:13]
	v_mfma_f32_16x16x32_bf16 v[58:61], v[146:149], v[162:165], v[58:61]
	v_mfma_f32_16x16x32_bf16 v[62:65], v[154:157], v[162:165], v[62:65]
	v_mfma_f32_16x16x32_bf16 v[38:41], v[146:149], v[170:173], v[38:41]
	v_mfma_f32_16x16x32_bf16 v[34:37], v[154:157], v[170:173], v[34:37]
	v_mfma_f32_16x16x32_bf16 v[22:25], v[146:149], v[180:183], v[22:25]
	v_mfma_f32_16x16x32_bf16 v[18:21], v[154:157], v[180:183], v[18:21]
	v_mfma_f32_16x16x32_bf16 v[6:9], v[146:149], v[188:191], v[6:9]
	v_mfma_f32_16x16x32_bf16 v[2:5], v[154:157], v[188:191], v[2:5]
	v_mfma_f32_16x16x32_bf16 v[58:61], v[150:153], v[166:169], v[58:61]
	v_mfma_f32_16x16x32_bf16 v[62:65], v[158:161], v[166:169], v[62:65]
	v_mfma_f32_16x16x32_bf16 v[38:41], v[150:153], v[174:177], v[38:41]
	v_mfma_f32_16x16x32_bf16 v[34:37], v[158:161], v[174:177], v[34:37]
	v_mfma_f32_16x16x32_bf16 v[22:25], v[150:153], v[184:187], v[22:25]
	v_mfma_f32_16x16x32_bf16 v[18:21], v[158:161], v[184:187], v[18:21]
	v_mfma_f32_16x16x32_bf16 v[6:9], v[150:153], v[198:201], v[6:9]
	v_mfma_f32_16x16x32_bf16 v[2:5], v[158:161], v[198:201], v[2:5]
	s_setprio 0
	s_barrier
	s_add_i32 s46, s46, 2
	s_add_u32 s20, s20, 0x100
	s_addc_u32 s45, s45, 0
	s_add_u32 s0, s0, 0x100
	s_addc_u32 s1, s1, 0
	s_cmp_gt_u32 s46, 13
	s_cbranch_scc0 .LBB0_547
	s_and_b64 vcc, exec, s[30:31]
	s_cbranch_vccz .LBB0_550
	s_barrier

; template <class Epi, class Sched, bool F8 = false, bool PF = false, bool I8 = false, int PID = -1>
; __device__ __forceinline__ void gemm_phase(LAS unsigned char* lds, LAS unsigned char* xlds, const int RP, const int RPB, const int nt, const Sched& S, const Epi& E, const int stagger_ticks) {
;     ...
;             const char* a1 = cA + (size_t)(t + 1) * kstep;
;             const char* a2 = last ? nA : cA + (size_t)(t + 2) * kstep; const char* b2 = last ? nB : cB + (size_t)(t + 2) * kstep;
;             const char* a3 = a2 + kstep; const char* b3 = b2 + kstep;
;             if constexpr (PF) { const char* pfa = (t + 4 < nt) ? cA + (size_t)(t + 4) * kstep : nA + (size_t)(t + 4 - nt) * kstep;
;                 asm volatile("s_mov_b32 m0, %2\n\ts_nop 0\n\tglobal_load_lds_dword %0, %1" :: "v"(voffP), "s"(pfa), "s"(ldsP) : "memory", "m0"); }
;             const bool relax = (Epi::RELAX > 0) && (t == 0) && epi_ran;
;             PG8_LDB(B0, 0, 0); PG8_LDB(B1, 0, 1); PG8_SCHED; PG8_LDA(At, 0, 0); PG8_STAGEA1(PG8_SA(1, 1), a1);
;             if (Sched::GATHER) { if (last) { const u32x4 nv = *nslot; vA0 = nv.x; vA1 = nv.y; vA2 = nv.z; vA3 = nv.w; } }
;             PG8_WAIT_VX(); PG8_WAIT_L(0); PG8_BAR; PG8_MMA(0, 0, At, B0); PG8_MMA(0, 1, At, B1); PG8_BAR; PG8_SCHED;
;             if constexpr (Epi::BIAS_DMA) { if (t == 0 && has_next) E.bias_dma(nxt, xlds + 8192 + ((ui + 1) & 1) * Epi::BIAS_STRIDE, wid, lane); }
;             PG8_LDA(At, 0, 1); PG8_STAGE(PG8_SB(0, 0), b2, voffB); PG8_STAGE(PG8_SB(0, 1), b2 + hstepB, voffB); PG8_STAGEA(PG8_SA(0, 0), a2, vA0, vA1);
;             PG8_WAIT_VX(); PG8_WAIT_L(0); PG8_BAR; PG8_MMA(1, 0, At, B0); PG8_MMA(1, 1, At, B1); PG8_BAR; PG8_SCHED;
;             PG8_LDB(B0, 1, 0); PG8_LDB(B1, 1, 1); PG8_SCHED; PG8_LDA(At, 1, 0); PG8_STAGEA1(PG8_SA(0, 1), a2);
;             PG8_WAIT_VR(); PG8_WAIT_L(0); PG8_BAR; PG8_MMA(0, 0, At, B0); PG8_MMA(0, 1, At, B1); PG8_BAR; PG8_SCHED;
;             PG8_LDA(At, 1, 1); PG8_STAGE(PG8_SB(1, 0), b3, voffB); PG8_STAGE(PG8_SB(1, 1), b3 + hstepB, voffB); PG8_STAGEA(PG8_SA(1, 0), a3, vA0, vA1);
;             PG8_WAIT_VR(); PG8_WAIT_L(0); PG8_BAR; PG8_MMA(1, 0, At, B0); PG8_MMA(1, 1, At, B1); PG8_BAR; PG8_SCHED;
;     ...
;         cur = nxt; cA = nA; cB = nB; ++ui;
;         has_next = has_nn; nxt = nn;
;         if (has_next) { nA = PG8_UNI64(S.Abase(nxt)); nB = PG8_UNI64(S.Bbase(nxt)); }
.LBB0_640:
	s_mov_b64 s[24:25], s[10:11]
	s_add_u32 s42, s24, 0x100
	s_mov_b64 s[4:5], s[8:9]
	s_addc_u32 s43, s25, 0
	s_mov_b64 s[8:9], s[0:1]
	s_add_u32 s0, s4, 0x20080
	s_mov_b64 s[10:11], s[2:3]
	s_mov_b32 s15, s26
	s_mov_b32 s41, s6
	s_mov_b32 s6, s14
	s_mov_b32 s26, s7
	s_addc_u32 s1, s5, 0
	s_mov_b32 s44, -2
	s_mov_b32 s45, s29
	v_add_u32_e32 v131, 0x10000, v197
	ds_read_b128 v[132:135], v131
	ds_read_b128 v[136:139], v131 offset:1024
	ds_read_b128 v[140:143], v131 offset:2048
	ds_read_b128 v[144:147], v131 offset:3072
	v_add_u32_e32 v131, 0x14000, v197
	ds_read_b128 v[148:151], v131
	ds_read_b128 v[152:155], v131 offset:1024
	ds_read_b128 v[156:159], v131 offset:2048
	ds_read_b128 v[160:163], v131 offset:3072
	s_add_u32 s2, s0, 0xfffe0080
	s_addc_u32 s3, s1, -1
	s_cmp_eq_u32 s44, 4
	s_cselect_b32 s24, s8, s2
	s_cselect_b32 s25, s9, s3
	s_cselect_b32 s4, s10, s42
	s_cselect_b32 s5, s11, s43
	s_add_u32 s2, s24, 0x80
	s_addc_u32 s3, s25, 0
	ds_read_b128 v[164:167], v198
	ds_read_b128 v[168:171], v198 offset:1024
	ds_read_b128 v[172:175], v198 offset:2048
	ds_read_b128 v[176:179], v198 offset:3072
	ds_read_b128 v[180:183], v198 offset:4096
	ds_read_b128 v[184:187], v198 offset:5120
	ds_read_b128 v[202:205], v198 offset:6144
	ds_read_b128 v[206:209], v198 offset:7168
	s_add_i32 s46, s45, 0xc000
	s_mov_b32 m0, s46
	s_nop 0
	global_load_lds_dwordx4 v1, s[0:1]
	s_add_i32 s46, s45, 0xe000
	s_mov_b32 m0, s46
	s_nop 0
	global_load_lds_dwordx4 v194, s[0:1]
	s_waitcnt vmcnt(8)
	s_waitcnt lgkmcnt(0)
	s_barrier
	s_setprio 1
	s_waitcnt lgkmcnt(6)
	v_mfma_f32_16x16x128_f8f6f4 v[114:117], v[132:139], v[164:171], 0
	v_mfma_f32_16x16x128_f8f6f4 v[118:121], v[140:147], v[164:171], 0
	s_waitcnt lgkmcnt(4)
	v_mfma_f32_16x16x128_f8f6f4 v[102:105], v[132:139], v[172:179], 0
	v_mfma_f32_16x16x128_f8f6f4 v[98:101], v[140:147], v[172:179], 0
	s_waitcnt lgkmcnt(2)
	v_mfma_f32_16x16x128_f8f6f4 v[188:191], v[132:139], v[180:187], 0
	v_mfma_f32_16x16x128_f8f6f4 v[210:213], v[140:147], v[180:187], 0
	s_waitcnt lgkmcnt(0)
	v_mfma_f32_16x16x128_f8f6f4 v[214:217], v[132:139], v[202:209], 0
	v_mfma_f32_16x16x128_f8f6f4 v[218:221], v[140:147], v[202:209], 0
	v_mfma_f32_16x16x128_f8f6f4 v[122:125], v[148:155], v[164:171], 0
	v_mfma_f32_16x16x128_f8f6f4 v[126:129], v[156:163], v[164:171], 0
	v_mfma_f32_16x16x128_f8f6f4 v[110:113], v[148:155], v[172:179], 0
	v_mfma_f32_16x16x128_f8f6f4 v[106:109], v[156:163], v[172:179], 0
	v_mfma_f32_16x16x128_f8f6f4 v[164:167], v[148:155], v[180:187], 0
	v_mfma_f32_16x16x128_f8f6f4 v[168:171], v[156:163], v[180:187], 0
	v_mfma_f32_16x16x128_f8f6f4 v[172:175], v[148:155], v[202:209], 0
	v_mfma_f32_16x16x128_f8f6f4 v[176:179], v[156:163], v[202:209], 0
	s_setprio 0
	s_barrier
	ds_read_b128 v[66:69], v198 offset:16384
	ds_read_b128 v[70:73], v198 offset:17408
	s_nop 2
	ds_read_b128 v[74:77], v198 offset:18432
	ds_read_b128 v[78:81], v198 offset:19456
	ds_read_b128 v[82:85], v198 offset:20480
	ds_read_b128 v[86:89], v198 offset:21504
	ds_read_b128 v[90:93], v198 offset:22528
	ds_read_b128 v[94:97], v198 offset:23552
	s_add_i32 s46, s45, 0x10000
	s_mov_b32 m0, s46
	s_nop 0
	global_load_lds_dwordx4 v195, s[4:5]
	s_add_i32 s46, s45, 0x12000
	s_mov_b32 m0, s46
	s_nop 0
	global_load_lds_dwordx4 v196, s[4:5]
	s_add_u32 s46, s4, 0x2000
	s_addc_u32 s47, s5, 0
	s_add_i32 s48, s45, 0x14000
	s_mov_b32 m0, s48
	s_nop 0
	global_load_lds_dwordx4 v195, s[46:47]
	s_add_i32 s48, s45, 0x16000
	s_mov_b32 m0, s48
	s_nop 0
	global_load_lds_dwordx4 v196, s[46:47]
	s_add_i32 s46, s45, 0x2000
	s_mov_b32 m0, s45
	s_nop 0
	global_load_lds_dwordx4 v1, s[24:25]
	s_nop 0
	s_mov_b32 m0, s46
	s_nop 0
	global_load_lds_dwordx4 v194, s[24:25]
	s_waitcnt vmcnt(8)
	s_waitcnt lgkmcnt(0)
	s_barrier
	s_setprio 1
	s_waitcnt lgkmcnt(6)
	v_mfma_f32_16x16x128_f8f6f4 v[54:57], v[132:139], v[66:73], 0
	v_mfma_f32_16x16x128_f8f6f4 v[50:53], v[140:147], v[66:73], 0
	s_waitcnt lgkmcnt(4)
	v_mfma_f32_16x16x128_f8f6f4 v[180:183], v[132:139], v[74:81], 0
	v_mfma_f32_16x16x128_f8f6f4 v[184:187], v[140:147], v[74:81], 0
	s_waitcnt lgkmcnt(2)
	v_mfma_f32_16x16x128_f8f6f4 v[202:205], v[132:139], v[82:89], 0
	v_mfma_f32_16x16x128_f8f6f4 v[206:209], v[140:147], v[82:89], 0
	s_waitcnt lgkmcnt(0)
	v_mfma_f32_16x16x128_f8f6f4 v[222:225], v[132:139], v[90:97], 0
	v_mfma_f32_16x16x128_f8f6f4 v[226:229], v[140:147], v[90:97], 0
	v_mfma_f32_16x16x128_f8f6f4 v[62:65], v[148:155], v[66:73], 0
	v_mfma_f32_16x16x128_f8f6f4 v[58:61], v[156:163], v[66:73], 0
	v_mfma_f32_16x16x128_f8f6f4 v[230:233], v[148:155], v[74:81], 0
	v_mfma_f32_16x16x128_f8f6f4 v[234:237], v[156:163], v[74:81], 0
	v_mfma_f32_16x16x128_f8f6f4 v[238:241], v[148:155], v[82:89], 0
	v_mfma_f32_16x16x128_f8f6f4 v[242:245], v[156:163], v[82:89], 0
	v_mfma_f32_16x16x128_f8f6f4 v[246:249], v[148:155], v[90:97], 0
	v_mfma_f32_16x16x128_f8f6f4 v[250:253], v[156:163], v[90:97], 0
	s_setprio 0
	s_barrier
	s_nop 3
	v_add_u32_e32 v14, 0x18000, v197
	v_add_u32_e32 v18, 0x1c000, v197
	ds_read_b128 v[2:5], v14
	ds_read_b128 v[6:9], v14 offset:1024
	ds_read_b128 v[10:13], v14 offset:2048
	ds_read_b128 v[14:17], v14 offset:3072
	ds_read_b128 v[132:135], v18
	ds_read_b128 v[136:139], v18 offset:1024
	ds_read_b128 v[140:143], v18 offset:2048
	ds_read_b128 v[144:147], v18 offset:3072
	ds_read_b128 v[18:21], v198 offset:32768
	ds_read_b128 v[22:25], v198 offset:33792
	ds_read_b128 v[26:29], v198 offset:34816
	ds_read_b128 v[30:33], v198 offset:35840
	ds_read_b128 v[34:37], v198 offset:36864
	ds_read_b128 v[38:41], v198 offset:37888
	ds_read_b128 v[42:45], v198 offset:38912
	ds_read_b128 v[46:49], v198 offset:39936
	s_add_u32 s24, s24, 0x20000
	s_addc_u32 s25, s25, 0
	s_add_i32 s46, s45, 0x4000
	s_mov_b32 m0, s46
	s_nop 0
	global_load_lds_dwordx4 v1, s[24:25]
	s_add_i32 s46, s45, 0x6000
	s_mov_b32 m0, s46
	s_nop 0
	global_load_lds_dwordx4 v194, s[24:25]
	s_waitcnt vmcnt(8)
	s_waitcnt lgkmcnt(0)
	s_barrier
; #define PG8_STAGE(bufoff, gbase, voff) do { PG8_GLDS((const char*)(gbase), (voff)[0], ldsb + (bufoff)); PG8_GLDS((const char*)(gbase), (voff)[1], ldsb + (bufoff) + 8192u); } while (0)
; #define PG8_STAGEA(bufoff, gbase, o0, o1) do { PG8_GLDS((const char*)(gbase), (o0), ldsb + (bufoff)); PG8_GLDS((const char*)(gbase), (o1), ldsb + (bufoff) + 8192u); } while (0)
; #define PG8_STAGEA1(bufoff, gbase) do { if constexpr (Sched::GATHER) { PG8_STAGEA(bufoff, gbase, vA2, vA3); } else { PG8_STAGEA(bufoff, (gbase) + hstep, vA0, vA1); } } while (0)
; #define PG8_WAIT_VR() PG8_WAIT_V(8)
; #define PG8_WAIT_VX() do { if (relax) asm volatile("s_waitcnt vmcnt(%0)" :: "n"(8 + Epi::RELAX) : "memory"); else PG8_WAIT_V(8); } while (0)
; #define PG8_WAIT_L(n) asm volatile("s_waitcnt lgkmcnt(" #n ")" ::: "memory")
; template <class Epi, class Sched, bool F8 = false, bool PF = false, bool I8 = false, int PID = -1>
; __device__ __forceinline__ void gemm_phase(LAS unsigned char* lds, LAS unsigned char* xlds, const int RP, const int RPB, const int nt, const Sched& S, const Epi& E, const int stagger_ticks) {
;     ...
;             PG8_LDB(B0, 0, 0); PG8_LDB(B1, 0, 1); PG8_SCHED; PG8_LDA(At, 0, 0); PG8_STAGEA1(PG8_SA(1, 1), a1);
;             if (Sched::GATHER) { if (last) { const u32x4 nv = *nslot; vA0 = nv.x; vA1 = nv.y; vA2 = nv.z; vA3 = nv.w; } }
;             PG8_WAIT_VX(); PG8_WAIT_L(0); PG8_BAR; PG8_MMA(0, 0, At, B0); PG8_MMA(0, 1, At, B1); PG8_BAR; PG8_SCHED;
;             if constexpr (Epi::BIAS_DMA) { if (t == 0 && has_next) E.bias_dma(nxt, xlds + 8192 + ((ui + 1) & 1) * Epi::BIAS_STRIDE, wid, lane); }
;             PG8_LDA(At, 0, 1); PG8_STAGE(PG8_SB(0, 0), b2, voffB); PG8_STAGE(PG8_SB(0, 1), b2 + hstepB, voffB); PG8_STAGEA(PG8_SA(0, 0), a2, vA0, vA1);
;             PG8_WAIT_VX(); PG8_WAIT_L(0); PG8_BAR; PG8_MMA(1, 0, At, B0); PG8_MMA(1, 1, At, B1); PG8_BAR; PG8_SCHED;
;             PG8_LDB(B0, 1, 0); PG8_LDB(B1, 1, 1); PG8_SCHED; PG8_LDA(At, 1, 0); PG8_STAGEA1(PG8_SA(0, 1), a2);
;             PG8_WAIT_VR(); PG8_WAIT_L(0); PG8_BAR; PG8_MMA(0, 0, At, B0); PG8_MMA(0, 1, At, B1); PG8_BAR; PG8_SCHED;
;             PG8_LDA(At, 1, 1); PG8_STAGE(PG8_SB(1, 0), b3, voffB); PG8_STAGE(PG8_SB(1, 1), b3 + hstepB, voffB); PG8_STAGEA(PG8_SA(1, 0), a3, vA0, vA1);
;             PG8_WAIT_VR(); PG8_WAIT_L(0); PG8_BAR; PG8_MMA(1, 0, At, B0); PG8_MMA(1, 1, At, B1); PG8_BAR; PG8_SCHED;
	s_setprio 1
	s_waitcnt lgkmcnt(6)
	v_mfma_f32_16x16x128_f8f6f4 v[114:117], v[2:9], v[18:25], v[114:117]
	v_mfma_f32_16x16x128_f8f6f4 v[118:121], v[10:17], v[18:25], v[118:121]
	s_waitcnt lgkmcnt(4)
	v_mfma_f32_16x16x128_f8f6f4 v[102:105], v[2:9], v[26:33], v[102:105]
	v_mfma_f32_16x16x128_f8f6f4 v[98:101], v[10:17], v[26:33], v[98:101]
	s_waitcnt lgkmcnt(2)
	v_mfma_f32_16x16x128_f8f6f4 v[86:89], v[2:9], v[34:41], v[188:191]
	v_mfma_f32_16x16x128_f8f6f4 v[82:85], v[10:17], v[34:41], v[210:213]
	s_waitcnt lgkmcnt(0)
	v_mfma_f32_16x16x128_f8f6f4 v[70:73], v[2:9], v[42:49], v[214:217]
	v_mfma_f32_16x16x128_f8f6f4 v[66:69], v[10:17], v[42:49], v[218:221]
	v_mfma_f32_16x16x128_f8f6f4 v[122:125], v[132:139], v[18:25], v[122:125]
	v_mfma_f32_16x16x128_f8f6f4 v[126:129], v[140:147], v[18:25], v[126:129]
	v_mfma_f32_16x16x128_f8f6f4 v[110:113], v[132:139], v[26:33], v[110:113]
	v_mfma_f32_16x16x128_f8f6f4 v[106:109], v[140:147], v[26:33], v[106:109]
	v_mfma_f32_16x16x128_f8f6f4 v[94:97], v[132:139], v[34:41], v[164:167]
	v_mfma_f32_16x16x128_f8f6f4 v[90:93], v[140:147], v[34:41], v[168:171]
	v_mfma_f32_16x16x128_f8f6f4 v[78:81], v[132:139], v[42:49], v[172:175]
	v_mfma_f32_16x16x128_f8f6f4 v[74:77], v[140:147], v[42:49], v[176:179]
	s_setprio 0
	s_barrier
	s_add_u32 s24, s4, 0x80
	ds_read_b128 v[26:29], v198 offset:49152
	ds_read_b128 v[30:33], v198 offset:50176
	ds_read_b128 v[148:151], v198 offset:51200
	ds_read_b128 v[152:155], v198 offset:52224
	ds_read_b128 v[156:159], v198 offset:53248
	ds_read_b128 v[160:163], v198 offset:54272
	ds_read_b128 v[164:167], v198 offset:55296
	ds_read_b128 v[168:171], v198 offset:56320
	s_addc_u32 s25, s5, 0
	s_add_i32 s46, s45, 0x18000
	s_mov_b32 m0, s46
	s_nop 0
	global_load_lds_dwordx4 v195, s[24:25]
	s_add_i32 s46, s45, 0x1a000
	s_mov_b32 m0, s46
	s_nop 0
	global_load_lds_dwordx4 v196, s[24:25]
	s_add_u32 s4, s4, 0x2080
	s_addc_u32 s5, s5, 0
	s_add_i32 s24, s45, 0x1c000
	s_mov_b32 m0, s24
	s_nop 0
	global_load_lds_dwordx4 v195, s[4:5]
	s_add_i32 s24, s45, 0x1e000
	s_mov_b32 m0, s24
	s_nop 0
	global_load_lds_dwordx4 v196, s[4:5]
	s_add_i32 s4, s45, 0x8000
	s_mov_b32 m0, s4
	s_nop 0
	global_load_lds_dwordx4 v1, s[2:3]
	s_add_i32 s45, s45, 0xa000
	s_mov_b32 m0, s45
	s_nop 0
	global_load_lds_dwordx4 v194, s[2:3]
	s_waitcnt vmcnt(8)
	s_waitcnt lgkmcnt(0)
	s_barrier
	s_setprio 1
	s_waitcnt lgkmcnt(6)
	v_mfma_f32_16x16x128_f8f6f4 v[54:57], v[2:9], v[26:33], v[54:57]
	v_mfma_f32_16x16x128_f8f6f4 v[50:53], v[10:17], v[26:33], v[50:53]
	s_waitcnt lgkmcnt(4)
	v_mfma_f32_16x16x128_f8f6f4 v[38:41], v[2:9], v[148:155], v[180:183]
	v_mfma_f32_16x16x128_f8f6f4 v[34:37], v[10:17], v[148:155], v[184:187]
	s_waitcnt lgkmcnt(2)
	v_mfma_f32_16x16x128_f8f6f4 v[22:25], v[2:9], v[156:163], v[202:205]
	v_mfma_f32_16x16x128_f8f6f4 v[18:21], v[10:17], v[156:163], v[206:209]
	s_waitcnt lgkmcnt(0)
	v_mfma_f32_16x16x128_f8f6f4 v[6:9], v[2:9], v[164:171], v[222:225]
	v_mfma_f32_16x16x128_f8f6f4 v[2:5], v[10:17], v[164:171], v[226:229]
	v_mfma_f32_16x16x128_f8f6f4 v[62:65], v[132:139], v[26:33], v[62:65]
	v_mfma_f32_16x16x128_f8f6f4 v[58:61], v[140:147], v[26:33], v[58:61]
	v_mfma_f32_16x16x128_f8f6f4 v[46:49], v[132:139], v[148:155], v[230:233]
	v_mfma_f32_16x16x128_f8f6f4 v[42:45], v[140:147], v[148:155], v[234:237]
	v_mfma_f32_16x16x128_f8f6f4 v[30:33], v[132:139], v[156:163], v[238:241]
	v_mfma_f32_16x16x128_f8f6f4 v[26:29], v[140:147], v[156:163], v[242:245]
	v_mfma_f32_16x16x128_f8f6f4 v[14:17], v[132:139], v[164:171], v[246:249]
	v_mfma_f32_16x16x128_f8f6f4 v[10:13], v[140:147], v[164:171], v[250:253]
	s_setprio 0
	s_barrier
	s_add_i32 s44, s44, 2
	s_add_u32 s42, s42, 0x100
	s_addc_u32 s43, s43, 0
	s_add_u32 s0, s0, 0x100
	s_addc_u32 s1, s1, 0
	s_cmp_gt_u32 s44, 5
.LBB0_641:
	s_mov_b32 s45, s29
	v_add_u32_e32 v131, 0x10000, v197
	ds_read_b128 v[132:135], v131
	ds_read_b128 v[136:139], v131 offset:1024
	ds_read_b128 v[140:143], v131 offset:2048
	ds_read_b128 v[144:147], v131 offset:3072
	v_add_u32_e32 v131, 0x14000, v197
	ds_read_b128 v[148:151], v131
	ds_read_b128 v[152:155], v131 offset:1024
	ds_read_b128 v[156:159], v131 offset:2048
	ds_read_b128 v[160:163], v131 offset:3072
	s_add_u32 s2, s0, 0xfffe0080
	s_addc_u32 s3, s1, -1
	s_cmp_eq_u32 s44, 4
	s_cselect_b32 s24, s8, s2
	s_cselect_b32 s25, s9, s3
	s_cselect_b32 s4, s10, s42
	s_cselect_b32 s5, s11, s43
	s_add_u32 s2, s24, 0x80
	s_addc_u32 s3, s25, 0
	ds_read_b128 v[164:167], v198
	ds_read_b128 v[168:171], v198 offset:1024
	ds_read_b128 v[172:175], v198 offset:2048
	ds_read_b128 v[176:179], v198 offset:3072
	ds_read_b128 v[180:183], v198 offset:4096
	ds_read_b128 v[184:187], v198 offset:5120
	ds_read_b128 v[202:205], v198 offset:6144
	ds_read_b128 v[206:209], v198 offset:7168
	s_add_i32 s46, s45, 0xc000
	s_mov_b32 m0, s46
	s_nop 0
	global_load_lds_dwordx4 v1, s[0:1]
	s_add_i32 s46, s45, 0xe000
	s_mov_b32 m0, s46
	s_nop 0
	global_load_lds_dwordx4 v194, s[0:1]
	s_waitcnt vmcnt(8)
	s_waitcnt lgkmcnt(0)
	s_barrier
	s_setprio 1
	s_waitcnt lgkmcnt(6)
	v_mfma_f32_16x16x128_f8f6f4 v[114:117], v[132:139], v[164:171], v[114:117]
	v_mfma_f32_16x16x128_f8f6f4 v[118:121], v[140:147], v[164:171], v[118:121]
	s_waitcnt lgkmcnt(4)
	v_mfma_f32_16x16x128_f8f6f4 v[102:105], v[132:139], v[172:179], v[102:105]
	v_mfma_f32_16x16x128_f8f6f4 v[98:101], v[140:147], v[172:179], v[98:101]
	s_waitcnt lgkmcnt(2)
	v_mfma_f32_16x16x128_f8f6f4 v[188:191], v[132:139], v[180:187], v[86:89]
	v_mfma_f32_16x16x128_f8f6f4 v[210:213], v[140:147], v[180:187], v[82:85]
	s_waitcnt lgkmcnt(0)
	v_mfma_f32_16x16x128_f8f6f4 v[214:217], v[132:139], v[202:209], v[70:73]
	v_mfma_f32_16x16x128_f8f6f4 v[218:221], v[140:147], v[202:209], v[66:69]
	v_mfma_f32_16x16x128_f8f6f4 v[122:125], v[148:155], v[164:171], v[122:125]
	v_mfma_f32_16x16x128_f8f6f4 v[126:129], v[156:163], v[164:171], v[126:129]
	v_mfma_f32_16x16x128_f8f6f4 v[110:113], v[148:155], v[172:179], v[110:113]
	v_mfma_f32_16x16x128_f8f6f4 v[106:109], v[156:163], v[172:179], v[106:109]
	v_mfma_f32_16x16x128_f8f6f4 v[164:167], v[148:155], v[180:187], v[94:97]
	v_mfma_f32_16x16x128_f8f6f4 v[168:171], v[156:163], v[180:187], v[90:93]
	v_mfma_f32_16x16x128_f8f6f4 v[172:175], v[148:155], v[202:209], v[78:81]
	v_mfma_f32_16x16x128_f8f6f4 v[176:179], v[156:163], v[202:209], v[74:77]
	s_setprio 0
	s_barrier
; #define PG8_STAGE(bufoff, gbase, voff) do { PG8_GLDS((const char*)(gbase), (voff)[0], ldsb + (bufoff)); PG8_GLDS((const char*)(gbase), (voff)[1], ldsb + (bufoff) + 8192u); } while (0)
; #define PG8_STAGEA(bufoff, gbase, o0, o1) do { PG8_GLDS((const char*)(gbase), (o0), ldsb + (bufoff)); PG8_GLDS((const char*)(gbase), (o1), ldsb + (bufoff) + 8192u); } while (0)
; #define PG8_STAGEA1(bufoff, gbase) do { if constexpr (Sched::GATHER) { PG8_STAGEA(bufoff, gbase, vA2, vA3); } else { PG8_STAGEA(bufoff, (gbase) + hstep, vA0, vA1); } } while (0)
; #define PG8_LDA(dst, b, h) do { if constexpr (F8) { _Pragma("unroll") for (int m = 0; m < 4; ++m) dst##8[m] = PG8_LD32(lds + PG8_SA(b, h) + aoff + m * 2048); } else { \
;         _Pragma("unroll") for (int m = 0; m < 4; ++m) _Pragma("unroll") for (int k = 0; k < 2; ++k) dst[m][k] = *(const LAS bf16x8*)(lds + PG8_SA(b, h) + aoff + m * 2048 + k * 1024); } } while (0)
; #define PG8_LDB(dst, b, h) do { if constexpr (F8) { _Pragma("unroll") for (int n = 0; n < 2; ++n) dst##8[n] = PG8_LD32(lds + PG8_SB(b, h) + boff + n * 2048); } else { \
;         _Pragma("unroll") for (int n = 0; n < 2; ++n) _Pragma("unroll") for (int k = 0; k < 2; ++k) dst[n][k] = *(const LAS bf16x8*)(lds + PG8_SB(b, h) + boff + n * 2048 + k * 1024); } } while (0)
; #define PG8_WAIT_VR() PG8_WAIT_V(8)
; template <class Epi, class Sched, bool F8 = false, bool PF = false, bool I8 = false, int PID = -1>
; __device__ __forceinline__ void gemm_phase(LAS unsigned char* lds, LAS unsigned char* xlds, const int RP, const int RPB, const int nt, const Sched& S, const Epi& E, const int stagger_ticks) {
;     ...
;             PG8_LDA(At, 0, 1); PG8_STAGE(PG8_SB(0, 0), b2, voffB); PG8_STAGE(PG8_SB(0, 1), b2 + hstepB, voffB); PG8_STAGEA(PG8_SA(0, 0), a2, vA0, vA1);
;             PG8_WAIT_VX(); PG8_WAIT_L(0); PG8_BAR; PG8_MMA(1, 0, At, B0); PG8_MMA(1, 1, At, B1); PG8_BAR; PG8_SCHED;
;             PG8_LDB(B0, 1, 0); PG8_LDB(B1, 1, 1); PG8_SCHED; PG8_LDA(At, 1, 0); PG8_STAGEA1(PG8_SA(0, 1), a2);
;             PG8_WAIT_VR(); PG8_WAIT_L(0); PG8_BAR; PG8_MMA(0, 0, At, B0); PG8_MMA(0, 1, At, B1); PG8_BAR; PG8_SCHED;
;             PG8_LDA(At, 1, 1); PG8_STAGE(PG8_SB(1, 0), b3, voffB); PG8_STAGE(PG8_SB(1, 1), b3 + hstepB, voffB); PG8_STAGEA(PG8_SA(1, 0), a3, vA0, vA1);
;             PG8_WAIT_VR(); PG8_WAIT_L(0); PG8_BAR; PG8_MMA(1, 0, At, B0); PG8_MMA(1, 1, At, B1); PG8_BAR; PG8_SCHED;
	ds_read_b128 v[66:69], v198 offset:16384
	ds_read_b128 v[70:73], v198 offset:17408
	s_nop 2
	ds_read_b128 v[74:77], v198 offset:18432
	ds_read_b128 v[78:81], v198 offset:19456
	ds_read_b128 v[82:85], v198 offset:20480
	ds_read_b128 v[86:89], v198 offset:21504
	ds_read_b128 v[90:93], v198 offset:22528
	ds_read_b128 v[94:97], v198 offset:23552
	s_add_i32 s46, s45, 0x10000
	s_mov_b32 m0, s46
	s_nop 0
	global_load_lds_dwordx4 v195, s[4:5]
	s_add_i32 s46, s45, 0x12000
	s_mov_b32 m0, s46
	s_nop 0
	global_load_lds_dwordx4 v196, s[4:5]
	s_add_u32 s46, s4, 0x2000
	s_addc_u32 s47, s5, 0
	s_add_i32 s48, s45, 0x14000
	s_mov_b32 m0, s48
	s_nop 0
	global_load_lds_dwordx4 v195, s[46:47]
	s_add_i32 s48, s45, 0x16000
	s_mov_b32 m0, s48
	s_nop 0
	global_load_lds_dwordx4 v196, s[46:47]
	s_add_i32 s46, s45, 0x2000
	s_mov_b32 m0, s45
	s_nop 0
	global_load_lds_dwordx4 v1, s[24:25]
	s_nop 0
	s_mov_b32 m0, s46
	s_nop 0
	global_load_lds_dwordx4 v194, s[24:25]
	s_waitcnt vmcnt(8)
	s_waitcnt lgkmcnt(0)
	s_barrier
	s_setprio 1
	s_waitcnt lgkmcnt(6)
	v_mfma_f32_16x16x128_f8f6f4 v[54:57], v[132:139], v[66:73], v[54:57]
	v_mfma_f32_16x16x128_f8f6f4 v[50:53], v[140:147], v[66:73], v[50:53]
	s_waitcnt lgkmcnt(4)
	v_mfma_f32_16x16x128_f8f6f4 v[180:183], v[132:139], v[74:81], v[38:41]
	v_mfma_f32_16x16x128_f8f6f4 v[184:187], v[140:147], v[74:81], v[34:37]
	s_waitcnt lgkmcnt(2)
	v_mfma_f32_16x16x128_f8f6f4 v[202:205], v[132:139], v[82:89], v[22:25]
	v_mfma_f32_16x16x128_f8f6f4 v[206:209], v[140:147], v[82:89], v[18:21]
	s_waitcnt lgkmcnt(0)
	v_mfma_f32_16x16x128_f8f6f4 v[222:225], v[132:139], v[90:97], v[6:9]
	v_mfma_f32_16x16x128_f8f6f4 v[226:229], v[140:147], v[90:97], v[2:5]
	v_mfma_f32_16x16x128_f8f6f4 v[62:65], v[148:155], v[66:73], v[62:65]
	v_mfma_f32_16x16x128_f8f6f4 v[58:61], v[156:163], v[66:73], v[58:61]
	v_mfma_f32_16x16x128_f8f6f4 v[230:233], v[148:155], v[74:81], v[46:49]
	v_mfma_f32_16x16x128_f8f6f4 v[234:237], v[156:163], v[74:81], v[42:45]
	v_mfma_f32_16x16x128_f8f6f4 v[238:241], v[148:155], v[82:89], v[30:33]
	v_mfma_f32_16x16x128_f8f6f4 v[242:245], v[156:163], v[82:89], v[26:29]
	v_mfma_f32_16x16x128_f8f6f4 v[246:249], v[148:155], v[90:97], v[14:17]
	v_mfma_f32_16x16x128_f8f6f4 v[250:253], v[156:163], v[90:97], v[10:13]
	s_setprio 0
	s_barrier
	s_nop 3
	v_add_u32_e32 v14, 0x18000, v197
	v_add_u32_e32 v18, 0x1c000, v197
	ds_read_b128 v[2:5], v14
	ds_read_b128 v[6:9], v14 offset:1024
	ds_read_b128 v[10:13], v14 offset:2048
	ds_read_b128 v[14:17], v14 offset:3072
	ds_read_b128 v[132:135], v18
	ds_read_b128 v[136:139], v18 offset:1024
	ds_read_b128 v[140:143], v18 offset:2048
	ds_read_b128 v[144:147], v18 offset:3072
	ds_read_b128 v[18:21], v198 offset:32768
	ds_read_b128 v[22:25], v198 offset:33792
	ds_read_b128 v[26:29], v198 offset:34816
	ds_read_b128 v[30:33], v198 offset:35840
	ds_read_b128 v[34:37], v198 offset:36864
	ds_read_b128 v[38:41], v198 offset:37888
	ds_read_b128 v[42:45], v198 offset:38912
	ds_read_b128 v[46:49], v198 offset:39936
	s_add_u32 s24, s24, 0x20000
	s_addc_u32 s25, s25, 0
	s_add_i32 s46, s45, 0x4000
	s_mov_b32 m0, s46
	s_nop 0
	global_load_lds_dwordx4 v1, s[24:25]
	s_add_i32 s46, s45, 0x6000
	s_mov_b32 m0, s46
	s_nop 0
	global_load_lds_dwordx4 v194, s[24:25]
	s_waitcnt vmcnt(8)
	s_waitcnt lgkmcnt(0)
	s_barrier
; #define PG8_STAGE(bufoff, gbase, voff) do { PG8_GLDS((const char*)(gbase), (voff)[0], ldsb + (bufoff)); PG8_GLDS((const char*)(gbase), (voff)[1], ldsb + (bufoff) + 8192u); } while (0)
; #define PG8_STAGEA(bufoff, gbase, o0, o1) do { PG8_GLDS((const char*)(gbase), (o0), ldsb + (bufoff)); PG8_GLDS((const char*)(gbase), (o1), ldsb + (bufoff) + 8192u); } while (0)
; #define PG8_STAGEA1(bufoff, gbase) do { if constexpr (Sched::GATHER) { PG8_STAGEA(bufoff, gbase, vA2, vA3); } else { PG8_STAGEA(bufoff, (gbase) + hstep, vA0, vA1); } } while (0)
; #define PG8_LDA(dst, b, h) do { if constexpr (F8) { _Pragma("unroll") for (int m = 0; m < 4; ++m) dst##8[m] = PG8_LD32(lds + PG8_SA(b, h) + aoff + m * 2048); } else { \
;         _Pragma("unroll") for (int m = 0; m < 4; ++m) _Pragma("unroll") for (int k = 0; k < 2; ++k) dst[m][k] = *(const LAS bf16x8*)(lds + PG8_SA(b, h) + aoff + m * 2048 + k * 1024); } } while (0)
; #define PG8_LDB(dst, b, h) do { if constexpr (F8) { _Pragma("unroll") for (int n = 0; n < 2; ++n) dst##8[n] = PG8_LD32(lds + PG8_SB(b, h) + boff + n * 2048); } else { \
;         _Pragma("unroll") for (int n = 0; n < 2; ++n) _Pragma("unroll") for (int k = 0; k < 2; ++k) dst[n][k] = *(const LAS bf16x8*)(lds + PG8_SB(b, h) + boff + n * 2048 + k * 1024); } } while (0)
; #define PG8_WAIT_VR() PG8_WAIT_V(8)
; #define PG8_WAIT_L(n) asm volatile("s_waitcnt lgkmcnt(" #n ")" ::: "memory")
; #define PG8_BAR __builtin_amdgcn_s_barrier()
; #define PG8_SCHED __builtin_amdgcn_sched_barrier(0)
; template <class Epi, class Sched, bool F8 = false, bool PF = false, bool I8 = false, int PID = -1>
; __device__ __forceinline__ void gemm_phase(LAS unsigned char* lds, LAS unsigned char* xlds, const int RP, const int RPB, const int nt, const Sched& S, const Epi& E, const int stagger_ticks) {
;     ...
;             PG8_LDB(B0, 1, 0); PG8_LDB(B1, 1, 1); PG8_SCHED; PG8_LDA(At, 1, 0); PG8_STAGEA1(PG8_SA(0, 1), a2);
;             PG8_WAIT_VR(); PG8_WAIT_L(0); PG8_BAR; PG8_MMA(0, 0, At, B0); PG8_MMA(0, 1, At, B1); PG8_BAR; PG8_SCHED;
;             PG8_LDA(At, 1, 1); PG8_STAGE(PG8_SB(1, 0), b3, voffB); PG8_STAGE(PG8_SB(1, 1), b3 + hstepB, voffB); PG8_STAGEA(PG8_SA(1, 0), a3, vA0, vA1);
;             PG8_WAIT_VR(); PG8_WAIT_L(0); PG8_BAR; PG8_MMA(1, 0, At, B0); PG8_MMA(1, 1, At, B1); PG8_BAR; PG8_SCHED;
;         }
;         PROF_END(1); PROF_BEGIN(3);
;         if (wr == 0) PG8_BAR;
	s_setprio 1
	s_waitcnt lgkmcnt(6)
	v_mfma_f32_16x16x128_f8f6f4 v[114:117], v[2:9], v[18:25], v[114:117]
	v_mfma_f32_16x16x128_f8f6f4 v[118:121], v[10:17], v[18:25], v[118:121]
	s_waitcnt lgkmcnt(4)
	v_mfma_f32_16x16x128_f8f6f4 v[102:105], v[2:9], v[26:33], v[102:105]
	v_mfma_f32_16x16x128_f8f6f4 v[98:101], v[10:17], v[26:33], v[98:101]
	s_waitcnt lgkmcnt(2)
	v_mfma_f32_16x16x128_f8f6f4 v[86:89], v[2:9], v[34:41], v[188:191]
	v_mfma_f32_16x16x128_f8f6f4 v[82:85], v[10:17], v[34:41], v[210:213]
	s_waitcnt lgkmcnt(0)
	v_mfma_f32_16x16x128_f8f6f4 v[70:73], v[2:9], v[42:49], v[214:217]
	v_mfma_f32_16x16x128_f8f6f4 v[66:69], v[10:17], v[42:49], v[218:221]
	v_mfma_f32_16x16x128_f8f6f4 v[122:125], v[132:139], v[18:25], v[122:125]
	v_mfma_f32_16x16x128_f8f6f4 v[126:129], v[140:147], v[18:25], v[126:129]
	v_mfma_f32_16x16x128_f8f6f4 v[110:113], v[132:139], v[26:33], v[110:113]
	v_mfma_f32_16x16x128_f8f6f4 v[106:109], v[140:147], v[26:33], v[106:109]
	v_mfma_f32_16x16x128_f8f6f4 v[94:97], v[132:139], v[34:41], v[164:167]
	v_mfma_f32_16x16x128_f8f6f4 v[90:93], v[140:147], v[34:41], v[168:171]
	v_mfma_f32_16x16x128_f8f6f4 v[78:81], v[132:139], v[42:49], v[172:175]
	v_mfma_f32_16x16x128_f8f6f4 v[74:77], v[140:147], v[42:49], v[176:179]
	s_setprio 0
	s_barrier
	s_add_u32 s24, s4, 0x80
	ds_read_b128 v[26:29], v198 offset:49152
	ds_read_b128 v[30:33], v198 offset:50176
	ds_read_b128 v[148:151], v198 offset:51200
	ds_read_b128 v[152:155], v198 offset:52224
	ds_read_b128 v[156:159], v198 offset:53248
	ds_read_b128 v[160:163], v198 offset:54272
	ds_read_b128 v[164:167], v198 offset:55296
	ds_read_b128 v[168:171], v198 offset:56320
	s_addc_u32 s25, s5, 0
	s_add_i32 s46, s45, 0x18000
	s_mov_b32 m0, s46
	s_nop 0
	global_load_lds_dwordx4 v195, s[24:25]
	s_add_i32 s46, s45, 0x1a000
	s_mov_b32 m0, s46
	s_nop 0
	global_load_lds_dwordx4 v196, s[24:25]
	s_add_u32 s4, s4, 0x2080
	s_addc_u32 s5, s5, 0
	s_add_i32 s24, s45, 0x1c000
	s_mov_b32 m0, s24
	s_nop 0
	global_load_lds_dwordx4 v195, s[4:5]
	s_add_i32 s24, s45, 0x1e000
	s_mov_b32 m0, s24
	s_nop 0
	global_load_lds_dwordx4 v196, s[4:5]
	s_add_i32 s4, s45, 0x8000
	s_mov_b32 m0, s4
	s_nop 0
	global_load_lds_dwordx4 v1, s[2:3]
	s_add_i32 s45, s45, 0xa000
	s_mov_b32 m0, s45
	s_nop 0
	global_load_lds_dwordx4 v194, s[2:3]
	s_waitcnt vmcnt(8)
	s_waitcnt lgkmcnt(0)
	s_barrier
	s_setprio 1
	s_waitcnt lgkmcnt(6)
	v_mfma_f32_16x16x128_f8f6f4 v[54:57], v[2:9], v[26:33], v[54:57]
	v_mfma_f32_16x16x128_f8f6f4 v[50:53], v[10:17], v[26:33], v[50:53]
	s_waitcnt lgkmcnt(4)
	v_mfma_f32_16x16x128_f8f6f4 v[38:41], v[2:9], v[148:155], v[180:183]
	v_mfma_f32_16x16x128_f8f6f4 v[34:37], v[10:17], v[148:155], v[184:187]
	s_waitcnt lgkmcnt(2)
	v_mfma_f32_16x16x128_f8f6f4 v[22:25], v[2:9], v[156:163], v[202:205]
	v_mfma_f32_16x16x128_f8f6f4 v[18:21], v[10:17], v[156:163], v[206:209]
	s_waitcnt lgkmcnt(0)
	v_mfma_f32_16x16x128_f8f6f4 v[6:9], v[2:9], v[164:171], v[222:225]
	v_mfma_f32_16x16x128_f8f6f4 v[2:5], v[10:17], v[164:171], v[226:229]
	v_mfma_f32_16x16x128_f8f6f4 v[62:65], v[132:139], v[26:33], v[62:65]
	v_mfma_f32_16x16x128_f8f6f4 v[58:61], v[140:147], v[26:33], v[58:61]
	v_mfma_f32_16x16x128_f8f6f4 v[46:49], v[132:139], v[148:155], v[230:233]
	v_mfma_f32_16x16x128_f8f6f4 v[42:45], v[140:147], v[148:155], v[234:237]
	v_mfma_f32_16x16x128_f8f6f4 v[30:33], v[132:139], v[156:163], v[238:241]
	v_mfma_f32_16x16x128_f8f6f4 v[26:29], v[140:147], v[156:163], v[242:245]
	v_mfma_f32_16x16x128_f8f6f4 v[14:17], v[132:139], v[164:171], v[246:249]
	v_mfma_f32_16x16x128_f8f6f4 v[10:13], v[140:147], v[164:171], v[250:253]
	s_setprio 0
	s_barrier
	s_add_i32 s44, s44, 2
	s_add_u32 s42, s42, 0x100
	s_addc_u32 s43, s43, 0
	s_add_u32 s0, s0, 0x100
	s_addc_u32 s1, s1, 0
	s_cmp_gt_u32 s44, 5
	s_cbranch_scc0 .LBB0_641
	s_and_b64 vcc, exec, s[22:23]
	s_cbranch_vccz .LBB0_644
	s_barrier

; template <class Epi, class Sched, bool F8 = false, bool PF = false, bool I8 = false, int PID = -1>
; __device__ __forceinline__ void gemm_phase(LAS unsigned char* lds, LAS unsigned char* xlds, const int RP, const int RPB, const int nt, const Sched& S, const Epi& E, const int stagger_ticks) {
;     ...
;             const char* a1 = cA + (size_t)(t + 1) * kstep;
;             const char* a2 = last ? nA : cA + (size_t)(t + 2) * kstep; const char* b2 = last ? nB : cB + (size_t)(t + 2) * kstep;
;             const char* a3 = a2 + kstep; const char* b3 = b2 + kstep;
;             if constexpr (PF) { const char* pfa = (t + 4 < nt) ? cA + (size_t)(t + 4) * kstep : nA + (size_t)(t + 4 - nt) * kstep;
;                 asm volatile("s_mov_b32 m0, %2\n\ts_nop 0\n\tglobal_load_lds_dword %0, %1" :: "v"(voffP), "s"(pfa), "s"(ldsP) : "memory", "m0"); }
;             const bool relax = (Epi::RELAX > 0) && (t == 0) && epi_ran;
;             PG8_LDB(B0, 0, 0); PG8_LDB(B1, 0, 1); PG8_SCHED; PG8_LDA(At, 0, 0); PG8_STAGEA1(PG8_SA(1, 1), a1);
;             if (Sched::GATHER) { if (last) { const u32x4 nv = *nslot; vA0 = nv.x; vA1 = nv.y; vA2 = nv.z; vA3 = nv.w; } }
;             PG8_WAIT_VX(); PG8_WAIT_L(0); PG8_BAR; PG8_MMA(0, 0, At, B0); PG8_MMA(0, 1, At, B1); PG8_BAR; PG8_SCHED;
;             if constexpr (Epi::BIAS_DMA) { if (t == 0 && has_next) E.bias_dma(nxt, xlds + 8192 + ((ui + 1) & 1) * Epi::BIAS_STRIDE, wid, lane); }
;             PG8_LDA(At, 0, 1); PG8_STAGE(PG8_SB(0, 0), b2, voffB); PG8_STAGE(PG8_SB(0, 1), b2 + hstepB, voffB); PG8_STAGEA(PG8_SA(0, 0), a2, vA0, vA1);
;             PG8_WAIT_VX(); PG8_WAIT_L(0); PG8_BAR; PG8_MMA(1, 0, At, B0); PG8_MMA(1, 1, At, B1); PG8_BAR; PG8_SCHED;
;             PG8_LDB(B0, 1, 0); PG8_LDB(B1, 1, 1); PG8_SCHED; PG8_LDA(At, 1, 0); PG8_STAGEA1(PG8_SA(0, 1), a2);
;             PG8_WAIT_VR(); PG8_WAIT_L(0); PG8_BAR; PG8_MMA(0, 0, At, B0); PG8_MMA(0, 1, At, B1); PG8_BAR; PG8_SCHED;
;             PG8_LDA(At, 1, 1); PG8_STAGE(PG8_SB(1, 0), b3, voffB); PG8_STAGE(PG8_SB(1, 1), b3 + hstepB, voffB); PG8_STAGEA(PG8_SA(1, 0), a3, vA0, vA1);
;             PG8_WAIT_VR(); PG8_WAIT_L(0); PG8_BAR; PG8_MMA(1, 0, At, B0); PG8_MMA(1, 1, At, B1); PG8_BAR; PG8_SCHED;
;     ...
;         cur = nxt; cA = nA; cB = nB; ++ui;
;         has_next = has_nn; nxt = nn;
;         if (has_next) { nA = PG8_UNI64(S.Abase(nxt)); nB = PG8_UNI64(S.Bbase(nxt)); }
.LBB0_752:
	s_mov_b64 s[30:31], s[8:9]
	s_add_u32 s43, s30, 0x100
	s_mov_b64 s[28:29], s[6:7]
	s_addc_u32 s44, s31, 0
	s_mov_b64 s[6:7], s[0:1]
	s_add_u32 s0, s28, 0x20080
	s_mov_b64 s[8:9], s[2:3]
	s_mov_b32 s13, s27
	s_mov_b32 s14, s4
	s_mov_b32 s4, s12
	s_mov_b32 s27, s5
	s_addc_u32 s1, s29, 0
	s_mov_b32 s45, -2
	s_mov_b32 s46, s38
	v_add_u32_e32 v142, 0x10000, v177
	v_add_u32_e32 v155, 0x14000, v177
	ds_read_b128 v[130:133], v142
	ds_read_b128 v[134:137], v142 offset:1024
	ds_read_b128 v[138:141], v142 offset:2048
	ds_read_b128 v[142:145], v142 offset:3072
	ds_read_b128 v[146:149], v155
	ds_read_b128 v[150:153], v155 offset:1024
	ds_read_b128 v[156:159], v155 offset:2048
	ds_read_b128 v[160:163], v155 offset:3072
	s_add_u32 s2, s0, 0xfffe0080
	s_addc_u32 s3, s1, -1
	s_cmp_eq_u32 s45, 4
	s_cselect_b32 s30, s6, s2
	s_cselect_b32 s31, s7, s3
	s_cselect_b32 s28, s8, s43
	s_cselect_b32 s29, s9, s44
	s_add_u32 s2, s30, 0x80
	s_addc_u32 s3, s31, 0
	ds_read_b128 v[164:167], v178
	ds_read_b128 v[168:171], v178 offset:1024
	ds_read_b128 v[180:183], v178 offset:2048
	ds_read_b128 v[184:187], v178 offset:3072
	ds_read_b128 v[188:191], v178 offset:4096
	ds_read_b128 v[192:195], v178 offset:5120
	ds_read_b128 v[196:199], v178 offset:6144
	ds_read_b128 v[200:203], v178 offset:7168
	s_add_i32 s47, s46, 0xc000
	s_mov_b32 m0, s47
	s_nop 0
	global_load_lds_dwordx4 v1, s[0:1]
	s_add_i32 s47, s46, 0xe000
	s_mov_b32 m0, s47
	s_nop 0
	global_load_lds_dwordx4 v174, s[0:1]
	s_waitcnt vmcnt(8)
	s_waitcnt lgkmcnt(0)
	s_barrier
	s_setprio 1
	s_waitcnt lgkmcnt(6)
	v_mfma_f32_16x16x128_f8f6f4 v[114:117], v[130:137], v[164:171], 0
	v_mfma_f32_16x16x128_f8f6f4 v[118:121], v[138:145], v[164:171], 0
	s_waitcnt lgkmcnt(4)
	v_mfma_f32_16x16x128_f8f6f4 v[110:113], v[130:137], v[180:187], 0
	v_mfma_f32_16x16x128_f8f6f4 v[106:109], v[138:145], v[180:187], 0
	s_waitcnt lgkmcnt(2)
	v_mfma_f32_16x16x128_f8f6f4 v[204:207], v[130:137], v[188:195], 0
	v_mfma_f32_16x16x128_f8f6f4 v[208:211], v[138:145], v[188:195], 0
	s_waitcnt lgkmcnt(0)
	v_mfma_f32_16x16x128_f8f6f4 v[212:215], v[130:137], v[196:203], 0
	v_mfma_f32_16x16x128_f8f6f4 v[216:219], v[138:145], v[196:203], 0
	v_mfma_f32_16x16x128_f8f6f4 v[122:125], v[146:153], v[164:171], 0
	v_mfma_f32_16x16x128_f8f6f4 v[126:129], v[156:163], v[164:171], 0
	v_mfma_f32_16x16x128_f8f6f4 v[102:105], v[146:153], v[180:187], 0
	v_mfma_f32_16x16x128_f8f6f4 v[98:101], v[156:163], v[180:187], 0
	v_mfma_f32_16x16x128_f8f6f4 v[164:167], v[146:153], v[188:195], 0
	v_mfma_f32_16x16x128_f8f6f4 v[168:171], v[156:163], v[188:195], 0
	v_mfma_f32_16x16x128_f8f6f4 v[180:183], v[146:153], v[196:203], 0
	v_mfma_f32_16x16x128_f8f6f4 v[184:187], v[156:163], v[196:203], 0
	s_setprio 0
	s_barrier
	s_nop 4
	ds_read_b128 v[66:69], v178 offset:16384
	ds_read_b128 v[70:73], v178 offset:17408
	ds_read_b128 v[74:77], v178 offset:18432
	ds_read_b128 v[78:81], v178 offset:19456
	ds_read_b128 v[82:85], v178 offset:20480
	ds_read_b128 v[86:89], v178 offset:21504
	ds_read_b128 v[90:93], v178 offset:22528
	ds_read_b128 v[94:97], v178 offset:23552
	s_add_i32 s47, s46, 0x10000
	s_mov_b32 m0, s47
	s_nop 0
	global_load_lds_dwordx4 v175, s[28:29]
	s_add_i32 s47, s46, 0x12000
	s_mov_b32 m0, s47
	s_nop 0
	global_load_lds_dwordx4 v176, s[28:29]
	s_add_u32 s48, s28, 0x2000
	s_addc_u32 s49, s29, 0
	s_add_i32 s47, s46, 0x14000
	s_mov_b32 m0, s47
	s_nop 0
	global_load_lds_dwordx4 v175, s[48:49]
	s_add_i32 s47, s46, 0x16000
	s_mov_b32 m0, s47
	s_nop 0
	global_load_lds_dwordx4 v176, s[48:49]
	s_add_i32 s47, s46, 0x2000
	s_mov_b32 m0, s46
	s_nop 0
	global_load_lds_dwordx4 v1, s[30:31]
	s_nop 0
	s_mov_b32 m0, s47
	s_nop 0
	global_load_lds_dwordx4 v174, s[30:31]
	s_waitcnt vmcnt(8)
	s_waitcnt lgkmcnt(0)
	s_barrier
	s_setprio 1
	s_waitcnt lgkmcnt(6)
	v_mfma_f32_16x16x128_f8f6f4 v[62:65], v[130:137], v[66:73], 0
	v_mfma_f32_16x16x128_f8f6f4 v[58:61], v[138:145], v[66:73], 0
	s_waitcnt lgkmcnt(4)
	v_mfma_f32_16x16x128_f8f6f4 v[188:191], v[130:137], v[74:81], 0
	v_mfma_f32_16x16x128_f8f6f4 v[192:195], v[138:145], v[74:81], 0
	s_waitcnt lgkmcnt(2)
	v_mfma_f32_16x16x128_f8f6f4 v[196:199], v[130:137], v[82:89], 0
	v_mfma_f32_16x16x128_f8f6f4 v[200:203], v[138:145], v[82:89], 0
	s_waitcnt lgkmcnt(0)
	v_mfma_f32_16x16x128_f8f6f4 v[220:223], v[130:137], v[90:97], 0
	v_mfma_f32_16x16x128_f8f6f4 v[224:227], v[138:145], v[90:97], 0
	v_mfma_f32_16x16x128_f8f6f4 v[54:57], v[146:153], v[66:73], 0
	v_mfma_f32_16x16x128_f8f6f4 v[50:53], v[156:163], v[66:73], 0
	v_mfma_f32_16x16x128_f8f6f4 v[228:231], v[146:153], v[74:81], 0
	v_mfma_f32_16x16x128_f8f6f4 v[232:235], v[156:163], v[74:81], 0
	v_mfma_f32_16x16x128_f8f6f4 v[236:239], v[146:153], v[82:89], 0
	v_mfma_f32_16x16x128_f8f6f4 v[240:243], v[156:163], v[82:89], 0
	v_mfma_f32_16x16x128_f8f6f4 v[244:247], v[146:153], v[90:97], 0
	v_mfma_f32_16x16x128_f8f6f4 v[248:251], v[156:163], v[90:97], 0
	s_setprio 0
	s_barrier
	v_add_u32_e32 v10, 0x18000, v177
	s_nop 3
	ds_read_b128 v[2:5], v10
	ds_read_b128 v[6:9], v10 offset:1024
	ds_read_b128 v[18:21], v10 offset:2048
	ds_read_b128 v[22:25], v10 offset:3072
	v_add_u32_e32 v10, 0x1c000, v177
	ds_read_b128 v[130:133], v10
	ds_read_b128 v[134:137], v10 offset:1024
	ds_read_b128 v[138:141], v10 offset:2048
	ds_read_b128 v[142:145], v10 offset:3072
	ds_read_b128 v[10:13], v178 offset:32768
	ds_read_b128 v[14:17], v178 offset:33792
	ds_read_b128 v[26:29], v178 offset:34816
	ds_read_b128 v[30:33], v178 offset:35840
	ds_read_b128 v[34:37], v178 offset:36864
	ds_read_b128 v[38:41], v178 offset:37888
	ds_read_b128 v[42:45], v178 offset:38912
	ds_read_b128 v[46:49], v178 offset:39936
	s_add_u32 s30, s30, 0x20000
	s_addc_u32 s31, s31, 0
	s_add_i32 s47, s46, 0x4000
	s_mov_b32 m0, s47
	s_nop 0
	global_load_lds_dwordx4 v1, s[30:31]
	s_add_i32 s47, s46, 0x6000
	s_mov_b32 m0, s47
	s_nop 0
	global_load_lds_dwordx4 v174, s[30:31]
	s_waitcnt vmcnt(8)
	s_waitcnt lgkmcnt(0)
	s_barrier
; #define PG8_STAGE(bufoff, gbase, voff) do { PG8_GLDS((const char*)(gbase), (voff)[0], ldsb + (bufoff)); PG8_GLDS((const char*)(gbase), (voff)[1], ldsb + (bufoff) + 8192u); } while (0)
; #define PG8_STAGEA(bufoff, gbase, o0, o1) do { PG8_GLDS((const char*)(gbase), (o0), ldsb + (bufoff)); PG8_GLDS((const char*)(gbase), (o1), ldsb + (bufoff) + 8192u); } while (0)
; #define PG8_STAGEA1(bufoff, gbase) do { if constexpr (Sched::GATHER) { PG8_STAGEA(bufoff, gbase, vA2, vA3); } else { PG8_STAGEA(bufoff, (gbase) + hstep, vA0, vA1); } } while (0)
; #define PG8_WAIT_VR() PG8_WAIT_V(8)
; #define PG8_WAIT_VX() do { if (relax) asm volatile("s_waitcnt vmcnt(%0)" :: "n"(8 + Epi::RELAX) : "memory"); else PG8_WAIT_V(8); } while (0)
; #define PG8_WAIT_L(n) asm volatile("s_waitcnt lgkmcnt(" #n ")" ::: "memory")
; template <class Epi, class Sched, bool F8 = false, bool PF = false, bool I8 = false, int PID = -1>
; __device__ __forceinline__ void gemm_phase(LAS unsigned char* lds, LAS unsigned char* xlds, const int RP, const int RPB, const int nt, const Sched& S, const Epi& E, const int stagger_ticks) {
;     ...
;             PG8_LDB(B0, 0, 0); PG8_LDB(B1, 0, 1); PG8_SCHED; PG8_LDA(At, 0, 0); PG8_STAGEA1(PG8_SA(1, 1), a1);
;             if (Sched::GATHER) { if (last) { const u32x4 nv = *nslot; vA0 = nv.x; vA1 = nv.y; vA2 = nv.z; vA3 = nv.w; } }
;             PG8_WAIT_VX(); PG8_WAIT_L(0); PG8_BAR; PG8_MMA(0, 0, At, B0); PG8_MMA(0, 1, At, B1); PG8_BAR; PG8_SCHED;
;             if constexpr (Epi::BIAS_DMA) { if (t == 0 && has_next) E.bias_dma(nxt, xlds + 8192 + ((ui + 1) & 1) * Epi::BIAS_STRIDE, wid, lane); }
;             PG8_LDA(At, 0, 1); PG8_STAGE(PG8_SB(0, 0), b2, voffB); PG8_STAGE(PG8_SB(0, 1), b2 + hstepB, voffB); PG8_STAGEA(PG8_SA(0, 0), a2, vA0, vA1);
;             PG8_WAIT_VX(); PG8_WAIT_L(0); PG8_BAR; PG8_MMA(1, 0, At, B0); PG8_MMA(1, 1, At, B1); PG8_BAR; PG8_SCHED;
;             PG8_LDB(B0, 1, 0); PG8_LDB(B1, 1, 1); PG8_SCHED; PG8_LDA(At, 1, 0); PG8_STAGEA1(PG8_SA(0, 1), a2);
;             PG8_WAIT_VR(); PG8_WAIT_L(0); PG8_BAR; PG8_MMA(0, 0, At, B0); PG8_MMA(0, 1, At, B1); PG8_BAR; PG8_SCHED;
;             PG8_LDA(At, 1, 1); PG8_STAGE(PG8_SB(1, 0), b3, voffB); PG8_STAGE(PG8_SB(1, 1), b3 + hstepB, voffB); PG8_STAGEA(PG8_SA(1, 0), a3, vA0, vA1);
;             PG8_WAIT_VR(); PG8_WAIT_L(0); PG8_BAR; PG8_MMA(1, 0, At, B0); PG8_MMA(1, 1, At, B1); PG8_BAR; PG8_SCHED;
	s_setprio 1
	s_waitcnt lgkmcnt(6)
	v_mfma_f32_16x16x128_f8f6f4 v[114:117], v[2:9], v[10:17], v[114:117]
	v_mfma_f32_16x16x128_f8f6f4 v[118:121], v[18:25], v[10:17], v[118:121]
	s_waitcnt lgkmcnt(4)
	v_mfma_f32_16x16x128_f8f6f4 v[110:113], v[2:9], v[26:33], v[110:113]
	v_mfma_f32_16x16x128_f8f6f4 v[106:109], v[18:25], v[26:33], v[106:109]
	s_waitcnt lgkmcnt(2)
	v_mfma_f32_16x16x128_f8f6f4 v[94:97], v[2:9], v[34:41], v[204:207]
	v_mfma_f32_16x16x128_f8f6f4 v[90:93], v[18:25], v[34:41], v[208:211]
	s_waitcnt lgkmcnt(0)
	v_mfma_f32_16x16x128_f8f6f4 v[78:81], v[2:9], v[42:49], v[212:215]
	v_mfma_f32_16x16x128_f8f6f4 v[74:77], v[18:25], v[42:49], v[216:219]
	v_mfma_f32_16x16x128_f8f6f4 v[122:125], v[130:137], v[10:17], v[122:125]
	v_mfma_f32_16x16x128_f8f6f4 v[126:129], v[138:145], v[10:17], v[126:129]
	v_mfma_f32_16x16x128_f8f6f4 v[102:105], v[130:137], v[26:33], v[102:105]
	v_mfma_f32_16x16x128_f8f6f4 v[98:101], v[138:145], v[26:33], v[98:101]
	v_mfma_f32_16x16x128_f8f6f4 v[86:89], v[130:137], v[34:41], v[164:167]
	v_mfma_f32_16x16x128_f8f6f4 v[82:85], v[138:145], v[34:41], v[168:171]
	v_mfma_f32_16x16x128_f8f6f4 v[70:73], v[130:137], v[42:49], v[180:183]
	v_mfma_f32_16x16x128_f8f6f4 v[66:69], v[138:145], v[42:49], v[184:187]
	s_setprio 0
	s_barrier
	s_add_u32 s30, s28, 0x80
	ds_read_b128 v[34:37], v178 offset:49152
	ds_read_b128 v[38:41], v178 offset:50176
	ds_read_b128 v[146:149], v178 offset:51200
	ds_read_b128 v[150:153], v178 offset:52224
	ds_read_b128 v[156:159], v178 offset:53248
	ds_read_b128 v[160:163], v178 offset:54272
	ds_read_b128 v[164:167], v178 offset:55296
	ds_read_b128 v[168:171], v178 offset:56320
	s_addc_u32 s31, s29, 0
	s_add_i32 s47, s46, 0x18000
	s_mov_b32 m0, s47
	s_nop 0
	global_load_lds_dwordx4 v175, s[30:31]
	s_add_i32 s47, s46, 0x1a000
	s_mov_b32 m0, s47
	s_nop 0
	global_load_lds_dwordx4 v176, s[30:31]
	s_add_u32 s28, s28, 0x2080
	s_addc_u32 s29, s29, 0
	s_add_i32 s30, s46, 0x1c000
	s_mov_b32 m0, s30
	s_nop 0
	global_load_lds_dwordx4 v175, s[28:29]
	s_add_i32 s30, s46, 0x1e000
	s_mov_b32 m0, s30
	s_nop 0
	global_load_lds_dwordx4 v176, s[28:29]
	s_add_i32 s28, s46, 0x8000
	s_mov_b32 m0, s28
	s_nop 0
	global_load_lds_dwordx4 v1, s[2:3]
	s_add_i32 s46, s46, 0xa000
	s_mov_b32 m0, s46
	s_nop 0
	global_load_lds_dwordx4 v174, s[2:3]
	s_waitcnt vmcnt(8)
	s_waitcnt lgkmcnt(0)
	s_barrier
	s_setprio 1
	s_waitcnt lgkmcnt(6)
	v_mfma_f32_16x16x128_f8f6f4 v[62:65], v[2:9], v[34:41], v[62:65]
	v_mfma_f32_16x16x128_f8f6f4 v[58:61], v[18:25], v[34:41], v[58:61]
	s_waitcnt lgkmcnt(4)
	v_mfma_f32_16x16x128_f8f6f4 v[46:49], v[2:9], v[146:153], v[188:191]
	v_mfma_f32_16x16x128_f8f6f4 v[42:45], v[18:25], v[146:153], v[192:195]
	s_waitcnt lgkmcnt(2)
	v_mfma_f32_16x16x128_f8f6f4 v[30:33], v[2:9], v[156:163], v[196:199]
	v_mfma_f32_16x16x128_f8f6f4 v[26:29], v[18:25], v[156:163], v[200:203]
	s_waitcnt lgkmcnt(0)
	v_mfma_f32_16x16x128_f8f6f4 v[14:17], v[2:9], v[164:171], v[220:223]
	v_mfma_f32_16x16x128_f8f6f4 v[10:13], v[18:25], v[164:171], v[224:227]
	v_mfma_f32_16x16x128_f8f6f4 v[54:57], v[130:137], v[34:41], v[54:57]
	v_mfma_f32_16x16x128_f8f6f4 v[50:53], v[138:145], v[34:41], v[50:53]
	v_mfma_f32_16x16x128_f8f6f4 v[38:41], v[130:137], v[146:153], v[228:231]
	v_mfma_f32_16x16x128_f8f6f4 v[34:37], v[138:145], v[146:153], v[232:235]
	v_mfma_f32_16x16x128_f8f6f4 v[22:25], v[130:137], v[156:163], v[236:239]
	v_mfma_f32_16x16x128_f8f6f4 v[18:21], v[138:145], v[156:163], v[240:243]
	v_mfma_f32_16x16x128_f8f6f4 v[6:9], v[130:137], v[164:171], v[244:247]
	v_mfma_f32_16x16x128_f8f6f4 v[2:5], v[138:145], v[164:171], v[248:251]
	s_setprio 0
	s_barrier
	s_add_i32 s45, s45, 2
	s_add_u32 s43, s43, 0x100
	s_addc_u32 s44, s44, 0
	s_add_u32 s0, s0, 0x100
	s_addc_u32 s1, s1, 0
	s_cmp_gt_u32 s45, 5
.LBB0_753:
	s_mov_b32 s46, s38
	v_add_u32_e32 v142, 0x10000, v177
	v_add_u32_e32 v155, 0x14000, v177
	ds_read_b128 v[130:133], v142
	ds_read_b128 v[134:137], v142 offset:1024
	ds_read_b128 v[138:141], v142 offset:2048
	ds_read_b128 v[142:145], v142 offset:3072
	ds_read_b128 v[146:149], v155
	ds_read_b128 v[150:153], v155 offset:1024
	ds_read_b128 v[156:159], v155 offset:2048
	ds_read_b128 v[160:163], v155 offset:3072
	s_add_u32 s2, s0, 0xfffe0080
	s_addc_u32 s3, s1, -1
	s_cmp_eq_u32 s45, 4
	s_cselect_b32 s30, s6, s2
	s_cselect_b32 s31, s7, s3
	s_cselect_b32 s28, s8, s43
	s_cselect_b32 s29, s9, s44
	s_add_u32 s2, s30, 0x80
	s_addc_u32 s3, s31, 0
	ds_read_b128 v[164:167], v178
	ds_read_b128 v[168:171], v178 offset:1024
	ds_read_b128 v[180:183], v178 offset:2048
	ds_read_b128 v[184:187], v178 offset:3072
	ds_read_b128 v[188:191], v178 offset:4096
	ds_read_b128 v[192:195], v178 offset:5120
	ds_read_b128 v[196:199], v178 offset:6144
	ds_read_b128 v[200:203], v178 offset:7168
	s_add_i32 s47, s46, 0xc000
	s_mov_b32 m0, s47
	s_nop 0
	global_load_lds_dwordx4 v1, s[0:1]
	s_add_i32 s47, s46, 0xe000
	s_mov_b32 m0, s47
	s_nop 0
	global_load_lds_dwordx4 v174, s[0:1]
	s_waitcnt vmcnt(8)
	s_waitcnt lgkmcnt(0)
	s_barrier
	s_setprio 1
	s_waitcnt lgkmcnt(6)
	v_mfma_f32_16x16x128_f8f6f4 v[114:117], v[130:137], v[164:171], v[114:117]
	v_mfma_f32_16x16x128_f8f6f4 v[118:121], v[138:145], v[164:171], v[118:121]
	s_waitcnt lgkmcnt(4)
	v_mfma_f32_16x16x128_f8f6f4 v[110:113], v[130:137], v[180:187], v[110:113]
	v_mfma_f32_16x16x128_f8f6f4 v[106:109], v[138:145], v[180:187], v[106:109]
	s_waitcnt lgkmcnt(2)
	v_mfma_f32_16x16x128_f8f6f4 v[204:207], v[130:137], v[188:195], v[94:97]
	v_mfma_f32_16x16x128_f8f6f4 v[208:211], v[138:145], v[188:195], v[90:93]
	s_waitcnt lgkmcnt(0)
	v_mfma_f32_16x16x128_f8f6f4 v[212:215], v[130:137], v[196:203], v[78:81]
	v_mfma_f32_16x16x128_f8f6f4 v[216:219], v[138:145], v[196:203], v[74:77]
	v_mfma_f32_16x16x128_f8f6f4 v[122:125], v[146:153], v[164:171], v[122:125]
	v_mfma_f32_16x16x128_f8f6f4 v[126:129], v[156:163], v[164:171], v[126:129]
	v_mfma_f32_16x16x128_f8f6f4 v[102:105], v[146:153], v[180:187], v[102:105]
	v_mfma_f32_16x16x128_f8f6f4 v[98:101], v[156:163], v[180:187], v[98:101]
	v_mfma_f32_16x16x128_f8f6f4 v[164:167], v[146:153], v[188:195], v[86:89]
	v_mfma_f32_16x16x128_f8f6f4 v[168:171], v[156:163], v[188:195], v[82:85]
	v_mfma_f32_16x16x128_f8f6f4 v[180:183], v[146:153], v[196:203], v[70:73]
	v_mfma_f32_16x16x128_f8f6f4 v[184:187], v[156:163], v[196:203], v[66:69]
	s_setprio 0
	s_barrier
; #define PG8_STAGE(bufoff, gbase, voff) do { PG8_GLDS((const char*)(gbase), (voff)[0], ldsb + (bufoff)); PG8_GLDS((const char*)(gbase), (voff)[1], ldsb + (bufoff) + 8192u); } while (0)
; #define PG8_STAGEA(bufoff, gbase, o0, o1) do { PG8_GLDS((const char*)(gbase), (o0), ldsb + (bufoff)); PG8_GLDS((const char*)(gbase), (o1), ldsb + (bufoff) + 8192u); } while (0)
; #define PG8_STAGEA1(bufoff, gbase) do { if constexpr (Sched::GATHER) { PG8_STAGEA(bufoff, gbase, vA2, vA3); } else { PG8_STAGEA(bufoff, (gbase) + hstep, vA0, vA1); } } while (0)
; #define PG8_LDA(dst, b, h) do { if constexpr (F8) { _Pragma("unroll") for (int m = 0; m < 4; ++m) dst##8[m] = PG8_LD32(lds + PG8_SA(b, h) + aoff + m * 2048); } else { \
;         _Pragma("unroll") for (int m = 0; m < 4; ++m) _Pragma("unroll") for (int k = 0; k < 2; ++k) dst[m][k] = *(const LAS bf16x8*)(lds + PG8_SA(b, h) + aoff + m * 2048 + k * 1024); } } while (0)
; #define PG8_LDB(dst, b, h) do { if constexpr (F8) { _Pragma("unroll") for (int n = 0; n < 2; ++n) dst##8[n] = PG8_LD32(lds + PG8_SB(b, h) + boff + n * 2048); } else { \
;         _Pragma("unroll") for (int n = 0; n < 2; ++n) _Pragma("unroll") for (int k = 0; k < 2; ++k) dst[n][k] = *(const LAS bf16x8*)(lds + PG8_SB(b, h) + boff + n * 2048 + k * 1024); } } while (0)
; #define PG8_WAIT_VR() PG8_WAIT_V(8)
; template <class Epi, class Sched, bool F8 = false, bool PF = false, bool I8 = false, int PID = -1>
; __device__ __forceinline__ void gemm_phase(LAS unsigned char* lds, LAS unsigned char* xlds, const int RP, const int RPB, const int nt, const Sched& S, const Epi& E, const int stagger_ticks) {
;     ...
;             PG8_LDA(At, 0, 1); PG8_STAGE(PG8_SB(0, 0), b2, voffB); PG8_STAGE(PG8_SB(0, 1), b2 + hstepB, voffB); PG8_STAGEA(PG8_SA(0, 0), a2, vA0, vA1);
;             PG8_WAIT_VX(); PG8_WAIT_L(0); PG8_BAR; PG8_MMA(1, 0, At, B0); PG8_MMA(1, 1, At, B1); PG8_BAR; PG8_SCHED;
;             PG8_LDB(B0, 1, 0); PG8_LDB(B1, 1, 1); PG8_SCHED; PG8_LDA(At, 1, 0); PG8_STAGEA1(PG8_SA(0, 1), a2);
;             PG8_WAIT_VR(); PG8_WAIT_L(0); PG8_BAR; PG8_MMA(0, 0, At, B0); PG8_MMA(0, 1, At, B1); PG8_BAR; PG8_SCHED;
;             PG8_LDA(At, 1, 1); PG8_STAGE(PG8_SB(1, 0), b3, voffB); PG8_STAGE(PG8_SB(1, 1), b3 + hstepB, voffB); PG8_STAGEA(PG8_SA(1, 0), a3, vA0, vA1);
;             PG8_WAIT_VR(); PG8_WAIT_L(0); PG8_BAR; PG8_MMA(1, 0, At, B0); PG8_MMA(1, 1, At, B1); PG8_BAR; PG8_SCHED;
	s_nop 4
	ds_read_b128 v[66:69], v178 offset:16384
	ds_read_b128 v[70:73], v178 offset:17408
	ds_read_b128 v[74:77], v178 offset:18432
	ds_read_b128 v[78:81], v178 offset:19456
	ds_read_b128 v[82:85], v178 offset:20480
	ds_read_b128 v[86:89], v178 offset:21504
	ds_read_b128 v[90:93], v178 offset:22528
	ds_read_b128 v[94:97], v178 offset:23552
	s_add_i32 s47, s46, 0x10000
	s_mov_b32 m0, s47
	s_nop 0
	global_load_lds_dwordx4 v175, s[28:29]
	s_add_i32 s47, s46, 0x12000
	s_mov_b32 m0, s47
	s_nop 0
	global_load_lds_dwordx4 v176, s[28:29]
	s_add_u32 s48, s28, 0x2000
	s_addc_u32 s49, s29, 0
	s_add_i32 s47, s46, 0x14000
	s_mov_b32 m0, s47
	s_nop 0
	global_load_lds_dwordx4 v175, s[48:49]
	s_add_i32 s47, s46, 0x16000
	s_mov_b32 m0, s47
	s_nop 0
	global_load_lds_dwordx4 v176, s[48:49]
	s_add_i32 s47, s46, 0x2000
	s_mov_b32 m0, s46
	s_nop 0
	global_load_lds_dwordx4 v1, s[30:31]
	s_nop 0
	s_mov_b32 m0, s47
	s_nop 0
	global_load_lds_dwordx4 v174, s[30:31]
	s_waitcnt vmcnt(8)
	s_waitcnt lgkmcnt(0)
	s_barrier
	s_setprio 1
	s_waitcnt lgkmcnt(6)
	v_mfma_f32_16x16x128_f8f6f4 v[62:65], v[130:137], v[66:73], v[62:65]
	v_mfma_f32_16x16x128_f8f6f4 v[58:61], v[138:145], v[66:73], v[58:61]
	s_waitcnt lgkmcnt(4)
	v_mfma_f32_16x16x128_f8f6f4 v[188:191], v[130:137], v[74:81], v[46:49]
	v_mfma_f32_16x16x128_f8f6f4 v[192:195], v[138:145], v[74:81], v[42:45]
	s_waitcnt lgkmcnt(2)
	v_mfma_f32_16x16x128_f8f6f4 v[196:199], v[130:137], v[82:89], v[30:33]
	v_mfma_f32_16x16x128_f8f6f4 v[200:203], v[138:145], v[82:89], v[26:29]
	s_waitcnt lgkmcnt(0)
	v_mfma_f32_16x16x128_f8f6f4 v[220:223], v[130:137], v[90:97], v[14:17]
	v_mfma_f32_16x16x128_f8f6f4 v[224:227], v[138:145], v[90:97], v[10:13]
	v_mfma_f32_16x16x128_f8f6f4 v[54:57], v[146:153], v[66:73], v[54:57]
	v_mfma_f32_16x16x128_f8f6f4 v[50:53], v[156:163], v[66:73], v[50:53]
	v_mfma_f32_16x16x128_f8f6f4 v[228:231], v[146:153], v[74:81], v[38:41]
	v_mfma_f32_16x16x128_f8f6f4 v[232:235], v[156:163], v[74:81], v[34:37]
	v_mfma_f32_16x16x128_f8f6f4 v[236:239], v[146:153], v[82:89], v[22:25]
	v_mfma_f32_16x16x128_f8f6f4 v[240:243], v[156:163], v[82:89], v[18:21]
	v_mfma_f32_16x16x128_f8f6f4 v[244:247], v[146:153], v[90:97], v[6:9]
	v_mfma_f32_16x16x128_f8f6f4 v[248:251], v[156:163], v[90:97], v[2:5]
	s_setprio 0
	s_barrier
	v_add_u32_e32 v10, 0x18000, v177
	s_nop 3
	ds_read_b128 v[2:5], v10
	ds_read_b128 v[6:9], v10 offset:1024
	ds_read_b128 v[18:21], v10 offset:2048
	ds_read_b128 v[22:25], v10 offset:3072
	v_add_u32_e32 v10, 0x1c000, v177
	ds_read_b128 v[130:133], v10
	ds_read_b128 v[134:137], v10 offset:1024
	ds_read_b128 v[138:141], v10 offset:2048
	ds_read_b128 v[142:145], v10 offset:3072
	ds_read_b128 v[10:13], v178 offset:32768
	ds_read_b128 v[14:17], v178 offset:33792
	ds_read_b128 v[26:29], v178 offset:34816
	ds_read_b128 v[30:33], v178 offset:35840
	ds_read_b128 v[34:37], v178 offset:36864
	ds_read_b128 v[38:41], v178 offset:37888
	ds_read_b128 v[42:45], v178 offset:38912
	ds_read_b128 v[46:49], v178 offset:39936
	s_add_u32 s30, s30, 0x20000
	s_addc_u32 s31, s31, 0
	s_add_i32 s47, s46, 0x4000
	s_mov_b32 m0, s47
	s_nop 0
	global_load_lds_dwordx4 v1, s[30:31]
	s_add_i32 s47, s46, 0x6000
	s_mov_b32 m0, s47
	s_nop 0
	global_load_lds_dwordx4 v174, s[30:31]
	s_waitcnt vmcnt(8)
	s_waitcnt lgkmcnt(0)
	s_barrier
; #define PG8_STAGE(bufoff, gbase, voff) do { PG8_GLDS((const char*)(gbase), (voff)[0], ldsb + (bufoff)); PG8_GLDS((const char*)(gbase), (voff)[1], ldsb + (bufoff) + 8192u); } while (0)
; #define PG8_STAGEA(bufoff, gbase, o0, o1) do { PG8_GLDS((const char*)(gbase), (o0), ldsb + (bufoff)); PG8_GLDS((const char*)(gbase), (o1), ldsb + (bufoff) + 8192u); } while (0)
; #define PG8_STAGEA1(bufoff, gbase) do { if constexpr (Sched::GATHER) { PG8_STAGEA(bufoff, gbase, vA2, vA3); } else { PG8_STAGEA(bufoff, (gbase) + hstep, vA0, vA1); } } while (0)
; #define PG8_LDA(dst, b, h) do { if constexpr (F8) { _Pragma("unroll") for (int m = 0; m < 4; ++m) dst##8[m] = PG8_LD32(lds + PG8_SA(b, h) + aoff + m * 2048); } else { \
;         _Pragma("unroll") for (int m = 0; m < 4; ++m) _Pragma("unroll") for (int k = 0; k < 2; ++k) dst[m][k] = *(const LAS bf16x8*)(lds + PG8_SA(b, h) + aoff + m * 2048 + k * 1024); } } while (0)
; #define PG8_LDB(dst, b, h) do { if constexpr (F8) { _Pragma("unroll") for (int n = 0; n < 2; ++n) dst##8[n] = PG8_LD32(lds + PG8_SB(b, h) + boff + n * 2048); } else { \
;         _Pragma("unroll") for (int n = 0; n < 2; ++n) _Pragma("unroll") for (int k = 0; k < 2; ++k) dst[n][k] = *(const LAS bf16x8*)(lds + PG8_SB(b, h) + boff + n * 2048 + k * 1024); } } while (0)
; #define PG8_WAIT_VR() PG8_WAIT_V(8)
; #define PG8_WAIT_L(n) asm volatile("s_waitcnt lgkmcnt(" #n ")" ::: "memory")
; #define PG8_BAR __builtin_amdgcn_s_barrier()
; #define PG8_SCHED __builtin_amdgcn_sched_barrier(0)
; template <class Epi, class Sched, bool F8 = false, bool PF = false, bool I8 = false, int PID = -1>
; __device__ __forceinline__ void gemm_phase(LAS unsigned char* lds, LAS unsigned char* xlds, const int RP, const int RPB, const int nt, const Sched& S, const Epi& E, const int stagger_ticks) {
;     ...
;             PG8_LDB(B0, 1, 0); PG8_LDB(B1, 1, 1); PG8_SCHED; PG8_LDA(At, 1, 0); PG8_STAGEA1(PG8_SA(0, 1), a2);
;             PG8_WAIT_VR(); PG8_WAIT_L(0); PG8_BAR; PG8_MMA(0, 0, At, B0); PG8_MMA(0, 1, At, B1); PG8_BAR; PG8_SCHED;
;             PG8_LDA(At, 1, 1); PG8_STAGE(PG8_SB(1, 0), b3, voffB); PG8_STAGE(PG8_SB(1, 1), b3 + hstepB, voffB); PG8_STAGEA(PG8_SA(1, 0), a3, vA0, vA1);
;             PG8_WAIT_VR(); PG8_WAIT_L(0); PG8_BAR; PG8_MMA(1, 0, At, B0); PG8_MMA(1, 1, At, B1); PG8_BAR; PG8_SCHED;
;         }
;         PROF_END(1); PROF_BEGIN(3);
;         if (wr == 0) PG8_BAR;
	s_setprio 1
	s_waitcnt lgkmcnt(6)
	v_mfma_f32_16x16x128_f8f6f4 v[114:117], v[2:9], v[10:17], v[114:117]
	v_mfma_f32_16x16x128_f8f6f4 v[118:121], v[18:25], v[10:17], v[118:121]
	s_waitcnt lgkmcnt(4)
	v_mfma_f32_16x16x128_f8f6f4 v[110:113], v[2:9], v[26:33], v[110:113]
	v_mfma_f32_16x16x128_f8f6f4 v[106:109], v[18:25], v[26:33], v[106:109]
	s_waitcnt lgkmcnt(2)
	v_mfma_f32_16x16x128_f8f6f4 v[94:97], v[2:9], v[34:41], v[204:207]
	v_mfma_f32_16x16x128_f8f6f4 v[90:93], v[18:25], v[34:41], v[208:211]
	s_waitcnt lgkmcnt(0)
	v_mfma_f32_16x16x128_f8f6f4 v[78:81], v[2:9], v[42:49], v[212:215]
	v_mfma_f32_16x16x128_f8f6f4 v[74:77], v[18:25], v[42:49], v[216:219]
	v_mfma_f32_16x16x128_f8f6f4 v[122:125], v[130:137], v[10:17], v[122:125]
	v_mfma_f32_16x16x128_f8f6f4 v[126:129], v[138:145], v[10:17], v[126:129]
	v_mfma_f32_16x16x128_f8f6f4 v[102:105], v[130:137], v[26:33], v[102:105]
	v_mfma_f32_16x16x128_f8f6f4 v[98:101], v[138:145], v[26:33], v[98:101]
	v_mfma_f32_16x16x128_f8f6f4 v[86:89], v[130:137], v[34:41], v[164:167]
	v_mfma_f32_16x16x128_f8f6f4 v[82:85], v[138:145], v[34:41], v[168:171]
	v_mfma_f32_16x16x128_f8f6f4 v[70:73], v[130:137], v[42:49], v[180:183]
	v_mfma_f32_16x16x128_f8f6f4 v[66:69], v[138:145], v[42:49], v[184:187]
	s_setprio 0
	s_barrier
	s_add_u32 s30, s28, 0x80
	ds_read_b128 v[34:37], v178 offset:49152
	ds_read_b128 v[38:41], v178 offset:50176
	ds_read_b128 v[146:149], v178 offset:51200
	ds_read_b128 v[150:153], v178 offset:52224
	ds_read_b128 v[156:159], v178 offset:53248
	ds_read_b128 v[160:163], v178 offset:54272
	ds_read_b128 v[164:167], v178 offset:55296
	ds_read_b128 v[168:171], v178 offset:56320
	s_addc_u32 s31, s29, 0
	s_add_i32 s47, s46, 0x18000
	s_mov_b32 m0, s47
	s_nop 0
	global_load_lds_dwordx4 v175, s[30:31]
	s_add_i32 s47, s46, 0x1a000
	s_mov_b32 m0, s47
	s_nop 0
	global_load_lds_dwordx4 v176, s[30:31]
	s_add_u32 s28, s28, 0x2080
	s_addc_u32 s29, s29, 0
	s_add_i32 s30, s46, 0x1c000
	s_mov_b32 m0, s30
	s_nop 0
	global_load_lds_dwordx4 v175, s[28:29]
	s_add_i32 s30, s46, 0x1e000
	s_mov_b32 m0, s30
	s_nop 0
	global_load_lds_dwordx4 v176, s[28:29]
	s_add_i32 s28, s46, 0x8000
	s_mov_b32 m0, s28
	s_nop 0
	global_load_lds_dwordx4 v1, s[2:3]
	s_add_i32 s46, s46, 0xa000
	s_mov_b32 m0, s46
	s_nop 0
	global_load_lds_dwordx4 v174, s[2:3]
	s_waitcnt vmcnt(8)
	s_waitcnt lgkmcnt(0)
	s_barrier
	s_setprio 1
	s_waitcnt lgkmcnt(6)
	v_mfma_f32_16x16x128_f8f6f4 v[62:65], v[2:9], v[34:41], v[62:65]
	v_mfma_f32_16x16x128_f8f6f4 v[58:61], v[18:25], v[34:41], v[58:61]
	s_waitcnt lgkmcnt(4)
	v_mfma_f32_16x16x128_f8f6f4 v[46:49], v[2:9], v[146:153], v[188:191]
	v_mfma_f32_16x16x128_f8f6f4 v[42:45], v[18:25], v[146:153], v[192:195]
	s_waitcnt lgkmcnt(2)
	v_mfma_f32_16x16x128_f8f6f4 v[30:33], v[2:9], v[156:163], v[196:199]
	v_mfma_f32_16x16x128_f8f6f4 v[26:29], v[18:25], v[156:163], v[200:203]
	s_waitcnt lgkmcnt(0)
	v_mfma_f32_16x16x128_f8f6f4 v[14:17], v[2:9], v[164:171], v[220:223]
	v_mfma_f32_16x16x128_f8f6f4 v[10:13], v[18:25], v[164:171], v[224:227]
	v_mfma_f32_16x16x128_f8f6f4 v[54:57], v[130:137], v[34:41], v[54:57]
	v_mfma_f32_16x16x128_f8f6f4 v[50:53], v[138:145], v[34:41], v[50:53]
	v_mfma_f32_16x16x128_f8f6f4 v[38:41], v[130:137], v[146:153], v[228:231]
	v_mfma_f32_16x16x128_f8f6f4 v[34:37], v[138:145], v[146:153], v[232:235]
	v_mfma_f32_16x16x128_f8f6f4 v[22:25], v[130:137], v[156:163], v[236:239]
	v_mfma_f32_16x16x128_f8f6f4 v[18:21], v[138:145], v[156:163], v[240:243]
	v_mfma_f32_16x16x128_f8f6f4 v[6:9], v[130:137], v[164:171], v[244:247]
	v_mfma_f32_16x16x128_f8f6f4 v[2:5], v[138:145], v[164:171], v[248:251]
	s_setprio 0
	s_barrier
	s_add_i32 s45, s45, 2
	s_add_u32 s43, s43, 0x100
	s_addc_u32 s44, s44, 0
	s_add_u32 s0, s0, 0x100
	s_addc_u32 s1, s1, 0
	s_cmp_gt_u32 s45, 5
	s_cbranch_scc0 .LBB0_753
	s_and_b64 vcc, exec, s[24:25]
	s_cbranch_vccz .LBB0_756
	s_barrier

; #define PG8_STAGE(bufoff, gbase, voff) do { PG8_GLDS((const char*)(gbase), (voff)[0], ldsb + (bufoff)); PG8_GLDS((const char*)(gbase), (voff)[1], ldsb + (bufoff) + 8192u); } while (0)
; template <class Epi, class Sched, bool F8 = false, bool PF = false, bool I8 = false, int PID = -1>
; __device__ __forceinline__ void gemm_phase(LAS unsigned char* lds, LAS unsigned char* xlds, const int RP, const int RPB, const int nt, const Sched& S, const Epi& E, const int stagger_ticks) {
;     ...
;             const char* a1 = cA + (size_t)(t + 1) * kstep;
;             const char* a2 = last ? nA : cA + (size_t)(t + 2) * kstep; const char* b2 = last ? nB : cB + (size_t)(t + 2) * kstep;
;             const char* a3 = a2 + kstep; const char* b3 = b2 + kstep;
;             if constexpr (PF) { const char* pfa = (t + 4 < nt) ? cA + (size_t)(t + 4) * kstep : nA + (size_t)(t + 4 - nt) * kstep;
;                 asm volatile("s_mov_b32 m0, %2\n\ts_nop 0\n\tglobal_load_lds_dword %0, %1" :: "v"(voffP), "s"(pfa), "s"(ldsP) : "memory", "m0"); }
;             const bool relax = (Epi::RELAX > 0) && (t == 0) && epi_ran;
;             PG8_LDB(B0, 0, 0); PG8_LDB(B1, 0, 1); PG8_SCHED; PG8_LDA(At, 0, 0); PG8_STAGEA1(PG8_SA(1, 1), a1);
;             if (Sched::GATHER) { if (last) { const u32x4 nv = *nslot; vA0 = nv.x; vA1 = nv.y; vA2 = nv.z; vA3 = nv.w; } }
;             PG8_WAIT_VX(); PG8_WAIT_L(0); PG8_BAR; PG8_MMA(0, 0, At, B0); PG8_MMA(0, 1, At, B1); PG8_BAR; PG8_SCHED;
;             if constexpr (Epi::BIAS_DMA) { if (t == 0 && has_next) E.bias_dma(nxt, xlds + 8192 + ((ui + 1) & 1) * Epi::BIAS_STRIDE, wid, lane); }
;             PG8_LDA(At, 0, 1); PG8_STAGE(PG8_SB(0, 0), b2, voffB); PG8_STAGE(PG8_SB(0, 1), b2 + hstepB, voffB); PG8_STAGEA(PG8_SA(0, 0), a2, vA0, vA1);
;             PG8_WAIT_VX(); PG8_WAIT_L(0); PG8_BAR; PG8_MMA(1, 0, At, B0); PG8_MMA(1, 1, At, B1); PG8_BAR; PG8_SCHED;
;             PG8_LDB(B0, 1, 0); PG8_LDB(B1, 1, 1); PG8_SCHED; PG8_LDA(At, 1, 0); PG8_STAGEA1(PG8_SA(0, 1), a2);
;             PG8_WAIT_VR(); PG8_WAIT_L(0); PG8_BAR; PG8_MMA(0, 0, At, B0); PG8_MMA(0, 1, At, B1); PG8_BAR; PG8_SCHED;
;             PG8_LDA(At, 1, 1); PG8_STAGE(PG8_SB(1, 0), b3, voffB); PG8_STAGE(PG8_SB(1, 1), b3 + hstepB, voffB); PG8_STAGEA(PG8_SA(1, 0), a3, vA0, vA1);
;             PG8_WAIT_VR(); PG8_WAIT_L(0); PG8_BAR; PG8_MMA(1, 0, At, B0); PG8_MMA(1, 1, At, B1); PG8_BAR; PG8_SCHED;
.LBB0_958:
	s_add_u32 s28, s2, 0x80
	s_addc_u32 s29, s3, 0
	s_and_b64 s[24:25], s[26:27], exec
	s_cselect_b32 s28, s20, s28
	s_cselect_b32 s29, s21, s29
	s_add_u32 s24, s28, 0x80
	s_addc_u32 s25, s29, 0
	s_waitcnt vmcnt(8)
	s_and_b64 s[26:27], s[26:27], exec
	s_waitcnt lgkmcnt(0)
	s_cselect_b32 s26, s8, s23
	s_cselect_b32 s27, s9, s63
	s_add_u32 s30, s26, 0x80
	s_addc_u32 s31, s27, 0
	s_barrier
	s_setprio 1
	s_waitcnt lgkmcnt(6)
	v_mfma_f32_16x16x128_f8f6f4 v[186:189], v[18:25], v[58:65], v[186:189]
	v_mfma_f32_16x16x128_f8f6f4 v[194:197], v[26:33], v[58:65], v[194:197]
	s_waitcnt lgkmcnt(4)
	v_mfma_f32_16x16x128_f8f6f4 v[190:193], v[18:25], v[50:57], v[190:193]
	v_mfma_f32_16x16x128_f8f6f4 v[182:185], v[26:33], v[50:57], v[182:185]
	s_waitcnt lgkmcnt(2)
	v_mfma_f32_16x16x128_f8f6f4 v[154:157], v[18:25], v[42:49], v[154:157]
	v_mfma_f32_16x16x128_f8f6f4 v[150:153], v[26:33], v[42:49], v[150:153]
	s_waitcnt lgkmcnt(0)
	v_mfma_f32_16x16x128_f8f6f4 v[138:141], v[18:25], v[34:41], v[138:141]
	v_mfma_f32_16x16x128_f8f6f4 v[134:137], v[26:33], v[34:41], v[134:137]
	v_mfma_f32_16x16x128_f8f6f4 v[174:177], v[2:9], v[58:65], v[174:177]
	v_mfma_f32_16x16x128_f8f6f4 v[178:181], v[10:17], v[58:65], v[178:181]
	v_mfma_f32_16x16x128_f8f6f4 v[170:173], v[2:9], v[50:57], v[170:173]
	v_mfma_f32_16x16x128_f8f6f4 v[166:169], v[10:17], v[50:57], v[166:169]
	v_mfma_f32_16x16x128_f8f6f4 v[162:165], v[2:9], v[42:49], v[162:165]
	v_mfma_f32_16x16x128_f8f6f4 v[158:161], v[10:17], v[42:49], v[158:161]
	v_mfma_f32_16x16x128_f8f6f4 v[146:149], v[2:9], v[34:41], v[146:149]
	v_mfma_f32_16x16x128_f8f6f4 v[142:145], v[10:17], v[34:41], v[142:145]
	s_setprio 0
	s_barrier
	ds_read_b128 v[34:37], v207 offset:16384
	ds_read_b128 v[38:41], v207 offset:17408
	ds_read_b128 v[42:45], v207 offset:18432
	ds_read_b128 v[46:49], v207 offset:19456
	ds_read_b128 v[50:53], v207 offset:20480
	ds_read_b128 v[54:57], v207 offset:21504
	ds_read_b128 v[58:61], v207 offset:22528
	ds_read_b128 v[62:65], v207 offset:23552
	s_add_i32 s66, s65, 0x10000
	s_mov_b32 m0, s66
	s_nop 0
	global_load_lds_dwordx4 v204, s[26:27]
	s_add_i32 s66, s65, 0x12000
	s_mov_b32 m0, s66
	s_nop 0
	global_load_lds_dwordx4 v205, s[26:27]
	s_add_u32 s66, s26, 0x2000
	s_addc_u32 s67, s27, 0
	s_add_i32 s68, s65, 0x14000
	s_mov_b32 m0, s68
	s_nop 0
	global_load_lds_dwordx4 v204, s[66:67]
	s_add_i32 s68, s65, 0x16000
	s_mov_b32 m0, s68
	s_nop 0
	global_load_lds_dwordx4 v205, s[66:67]
	s_waitcnt vmcnt(6)
	s_waitcnt lgkmcnt(0)
	s_barrier
	s_setprio 1
	s_waitcnt lgkmcnt(6)
	v_mfma_f32_16x16x128_f8f6f4 v[122:125], v[18:25], v[34:41], v[122:125]
	v_mfma_f32_16x16x128_f8f6f4 v[118:121], v[26:33], v[34:41], v[118:121]
	s_waitcnt lgkmcnt(4)
	v_mfma_f32_16x16x128_f8f6f4 v[106:109], v[18:25], v[42:49], v[106:109]
	v_mfma_f32_16x16x128_f8f6f4 v[102:105], v[26:33], v[42:49], v[102:105]
	s_mov_b32 m0, s65
	s_nop 0
	global_load_lds_dwordx4 v66, s[28:29]
	s_waitcnt lgkmcnt(2)
	v_mfma_f32_16x16x128_f8f6f4 v[90:93], v[18:25], v[50:57], v[90:93]
	v_mfma_f32_16x16x128_f8f6f4 v[86:89], v[26:33], v[50:57], v[86:89]
	s_waitcnt lgkmcnt(0)
	v_mfma_f32_16x16x128_f8f6f4 v[74:77], v[18:25], v[58:65], v[74:77]
	v_mfma_f32_16x16x128_f8f6f4 v[70:73], v[26:33], v[58:65], v[70:73]
	v_mfma_f32_16x16x128_f8f6f4 v[130:133], v[2:9], v[34:41], v[130:133]
	v_mfma_f32_16x16x128_f8f6f4 v[126:129], v[10:17], v[34:41], v[126:129]
	v_mfma_f32_16x16x128_f8f6f4 v[114:117], v[2:9], v[42:49], v[114:117]
	v_mfma_f32_16x16x128_f8f6f4 v[110:113], v[10:17], v[42:49], v[110:113]
	s_add_i32 s98, s65, 0x2000
	s_mov_b32 m0, s98
	s_nop 0
	global_load_lds_dwordx4 v67, s[28:29]
	v_mfma_f32_16x16x128_f8f6f4 v[98:101], v[2:9], v[50:57], v[98:101]
	v_mfma_f32_16x16x128_f8f6f4 v[94:97], v[10:17], v[50:57], v[94:97]
	v_mfma_f32_16x16x128_f8f6f4 v[82:85], v[2:9], v[58:65], v[82:85]
	v_mfma_f32_16x16x128_f8f6f4 v[78:81], v[10:17], v[58:65], v[78:81]
	s_setprio 0
	s_barrier
; #define PG8_STAGE(bufoff, gbase, voff) do { PG8_GLDS((const char*)(gbase), (voff)[0], ldsb + (bufoff)); PG8_GLDS((const char*)(gbase), (voff)[1], ldsb + (bufoff) + 8192u); } while (0)
; #define PG8_STAGEA(bufoff, gbase, o0, o1) do { PG8_GLDS((const char*)(gbase), (o0), ldsb + (bufoff)); PG8_GLDS((const char*)(gbase), (o1), ldsb + (bufoff) + 8192u); } while (0)
; #define PG8_STAGEA1(bufoff, gbase) do { if constexpr (Sched::GATHER) { PG8_STAGEA(bufoff, gbase, vA2, vA3); } else { PG8_STAGEA(bufoff, (gbase) + hstep, vA0, vA1); } } while (0)
; #define PG8_LDA(dst, b, h) do { if constexpr (F8) { _Pragma("unroll") for (int m = 0; m < 4; ++m) dst##8[m] = PG8_LD32(lds + PG8_SA(b, h) + aoff + m * 2048); } else { \
;         _Pragma("unroll") for (int m = 0; m < 4; ++m) _Pragma("unroll") for (int k = 0; k < 2; ++k) dst[m][k] = *(const LAS bf16x8*)(lds + PG8_SA(b, h) + aoff + m * 2048 + k * 1024); } } while (0)
; #define PG8_LDB(dst, b, h) do { if constexpr (F8) { _Pragma("unroll") for (int n = 0; n < 2; ++n) dst##8[n] = PG8_LD32(lds + PG8_SB(b, h) + boff + n * 2048); } else { \
;         _Pragma("unroll") for (int n = 0; n < 2; ++n) _Pragma("unroll") for (int k = 0; k < 2; ++k) dst[n][k] = *(const LAS bf16x8*)(lds + PG8_SB(b, h) + boff + n * 2048 + k * 1024); } } while (0)
; #define PG8_WAIT_VR() PG8_WAIT_V(8)
; #define PG8_WAIT_L(n) asm volatile("s_waitcnt lgkmcnt(" #n ")" ::: "memory")
; #define PG8_BAR __builtin_amdgcn_s_barrier()
; #define PG8_SCHED __builtin_amdgcn_sched_barrier(0)
; template <class Epi, class Sched, bool F8 = false, bool PF = false, bool I8 = false, int PID = -1>
; __device__ __forceinline__ void gemm_phase(LAS unsigned char* lds, LAS unsigned char* xlds, const int RP, const int RPB, const int nt, const Sched& S, const Epi& E, const int stagger_ticks) {
;     ...
;             PG8_LDB(B0, 1, 0); PG8_LDB(B1, 1, 1); PG8_SCHED; PG8_LDA(At, 1, 0); PG8_STAGEA1(PG8_SA(0, 1), a2);
;             PG8_WAIT_VR(); PG8_WAIT_L(0); PG8_BAR; PG8_MMA(0, 0, At, B0); PG8_MMA(0, 1, At, B1); PG8_BAR; PG8_SCHED;
;             PG8_LDA(At, 1, 1); PG8_STAGE(PG8_SB(1, 0), b3, voffB); PG8_STAGE(PG8_SB(1, 1), b3 + hstepB, voffB); PG8_STAGEA(PG8_SA(1, 0), a3, vA0, vA1);
;             PG8_WAIT_VR(); PG8_WAIT_L(0); PG8_BAR; PG8_MMA(1, 0, At, B0); PG8_MMA(1, 1, At, B1); PG8_BAR; PG8_SCHED;
	v_add_u32_e32 v14, 0x18000, v206
	v_add_u32_e32 v30, 0x1c000, v206
	ds_read_b128 v[2:5], v14
	ds_read_b128 v[6:9], v14 offset:1024
	ds_read_b128 v[10:13], v14 offset:2048
	ds_read_b128 v[14:17], v14 offset:3072
	ds_read_b128 v[18:21], v30
	ds_read_b128 v[22:25], v30 offset:1024
	ds_read_b128 v[26:29], v30 offset:2048
	ds_read_b128 v[30:33], v30 offset:3072
	ds_read_b128 v[34:37], v207 offset:32768
	ds_read_b128 v[38:41], v207 offset:33792
	ds_read_b128 v[42:45], v207 offset:34816
	ds_read_b128 v[46:49], v207 offset:35840
	ds_read_b128 v[50:53], v207 offset:36864
	ds_read_b128 v[54:57], v207 offset:37888
	ds_read_b128 v[58:61], v207 offset:38912
	ds_read_b128 v[62:65], v207 offset:39936
	s_add_i32 s66, s65, 0x4000
	s_mov_b32 m0, s66
	s_nop 0
	global_load_lds_dwordx4 v68, s[28:29]
	s_add_i32 s66, s65, 0x6000
	s_mov_b32 m0, s66
	s_nop 0
	global_load_lds_dwordx4 v69, s[28:29]
	s_waitcnt vmcnt(8)
	s_waitcnt lgkmcnt(0)
	s_barrier
	s_setprio 1
	s_waitcnt lgkmcnt(6)
	v_mfma_f32_16x16x128_f8f6f4 v[186:189], v[2:9], v[34:41], v[186:189]
	v_mfma_f32_16x16x128_f8f6f4 v[194:197], v[10:17], v[34:41], v[194:197]
	s_waitcnt lgkmcnt(4)
	v_mfma_f32_16x16x128_f8f6f4 v[190:193], v[2:9], v[42:49], v[190:193]
	v_mfma_f32_16x16x128_f8f6f4 v[182:185], v[10:17], v[42:49], v[182:185]
	s_waitcnt lgkmcnt(2)
	v_mfma_f32_16x16x128_f8f6f4 v[154:157], v[2:9], v[50:57], v[154:157]
	v_mfma_f32_16x16x128_f8f6f4 v[150:153], v[10:17], v[50:57], v[150:153]
	s_waitcnt lgkmcnt(0)
	v_mfma_f32_16x16x128_f8f6f4 v[138:141], v[2:9], v[58:65], v[138:141]
	v_mfma_f32_16x16x128_f8f6f4 v[134:137], v[10:17], v[58:65], v[134:137]
	v_mfma_f32_16x16x128_f8f6f4 v[174:177], v[18:25], v[34:41], v[174:177]
	v_mfma_f32_16x16x128_f8f6f4 v[178:181], v[26:33], v[34:41], v[178:181]
	v_mfma_f32_16x16x128_f8f6f4 v[170:173], v[18:25], v[42:49], v[170:173]
	v_mfma_f32_16x16x128_f8f6f4 v[166:169], v[26:33], v[42:49], v[166:169]
	v_mfma_f32_16x16x128_f8f6f4 v[162:165], v[18:25], v[50:57], v[162:165]
	v_mfma_f32_16x16x128_f8f6f4 v[158:161], v[26:33], v[50:57], v[158:161]
	v_mfma_f32_16x16x128_f8f6f4 v[146:149], v[18:25], v[58:65], v[146:149]
	v_mfma_f32_16x16x128_f8f6f4 v[142:145], v[26:33], v[58:65], v[142:145]
	s_setprio 0
	s_barrier
	ds_read_b128 v[34:37], v207 offset:49152
	ds_read_b128 v[38:41], v207 offset:50176
	ds_read_b128 v[42:45], v207 offset:51200
	ds_read_b128 v[46:49], v207 offset:52224
	ds_read_b128 v[50:53], v207 offset:53248
	ds_read_b128 v[54:57], v207 offset:54272
	ds_read_b128 v[58:61], v207 offset:55296
	ds_read_b128 v[62:65], v207 offset:56320
	s_add_i32 s28, s65, 0x18000
	s_mov_b32 m0, s28
	s_nop 0
	global_load_lds_dwordx4 v204, s[30:31]
	s_add_i32 s28, s65, 0x1a000
	s_mov_b32 m0, s28
	s_nop 0
	global_load_lds_dwordx4 v205, s[30:31]
	s_add_u32 s26, s26, 0x2080
	s_addc_u32 s27, s27, 0
	s_add_i32 s28, s65, 0x1c000
	s_mov_b32 m0, s28
	s_nop 0
	global_load_lds_dwordx4 v204, s[26:27]
	s_add_i32 s28, s65, 0x1e000
	s_mov_b32 m0, s28
	s_nop 0
	global_load_lds_dwordx4 v205, s[26:27]
	s_waitcnt vmcnt(6)
	s_waitcnt lgkmcnt(0)
	s_barrier
	s_setprio 1
	s_waitcnt lgkmcnt(6)
	v_mfma_f32_16x16x128_f8f6f4 v[122:125], v[2:9], v[34:41], v[122:125]
	v_mfma_f32_16x16x128_f8f6f4 v[118:121], v[10:17], v[34:41], v[118:121]
	s_waitcnt lgkmcnt(4)
	v_mfma_f32_16x16x128_f8f6f4 v[106:109], v[2:9], v[42:49], v[106:109]
	v_mfma_f32_16x16x128_f8f6f4 v[102:105], v[10:17], v[42:49], v[102:105]
	s_add_i32 s98, s65, 0x8000
	s_mov_b32 m0, s98
	s_nop 0
	global_load_lds_dwordx4 v66, s[24:25]
	s_waitcnt lgkmcnt(2)
	v_mfma_f32_16x16x128_f8f6f4 v[90:93], v[2:9], v[50:57], v[90:93]
	v_mfma_f32_16x16x128_f8f6f4 v[86:89], v[10:17], v[50:57], v[86:89]
	s_waitcnt lgkmcnt(0)
	v_mfma_f32_16x16x128_f8f6f4 v[74:77], v[2:9], v[58:65], v[74:77]
	v_mfma_f32_16x16x128_f8f6f4 v[70:73], v[10:17], v[58:65], v[70:73]
	v_mfma_f32_16x16x128_f8f6f4 v[130:133], v[18:25], v[34:41], v[130:133]
	v_mfma_f32_16x16x128_f8f6f4 v[126:129], v[26:33], v[34:41], v[126:129]
	v_mfma_f32_16x16x128_f8f6f4 v[114:117], v[18:25], v[42:49], v[114:117]
	v_mfma_f32_16x16x128_f8f6f4 v[110:113], v[26:33], v[42:49], v[110:113]
	s_add_i32 s98, s65, 0xa000
	s_mov_b32 m0, s98
	s_nop 0
	global_load_lds_dwordx4 v67, s[24:25]
	v_mfma_f32_16x16x128_f8f6f4 v[98:101], v[18:25], v[50:57], v[98:101]
	v_mfma_f32_16x16x128_f8f6f4 v[94:97], v[26:33], v[50:57], v[94:97]
	v_mfma_f32_16x16x128_f8f6f4 v[82:85], v[18:25], v[58:65], v[82:85]
	v_mfma_f32_16x16x128_f8f6f4 v[78:81], v[26:33], v[58:65], v[78:81]
	s_setprio 0
	s_barrier
	s_add_i32 s64, s64, 2
	s_add_u32 s23, s23, 0x100
	s_addc_u32 s63, s63, 0
	s_add_u32 s2, s2, 0x100
	s_addc_u32 s3, s3, 0
	s_cmp_gt_u32 s64, 5
	s_cbranch_scc1 .LBB0_961

; #define PG8_STAGE(bufoff, gbase, voff) do { PG8_GLDS((const char*)(gbase), (voff)[0], ldsb + (bufoff)); PG8_GLDS((const char*)(gbase), (voff)[1], ldsb + (bufoff) + 8192u); } while (0)
; template <class Epi, class Sched, bool F8 = false, bool PF = false, bool I8 = false, int PID = -1>
; __device__ __forceinline__ void gemm_phase(LAS unsigned char* lds, LAS unsigned char* xlds, const int RP, const int RPB, const int nt, const Sched& S, const Epi& E, const int stagger_ticks) {
;     ...
;             const char* a1 = cA + (size_t)(t + 1) * kstep;
;             const char* a2 = last ? nA : cA + (size_t)(t + 2) * kstep; const char* b2 = last ? nB : cB + (size_t)(t + 2) * kstep;
;             const char* a3 = a2 + kstep; const char* b3 = b2 + kstep;
;             if constexpr (PF) { const char* pfa = (t + 4 < nt) ? cA + (size_t)(t + 4) * kstep : nA + (size_t)(t + 4 - nt) * kstep;
;                 asm volatile("s_mov_b32 m0, %2\n\ts_nop 0\n\tglobal_load_lds_dword %0, %1" :: "v"(voffP), "s"(pfa), "s"(ldsP) : "memory", "m0"); }
;             const bool relax = (Epi::RELAX > 0) && (t == 0) && epi_ran;
;             PG8_LDB(B0, 0, 0); PG8_LDB(B1, 0, 1); PG8_SCHED; PG8_LDA(At, 0, 0); PG8_STAGEA1(PG8_SA(1, 1), a1);
;             if (Sched::GATHER) { if (last) { const u32x4 nv = *nslot; vA0 = nv.x; vA1 = nv.y; vA2 = nv.z; vA3 = nv.w; } }
;             PG8_WAIT_VX(); PG8_WAIT_L(0); PG8_BAR; PG8_MMA(0, 0, At, B0); PG8_MMA(0, 1, At, B1); PG8_BAR; PG8_SCHED;
;             if constexpr (Epi::BIAS_DMA) { if (t == 0 && has_next) E.bias_dma(nxt, xlds + 8192 + ((ui + 1) & 1) * Epi::BIAS_STRIDE, wid, lane); }
;             PG8_LDA(At, 0, 1); PG8_STAGE(PG8_SB(0, 0), b2, voffB); PG8_STAGE(PG8_SB(0, 1), b2 + hstepB, voffB); PG8_STAGEA(PG8_SA(0, 0), a2, vA0, vA1);
;             PG8_WAIT_VX(); PG8_WAIT_L(0); PG8_BAR; PG8_MMA(1, 0, At, B0); PG8_MMA(1, 1, At, B1); PG8_BAR; PG8_SCHED;
;             PG8_LDB(B0, 1, 0); PG8_LDB(B1, 1, 1); PG8_SCHED; PG8_LDA(At, 1, 0); PG8_STAGEA1(PG8_SA(0, 1), a2);
;             PG8_WAIT_VR(); PG8_WAIT_L(0); PG8_BAR; PG8_MMA(0, 0, At, B0); PG8_MMA(0, 1, At, B1); PG8_BAR; PG8_SCHED;
;             PG8_LDA(At, 1, 1); PG8_STAGE(PG8_SB(1, 0), b3, voffB); PG8_STAGE(PG8_SB(1, 1), b3 + hstepB, voffB); PG8_STAGEA(PG8_SA(1, 0), a3, vA0, vA1);
;             PG8_WAIT_VR(); PG8_WAIT_L(0); PG8_BAR; PG8_MMA(1, 0, At, B0); PG8_MMA(1, 1, At, B1); PG8_BAR; PG8_SCHED;
.Lmy_z958:
	s_add_u32 s28, s2, 0x80
	s_addc_u32 s29, s3, 0
	s_and_b64 s[24:25], s[26:27], exec
	s_cselect_b32 s28, s20, s28
	s_cselect_b32 s29, s21, s29
	s_add_u32 s24, s28, 0x80
	s_addc_u32 s25, s29, 0
	s_waitcnt vmcnt(8)
	s_and_b64 s[26:27], s[26:27], exec
	s_waitcnt lgkmcnt(0)
	s_cselect_b32 s26, s8, s23
	s_cselect_b32 s27, s9, s63
	s_add_u32 s30, s26, 0x80
	s_addc_u32 s31, s27, 0
	s_barrier
	s_setprio 1
	s_waitcnt lgkmcnt(6)
	v_mfma_f32_16x16x128_f8f6f4 v[186:189], v[18:25], v[58:65], 0
	v_mfma_f32_16x16x128_f8f6f4 v[194:197], v[26:33], v[58:65], 0
	s_waitcnt lgkmcnt(4)
	v_mfma_f32_16x16x128_f8f6f4 v[190:193], v[18:25], v[50:57], 0
	v_mfma_f32_16x16x128_f8f6f4 v[182:185], v[26:33], v[50:57], 0
	s_waitcnt lgkmcnt(2)
	v_mfma_f32_16x16x128_f8f6f4 v[154:157], v[18:25], v[42:49], 0
	v_mfma_f32_16x16x128_f8f6f4 v[150:153], v[26:33], v[42:49], 0
	s_waitcnt lgkmcnt(0)
	v_mfma_f32_16x16x128_f8f6f4 v[138:141], v[18:25], v[34:41], 0
	v_mfma_f32_16x16x128_f8f6f4 v[134:137], v[26:33], v[34:41], 0
	v_mfma_f32_16x16x128_f8f6f4 v[174:177], v[2:9], v[58:65], 0
	v_mfma_f32_16x16x128_f8f6f4 v[178:181], v[10:17], v[58:65], 0
	v_mfma_f32_16x16x128_f8f6f4 v[170:173], v[2:9], v[50:57], 0
	v_mfma_f32_16x16x128_f8f6f4 v[166:169], v[10:17], v[50:57], 0
	v_mfma_f32_16x16x128_f8f6f4 v[162:165], v[2:9], v[42:49], 0
	v_mfma_f32_16x16x128_f8f6f4 v[158:161], v[10:17], v[42:49], 0
	v_mfma_f32_16x16x128_f8f6f4 v[146:149], v[2:9], v[34:41], 0
	v_mfma_f32_16x16x128_f8f6f4 v[142:145], v[10:17], v[34:41], 0
	s_setprio 0
	s_barrier
	ds_read_b128 v[34:37], v207 offset:16384
	ds_read_b128 v[38:41], v207 offset:17408
	ds_read_b128 v[42:45], v207 offset:18432
	ds_read_b128 v[46:49], v207 offset:19456
	ds_read_b128 v[50:53], v207 offset:20480
	ds_read_b128 v[54:57], v207 offset:21504
	ds_read_b128 v[58:61], v207 offset:22528
	ds_read_b128 v[62:65], v207 offset:23552
	s_add_i32 s66, s65, 0x10000
	s_mov_b32 m0, s66
	s_nop 0
	global_load_lds_dwordx4 v204, s[26:27]
	s_add_i32 s66, s65, 0x12000
	s_mov_b32 m0, s66
	s_nop 0
	global_load_lds_dwordx4 v205, s[26:27]
	s_add_u32 s66, s26, 0x2000
	s_addc_u32 s67, s27, 0
	s_add_i32 s68, s65, 0x14000
	s_mov_b32 m0, s68
	s_nop 0
	global_load_lds_dwordx4 v204, s[66:67]
	s_add_i32 s68, s65, 0x16000
	s_mov_b32 m0, s68
	s_nop 0
	global_load_lds_dwordx4 v205, s[66:67]
	s_waitcnt vmcnt(6)
	s_waitcnt lgkmcnt(0)
	s_barrier
	s_setprio 1
	s_waitcnt lgkmcnt(6)
	v_mfma_f32_16x16x128_f8f6f4 v[122:125], v[18:25], v[34:41], 0
	v_mfma_f32_16x16x128_f8f6f4 v[118:121], v[26:33], v[34:41], 0
	s_waitcnt lgkmcnt(4)
	v_mfma_f32_16x16x128_f8f6f4 v[106:109], v[18:25], v[42:49], 0
	v_mfma_f32_16x16x128_f8f6f4 v[102:105], v[26:33], v[42:49], 0
	s_mov_b32 m0, s65
	s_nop 0
	global_load_lds_dwordx4 v66, s[28:29]
	s_waitcnt lgkmcnt(2)
	v_mfma_f32_16x16x128_f8f6f4 v[90:93], v[18:25], v[50:57], 0
	v_mfma_f32_16x16x128_f8f6f4 v[86:89], v[26:33], v[50:57], 0
	s_waitcnt lgkmcnt(0)
	v_mfma_f32_16x16x128_f8f6f4 v[74:77], v[18:25], v[58:65], 0
	v_mfma_f32_16x16x128_f8f6f4 v[70:73], v[26:33], v[58:65], 0
	v_mfma_f32_16x16x128_f8f6f4 v[130:133], v[2:9], v[34:41], 0
	v_mfma_f32_16x16x128_f8f6f4 v[126:129], v[10:17], v[34:41], 0
	v_mfma_f32_16x16x128_f8f6f4 v[114:117], v[2:9], v[42:49], 0
	v_mfma_f32_16x16x128_f8f6f4 v[110:113], v[10:17], v[42:49], 0
	s_add_i32 s98, s65, 0x2000
	s_mov_b32 m0, s98
	s_nop 0
	global_load_lds_dwordx4 v67, s[28:29]
	v_mfma_f32_16x16x128_f8f6f4 v[98:101], v[2:9], v[50:57], 0
	v_mfma_f32_16x16x128_f8f6f4 v[94:97], v[10:17], v[50:57], 0
	v_mfma_f32_16x16x128_f8f6f4 v[82:85], v[2:9], v[58:65], 0
	v_mfma_f32_16x16x128_f8f6f4 v[78:81], v[10:17], v[58:65], 0
	s_setprio 0
	s_barrier
	v_add_u32_e32 v14, 0x18000, v206
	v_add_u32_e32 v30, 0x1c000, v206
	ds_read_b128 v[2:5], v14
	ds_read_b128 v[6:9], v14 offset:1024
	ds_read_b128 v[10:13], v14 offset:2048
	ds_read_b128 v[14:17], v14 offset:3072
	ds_read_b128 v[18:21], v30
	ds_read_b128 v[22:25], v30 offset:1024
	ds_read_b128 v[26:29], v30 offset:2048
	ds_read_b128 v[30:33], v30 offset:3072
	ds_read_b128 v[34:37], v207 offset:32768
	ds_read_b128 v[38:41], v207 offset:33792
	ds_read_b128 v[42:45], v207 offset:34816
	ds_read_b128 v[46:49], v207 offset:35840
	ds_read_b128 v[50:53], v207 offset:36864
	ds_read_b128 v[54:57], v207 offset:37888
	ds_read_b128 v[58:61], v207 offset:38912
	ds_read_b128 v[62:65], v207 offset:39936
	s_add_i32 s66, s65, 0x4000
	s_mov_b32 m0, s66
	s_nop 0
	global_load_lds_dwordx4 v68, s[28:29]
	s_add_i32 s66, s65, 0x6000
	s_mov_b32 m0, s66
	s_nop 0
	global_load_lds_dwordx4 v69, s[28:29]
	s_waitcnt vmcnt(8)
	s_waitcnt lgkmcnt(0)
	s_barrier
; #define PG8_STAGE(bufoff, gbase, voff) do { PG8_GLDS((const char*)(gbase), (voff)[0], ldsb + (bufoff)); PG8_GLDS((const char*)(gbase), (voff)[1], ldsb + (bufoff) + 8192u); } while (0)
; #define PG8_STAGEA(bufoff, gbase, o0, o1) do { PG8_GLDS((const char*)(gbase), (o0), ldsb + (bufoff)); PG8_GLDS((const char*)(gbase), (o1), ldsb + (bufoff) + 8192u); } while (0)
; #define PG8_STAGEA1(bufoff, gbase) do { if constexpr (Sched::GATHER) { PG8_STAGEA(bufoff, gbase, vA2, vA3); } else { PG8_STAGEA(bufoff, (gbase) + hstep, vA0, vA1); } } while (0)
; #define PG8_LDA(dst, b, h) do { if constexpr (F8) { _Pragma("unroll") for (int m = 0; m < 4; ++m) dst##8[m] = PG8_LD32(lds + PG8_SA(b, h) + aoff + m * 2048); } else { \
;         _Pragma("unroll") for (int m = 0; m < 4; ++m) _Pragma("unroll") for (int k = 0; k < 2; ++k) dst[m][k] = *(const LAS bf16x8*)(lds + PG8_SA(b, h) + aoff + m * 2048 + k * 1024); } } while (0)
; #define PG8_LDB(dst, b, h) do { if constexpr (F8) { _Pragma("unroll") for (int n = 0; n < 2; ++n) dst##8[n] = PG8_LD32(lds + PG8_SB(b, h) + boff + n * 2048); } else { \
;         _Pragma("unroll") for (int n = 0; n < 2; ++n) _Pragma("unroll") for (int k = 0; k < 2; ++k) dst[n][k] = *(const LAS bf16x8*)(lds + PG8_SB(b, h) + boff + n * 2048 + k * 1024); } } while (0)
; #define PG8_WAIT_VR() PG8_WAIT_V(8)
; #define PG8_WAIT_L(n) asm volatile("s_waitcnt lgkmcnt(" #n ")" ::: "memory")
; #define PG8_BAR __builtin_amdgcn_s_barrier()
; #define PG8_SCHED __builtin_amdgcn_sched_barrier(0)
; template <class Epi, class Sched, bool F8 = false, bool PF = false, bool I8 = false, int PID = -1>
; __device__ __forceinline__ void gemm_phase(LAS unsigned char* lds, LAS unsigned char* xlds, const int RP, const int RPB, const int nt, const Sched& S, const Epi& E, const int stagger_ticks) {
;     ...
;             PG8_LDB(B0, 1, 0); PG8_LDB(B1, 1, 1); PG8_SCHED; PG8_LDA(At, 1, 0); PG8_STAGEA1(PG8_SA(0, 1), a2);
;             PG8_WAIT_VR(); PG8_WAIT_L(0); PG8_BAR; PG8_MMA(0, 0, At, B0); PG8_MMA(0, 1, At, B1); PG8_BAR; PG8_SCHED;
;             PG8_LDA(At, 1, 1); PG8_STAGE(PG8_SB(1, 0), b3, voffB); PG8_STAGE(PG8_SB(1, 1), b3 + hstepB, voffB); PG8_STAGEA(PG8_SA(1, 0), a3, vA0, vA1);
;             PG8_WAIT_VR(); PG8_WAIT_L(0); PG8_BAR; PG8_MMA(1, 0, At, B0); PG8_MMA(1, 1, At, B1); PG8_BAR; PG8_SCHED;
	s_setprio 1
	s_waitcnt lgkmcnt(6)
	v_mfma_f32_16x16x128_f8f6f4 v[186:189], v[2:9], v[34:41], v[186:189]
	v_mfma_f32_16x16x128_f8f6f4 v[194:197], v[10:17], v[34:41], v[194:197]
	s_waitcnt lgkmcnt(4)
	v_mfma_f32_16x16x128_f8f6f4 v[190:193], v[2:9], v[42:49], v[190:193]
	v_mfma_f32_16x16x128_f8f6f4 v[182:185], v[10:17], v[42:49], v[182:185]
	s_waitcnt lgkmcnt(2)
	v_mfma_f32_16x16x128_f8f6f4 v[154:157], v[2:9], v[50:57], v[154:157]
	v_mfma_f32_16x16x128_f8f6f4 v[150:153], v[10:17], v[50:57], v[150:153]
	s_waitcnt lgkmcnt(0)
	v_mfma_f32_16x16x128_f8f6f4 v[138:141], v[2:9], v[58:65], v[138:141]
	v_mfma_f32_16x16x128_f8f6f4 v[134:137], v[10:17], v[58:65], v[134:137]
	v_mfma_f32_16x16x128_f8f6f4 v[174:177], v[18:25], v[34:41], v[174:177]
	v_mfma_f32_16x16x128_f8f6f4 v[178:181], v[26:33], v[34:41], v[178:181]
	v_mfma_f32_16x16x128_f8f6f4 v[170:173], v[18:25], v[42:49], v[170:173]
	v_mfma_f32_16x16x128_f8f6f4 v[166:169], v[26:33], v[42:49], v[166:169]
	v_mfma_f32_16x16x128_f8f6f4 v[162:165], v[18:25], v[50:57], v[162:165]
	v_mfma_f32_16x16x128_f8f6f4 v[158:161], v[26:33], v[50:57], v[158:161]
	v_mfma_f32_16x16x128_f8f6f4 v[146:149], v[18:25], v[58:65], v[146:149]
	v_mfma_f32_16x16x128_f8f6f4 v[142:145], v[26:33], v[58:65], v[142:145]
	s_setprio 0
	s_barrier
	ds_read_b128 v[34:37], v207 offset:49152
	ds_read_b128 v[38:41], v207 offset:50176
	ds_read_b128 v[42:45], v207 offset:51200
	ds_read_b128 v[46:49], v207 offset:52224
	ds_read_b128 v[50:53], v207 offset:53248
	ds_read_b128 v[54:57], v207 offset:54272
	ds_read_b128 v[58:61], v207 offset:55296
	ds_read_b128 v[62:65], v207 offset:56320
	s_add_i32 s28, s65, 0x18000
	s_mov_b32 m0, s28
	s_nop 0
	global_load_lds_dwordx4 v204, s[30:31]
	s_add_i32 s28, s65, 0x1a000
	s_mov_b32 m0, s28
	s_nop 0
	global_load_lds_dwordx4 v205, s[30:31]
	s_add_u32 s26, s26, 0x2080
	s_addc_u32 s27, s27, 0
	s_add_i32 s28, s65, 0x1c000
	s_mov_b32 m0, s28
	s_nop 0
	global_load_lds_dwordx4 v204, s[26:27]
	s_add_i32 s28, s65, 0x1e000
	s_mov_b32 m0, s28
	s_nop 0
	global_load_lds_dwordx4 v205, s[26:27]
	s_waitcnt vmcnt(6)
	s_waitcnt lgkmcnt(0)
	s_barrier
	s_setprio 1
	s_waitcnt lgkmcnt(6)
	v_mfma_f32_16x16x128_f8f6f4 v[122:125], v[2:9], v[34:41], v[122:125]
	v_mfma_f32_16x16x128_f8f6f4 v[118:121], v[10:17], v[34:41], v[118:121]
	s_waitcnt lgkmcnt(4)
	v_mfma_f32_16x16x128_f8f6f4 v[106:109], v[2:9], v[42:49], v[106:109]
	v_mfma_f32_16x16x128_f8f6f4 v[102:105], v[10:17], v[42:49], v[102:105]
	s_add_i32 s98, s65, 0x8000
	s_mov_b32 m0, s98
	s_nop 0
	global_load_lds_dwordx4 v66, s[24:25]
	s_waitcnt lgkmcnt(2)
	v_mfma_f32_16x16x128_f8f6f4 v[90:93], v[2:9], v[50:57], v[90:93]
	v_mfma_f32_16x16x128_f8f6f4 v[86:89], v[10:17], v[50:57], v[86:89]
	s_waitcnt lgkmcnt(0)
	v_mfma_f32_16x16x128_f8f6f4 v[74:77], v[2:9], v[58:65], v[74:77]
	v_mfma_f32_16x16x128_f8f6f4 v[70:73], v[10:17], v[58:65], v[70:73]
	v_mfma_f32_16x16x128_f8f6f4 v[130:133], v[18:25], v[34:41], v[130:133]
	v_mfma_f32_16x16x128_f8f6f4 v[126:129], v[26:33], v[34:41], v[126:129]
	v_mfma_f32_16x16x128_f8f6f4 v[114:117], v[18:25], v[42:49], v[114:117]
	v_mfma_f32_16x16x128_f8f6f4 v[110:113], v[26:33], v[42:49], v[110:113]
	s_add_i32 s98, s65, 0xa000
	s_mov_b32 m0, s98
	s_nop 0
	global_load_lds_dwordx4 v67, s[24:25]
	v_mfma_f32_16x16x128_f8f6f4 v[98:101], v[18:25], v[50:57], v[98:101]
	v_mfma_f32_16x16x128_f8f6f4 v[94:97], v[26:33], v[50:57], v[94:97]
	v_mfma_f32_16x16x128_f8f6f4 v[82:85], v[18:25], v[58:65], v[82:85]
	v_mfma_f32_16x16x128_f8f6f4 v[78:81], v[26:33], v[58:65], v[78:81]
	s_setprio 0
	s_barrier
	s_add_i32 s64, s64, 2
	s_add_u32 s23, s23, 0x100
	s_addc_u32 s63, s63, 0
	s_add_u32 s2, s2, 0x100
	s_addc_u32 s3, s3, 0
	s_cmp_gt_u32 s64, 5
	s_branch .LBB0_959

; #define PG8_STAGE(bufoff, gbase, voff) do { PG8_GLDS((const char*)(gbase), (voff)[0], ldsb + (bufoff)); PG8_GLDS((const char*)(gbase), (voff)[1], ldsb + (bufoff) + 8192u); } while (0)
; #define PG8_STAGEA(bufoff, gbase, o0, o1) do { PG8_GLDS((const char*)(gbase), (o0), ldsb + (bufoff)); PG8_GLDS((const char*)(gbase), (o1), ldsb + (bufoff) + 8192u); } while (0)
; #define PG8_STAGEA1(bufoff, gbase) do { if constexpr (Sched::GATHER) { PG8_STAGEA(bufoff, gbase, vA2, vA3); } else { PG8_STAGEA(bufoff, (gbase) + hstep, vA0, vA1); } } while (0)
; #define PG8_WAIT_VR() PG8_WAIT_V(8)
; #define PG8_WAIT_VX() do { if (relax) asm volatile("s_waitcnt vmcnt(%0)" :: "n"(8 + Epi::RELAX) : "memory"); else PG8_WAIT_V(8); } while (0)
; #define PG8_WAIT_L(n) asm volatile("s_waitcnt lgkmcnt(" #n ")" ::: "memory")
; template <class Epi, class Sched, bool F8 = false, bool PF = false, bool I8 = false, int PID = -1>
; __device__ __forceinline__ void gemm_phase(LAS unsigned char* lds, LAS unsigned char* xlds, const int RP, const int RPB, const int nt, const Sched& S, const Epi& E, const int stagger_ticks) {
;     ...
;             PG8_LDB(B0, 0, 0); PG8_LDB(B1, 0, 1); PG8_SCHED; PG8_LDA(At, 0, 0); PG8_STAGEA1(PG8_SA(1, 1), a1);
;             if (Sched::GATHER) { if (last) { const u32x4 nv = *nslot; vA0 = nv.x; vA1 = nv.y; vA2 = nv.z; vA3 = nv.w; } }
;             PG8_WAIT_VX(); PG8_WAIT_L(0); PG8_BAR; PG8_MMA(0, 0, At, B0); PG8_MMA(0, 1, At, B1); PG8_BAR; PG8_SCHED;
;             if constexpr (Epi::BIAS_DMA) { if (t == 0 && has_next) E.bias_dma(nxt, xlds + 8192 + ((ui + 1) & 1) * Epi::BIAS_STRIDE, wid, lane); }
;             PG8_LDA(At, 0, 1); PG8_STAGE(PG8_SB(0, 0), b2, voffB); PG8_STAGE(PG8_SB(0, 1), b2 + hstepB, voffB); PG8_STAGEA(PG8_SA(0, 0), a2, vA0, vA1);
;             PG8_WAIT_VX(); PG8_WAIT_L(0); PG8_BAR; PG8_MMA(1, 0, At, B0); PG8_MMA(1, 1, At, B1); PG8_BAR; PG8_SCHED;
;             PG8_LDB(B0, 1, 0); PG8_LDB(B1, 1, 1); PG8_SCHED; PG8_LDA(At, 1, 0); PG8_STAGEA1(PG8_SA(0, 1), a2);
;             PG8_WAIT_VR(); PG8_WAIT_L(0); PG8_BAR; PG8_MMA(0, 0, At, B0); PG8_MMA(0, 1, At, B1); PG8_BAR; PG8_SCHED;
;             PG8_LDA(At, 1, 1); PG8_STAGE(PG8_SB(1, 0), b3, voffB); PG8_STAGE(PG8_SB(1, 1), b3 + hstepB, voffB); PG8_STAGEA(PG8_SA(1, 0), a3, vA0, vA1);
;             PG8_WAIT_VR(); PG8_WAIT_L(0); PG8_BAR; PG8_MMA(1, 0, At, B0); PG8_MMA(1, 1, At, B1); PG8_BAR; PG8_SCHED;
.LBB0_1062:
	s_add_u32 s30, s26, 0xfffe0080
	s_addc_u32 s31, s27, -1
	s_cmp_eq_u32 s73, 4
	s_cselect_b32 s38, s6, s30
	s_cselect_b32 s39, s7, s31
	s_cselect_b32 s34, s8, s25
	s_cselect_b32 s35, s9, s71
	s_add_u32 s30, s38, 0x80
	s_addc_u32 s31, s39, 0
	s_add_u32 s36, s34, 0x80
	s_addc_u32 s37, s35, 0
	ds_read_b128 v[170:173], v169 offset:16384
	ds_read_b128 v[174:177], v169 offset:17408
	ds_read_b128 v[178:181], v169 offset:18432
	ds_read_b128 v[182:185], v169 offset:19456
	ds_read_b128 v[186:189], v169 offset:20480
	ds_read_b128 v[190:193], v169 offset:21504
	ds_read_b128 v[194:197], v169 offset:22528
	ds_read_b128 v[198:201], v169 offset:23552
	s_add_i32 s75, s74, 0x10000
	s_mov_b32 m0, s75
	s_nop 0
	global_load_lds_dwordx4 v166, s[34:35]
	s_add_i32 s75, s74, 0x12000
	s_mov_b32 m0, s75
	s_nop 0
	global_load_lds_dwordx4 v167, s[34:35]
	s_add_u32 s76, s34, 0x2000
	s_addc_u32 s77, s35, 0
	s_add_i32 s75, s74, 0x14000
	s_mov_b32 m0, s75
	s_nop 0
	global_load_lds_dwordx4 v166, s[76:77]
	s_add_i32 s75, s74, 0x16000
	s_mov_b32 m0, s75
	s_nop 0
	global_load_lds_dwordx4 v167, s[76:77]
	s_add_i32 s75, s74, 0x2000
	s_mov_b32 m0, s74
	s_nop 0
	global_load_lds_dwordx4 v164, s[38:39]
	s_nop 0
	s_mov_b32 m0, s75
	s_nop 0
	global_load_lds_dwordx4 v165, s[38:39]
	s_waitcnt vmcnt(8)
	s_waitcnt lgkmcnt(0)
	s_barrier
	s_setprio 1
	s_waitcnt lgkmcnt(6)
	v_mfma_f32_16x16x128_f8f6f4 v[86:89], v[2:9], v[170:177], v[86:89]
	v_mfma_f32_16x16x128_f8f6f4 v[82:85], v[10:17], v[170:177], v[82:85]
	s_waitcnt lgkmcnt(4)
	v_mfma_f32_16x16x128_f8f6f4 v[70:73], v[2:9], v[178:185], v[70:73]
	v_mfma_f32_16x16x128_f8f6f4 v[66:69], v[10:17], v[178:185], v[66:69]
	s_waitcnt lgkmcnt(2)
	v_mfma_f32_16x16x128_f8f6f4 v[202:205], v[2:9], v[186:193], v[54:57]
	v_mfma_f32_16x16x128_f8f6f4 v[206:209], v[10:17], v[186:193], v[50:53]
	s_waitcnt lgkmcnt(0)
	v_mfma_f32_16x16x128_f8f6f4 v[210:213], v[2:9], v[194:201], v[38:41]
	v_mfma_f32_16x16x128_f8f6f4 v[214:217], v[10:17], v[194:201], v[34:37]
	v_mfma_f32_16x16x128_f8f6f4 v[94:97], v[18:25], v[170:177], v[94:97]
	v_mfma_f32_16x16x128_f8f6f4 v[90:93], v[26:33], v[170:177], v[90:93]
	v_mfma_f32_16x16x128_f8f6f4 v[78:81], v[18:25], v[178:185], v[78:81]
	v_mfma_f32_16x16x128_f8f6f4 v[74:77], v[26:33], v[178:185], v[74:77]
	v_mfma_f32_16x16x128_f8f6f4 v[218:221], v[18:25], v[186:193], v[62:65]
	v_mfma_f32_16x16x128_f8f6f4 v[186:189], v[26:33], v[186:193], v[58:61]
	v_mfma_f32_16x16x128_f8f6f4 v[190:193], v[18:25], v[194:201], v[46:49]
	v_mfma_f32_16x16x128_f8f6f4 v[194:197], v[26:33], v[194:201], v[42:45]
	s_setprio 0
	s_barrier
	v_add_u32_e32 v14, 0x18000, v168
	v_add_u32_e32 v30, 0x1c000, v168
	ds_read_b128 v[2:5], v14
	ds_read_b128 v[6:9], v14 offset:1024
	ds_read_b128 v[10:13], v14 offset:2048
	ds_read_b128 v[14:17], v14 offset:3072
	ds_read_b128 v[18:21], v30
	ds_read_b128 v[22:25], v30 offset:1024
	ds_read_b128 v[26:29], v30 offset:2048
	ds_read_b128 v[30:33], v30 offset:3072
	ds_read_b128 v[34:37], v169 offset:32768
	ds_read_b128 v[38:41], v169 offset:33792
	ds_read_b128 v[42:45], v169 offset:34816
	ds_read_b128 v[46:49], v169 offset:35840
	ds_read_b128 v[50:53], v169 offset:36864
	ds_read_b128 v[54:57], v169 offset:37888
	ds_read_b128 v[58:61], v169 offset:38912
	ds_read_b128 v[62:65], v169 offset:39936
	s_add_u32 s38, s38, 0x20000
	s_addc_u32 s39, s39, 0
	s_add_i32 s75, s74, 0x4000
	s_mov_b32 m0, s75
	s_nop 0
	global_load_lds_dwordx4 v164, s[38:39]
	s_add_i32 s75, s74, 0x6000
	s_mov_b32 m0, s75
	s_nop 0
	global_load_lds_dwordx4 v165, s[38:39]
	s_waitcnt vmcnt(8)
	s_waitcnt lgkmcnt(0)
	s_barrier
	s_setprio 1
	s_waitcnt lgkmcnt(6)
	v_mfma_f32_16x16x128_f8f6f4 v[150:153], v[2:9], v[34:41], v[150:153]
	v_mfma_f32_16x16x128_f8f6f4 v[146:149], v[10:17], v[34:41], v[146:149]
	s_waitcnt lgkmcnt(4)
	v_mfma_f32_16x16x128_f8f6f4 v[134:137], v[2:9], v[42:49], v[134:137]
	v_mfma_f32_16x16x128_f8f6f4 v[130:133], v[10:17], v[42:49], v[130:133]
	s_waitcnt lgkmcnt(2)
	v_mfma_f32_16x16x128_f8f6f4 v[118:121], v[2:9], v[50:57], v[118:121]
	v_mfma_f32_16x16x128_f8f6f4 v[114:117], v[10:17], v[50:57], v[114:117]
	s_waitcnt lgkmcnt(0)
	v_mfma_f32_16x16x128_f8f6f4 v[102:105], v[2:9], v[58:65], v[102:105]
	v_mfma_f32_16x16x128_f8f6f4 v[98:101], v[10:17], v[58:65], v[98:101]
	v_mfma_f32_16x16x128_f8f6f4 v[158:161], v[18:25], v[34:41], v[158:161]
	v_mfma_f32_16x16x128_f8f6f4 v[154:157], v[26:33], v[34:41], v[154:157]
	v_mfma_f32_16x16x128_f8f6f4 v[142:145], v[18:25], v[42:49], v[142:145]
	v_mfma_f32_16x16x128_f8f6f4 v[138:141], v[26:33], v[42:49], v[138:141]
	v_mfma_f32_16x16x128_f8f6f4 v[126:129], v[18:25], v[50:57], v[126:129]
	v_mfma_f32_16x16x128_f8f6f4 v[122:125], v[26:33], v[50:57], v[122:125]
	v_mfma_f32_16x16x128_f8f6f4 v[110:113], v[18:25], v[58:65], v[110:113]
	v_mfma_f32_16x16x128_f8f6f4 v[106:109], v[26:33], v[58:65], v[106:109]
	s_setprio 0
	s_barrier
	ds_read_b128 v[42:45], v169 offset:49152
	ds_read_b128 v[46:49], v169 offset:50176
	ds_read_b128 v[58:61], v169 offset:51200
	ds_read_b128 v[62:65], v169 offset:52224
	ds_read_b128 v[170:173], v169 offset:53248
	ds_read_b128 v[174:177], v169 offset:54272
	ds_read_b128 v[178:181], v169 offset:55296
	ds_read_b128 v[182:185], v169 offset:56320
	s_add_i32 s38, s74, 0x18000
	s_mov_b32 m0, s38
	s_nop 0
	global_load_lds_dwordx4 v166, s[36:37]
	s_add_i32 s38, s74, 0x1a000
	s_mov_b32 m0, s38
	s_nop 0
	global_load_lds_dwordx4 v167, s[36:37]
	s_add_u32 s34, s34, 0x2080
	s_addc_u32 s35, s35, 0
	s_add_i32 s36, s74, 0x1c000
	s_mov_b32 m0, s36
	s_nop 0
	global_load_lds_dwordx4 v166, s[34:35]
	s_add_i32 s36, s74, 0x1e000
	s_mov_b32 m0, s36
	s_nop 0
	global_load_lds_dwordx4 v167, s[34:35]
	s_add_i32 s34, s74, 0x8000
	s_mov_b32 m0, s34
	s_nop 0
	global_load_lds_dwordx4 v164, s[30:31]
	s_add_i32 s74, s74, 0xa000
	s_mov_b32 m0, s74
	s_nop 0
	global_load_lds_dwordx4 v165, s[30:31]
	s_waitcnt vmcnt(8)
	s_waitcnt lgkmcnt(0)
	s_barrier
; #define PG8_WAIT_VR() PG8_WAIT_V(8)
; template <class Epi, class Sched, bool F8 = false, bool PF = false, bool I8 = false, int PID = -1>
; __device__ __forceinline__ void gemm_phase(LAS unsigned char* lds, LAS unsigned char* xlds, const int RP, const int RPB, const int nt, const Sched& S, const Epi& E, const int stagger_ticks) {
;     ...
;         for (int t = 0; t < nt; t += 2) {
;             const bool last = (t == nt - 2);
;             unsigned ldsb = ldsb0; asm volatile("" : "+s"(ldsb));
;             const char* a1 = cA + (size_t)(t + 1) * kstep;
;             const char* a2 = last ? nA : cA + (size_t)(t + 2) * kstep; const char* b2 = last ? nB : cB + (size_t)(t + 2) * kstep;
;             const char* a3 = a2 + kstep; const char* b3 = b2 + kstep;
;             if constexpr (PF) { const char* pfa = (t + 4 < nt) ? cA + (size_t)(t + 4) * kstep : nA + (size_t)(t + 4 - nt) * kstep;
;                 asm volatile("s_mov_b32 m0, %2\n\ts_nop 0\n\tglobal_load_lds_dword %0, %1" :: "v"(voffP), "s"(pfa), "s"(ldsP) : "memory", "m0"); }
;             const bool relax = (Epi::RELAX > 0) && (t == 0) && epi_ran;
;             PG8_LDB(B0, 0, 0); PG8_LDB(B1, 0, 1); PG8_SCHED; PG8_LDA(At, 0, 0); PG8_STAGEA1(PG8_SA(1, 1), a1);
;             if (Sched::GATHER) { if (last) { const u32x4 nv = *nslot; vA0 = nv.x; vA1 = nv.y; vA2 = nv.z; vA3 = nv.w; } }
;             PG8_WAIT_VX(); PG8_WAIT_L(0); PG8_BAR; PG8_MMA(0, 0, At, B0); PG8_MMA(0, 1, At, B1); PG8_BAR; PG8_SCHED;
;             if constexpr (Epi::BIAS_DMA) { if (t == 0 && has_next) E.bias_dma(nxt, xlds + 8192 + ((ui + 1) & 1) * Epi::BIAS_STRIDE, wid, lane); }
;             PG8_LDA(At, 0, 1); PG8_STAGE(PG8_SB(0, 0), b2, voffB); PG8_STAGE(PG8_SB(0, 1), b2 + hstepB, voffB); PG8_STAGEA(PG8_SA(0, 0), a2, vA0, vA1);
;             PG8_WAIT_VX(); PG8_WAIT_L(0); PG8_BAR; PG8_MMA(1, 0, At, B0); PG8_MMA(1, 1, At, B1); PG8_BAR; PG8_SCHED;
;             PG8_LDB(B0, 1, 0); PG8_LDB(B1, 1, 1); PG8_SCHED; PG8_LDA(At, 1, 0); PG8_STAGEA1(PG8_SA(0, 1), a2);
;             PG8_WAIT_VR(); PG8_WAIT_L(0); PG8_BAR; PG8_MMA(0, 0, At, B0); PG8_MMA(0, 1, At, B1); PG8_BAR; PG8_SCHED;
;             PG8_LDA(At, 1, 1); PG8_STAGE(PG8_SB(1, 0), b3, voffB); PG8_STAGE(PG8_SB(1, 1), b3 + hstepB, voffB); PG8_STAGEA(PG8_SA(1, 0), a3, vA0, vA1);
;             PG8_WAIT_VR(); PG8_WAIT_L(0); PG8_BAR; PG8_MMA(1, 0, At, B0); PG8_MMA(1, 1, At, B1); PG8_BAR; PG8_SCHED;
	s_setprio 1
	s_waitcnt lgkmcnt(6)
	v_mfma_f32_16x16x128_f8f6f4 v[86:89], v[2:9], v[42:49], v[86:89]
	v_mfma_f32_16x16x128_f8f6f4 v[82:85], v[10:17], v[42:49], v[82:85]
	s_waitcnt lgkmcnt(4)
	v_mfma_f32_16x16x128_f8f6f4 v[70:73], v[2:9], v[58:65], v[70:73]
	v_mfma_f32_16x16x128_f8f6f4 v[66:69], v[10:17], v[58:65], v[66:69]
	s_waitcnt lgkmcnt(2)
	v_mfma_f32_16x16x128_f8f6f4 v[54:57], v[2:9], v[170:177], v[202:205]
	v_mfma_f32_16x16x128_f8f6f4 v[50:53], v[10:17], v[170:177], v[206:209]
	s_waitcnt lgkmcnt(0)
	v_mfma_f32_16x16x128_f8f6f4 v[38:41], v[2:9], v[178:185], v[210:213]
	v_mfma_f32_16x16x128_f8f6f4 v[34:37], v[10:17], v[178:185], v[214:217]
	v_mfma_f32_16x16x128_f8f6f4 v[94:97], v[18:25], v[42:49], v[94:97]
	v_mfma_f32_16x16x128_f8f6f4 v[90:93], v[26:33], v[42:49], v[90:93]
	v_mfma_f32_16x16x128_f8f6f4 v[78:81], v[18:25], v[58:65], v[78:81]
	v_mfma_f32_16x16x128_f8f6f4 v[74:77], v[26:33], v[58:65], v[74:77]
	v_mfma_f32_16x16x128_f8f6f4 v[62:65], v[18:25], v[170:177], v[218:221]
	v_mfma_f32_16x16x128_f8f6f4 v[58:61], v[26:33], v[170:177], v[186:189]
	v_mfma_f32_16x16x128_f8f6f4 v[46:49], v[18:25], v[178:185], v[190:193]
	v_mfma_f32_16x16x128_f8f6f4 v[42:45], v[26:33], v[178:185], v[194:197]
	s_setprio 0
	s_barrier
	s_add_i32 s73, s73, 2
	s_add_u32 s25, s25, 0x100
	s_addc_u32 s71, s71, 0
	s_add_u32 s26, s26, 0x100
	s_addc_u32 s27, s27, 0
	s_cmp_gt_u32 s73, 5
	s_cbranch_scc1 .LBB0_1065
.LBB0_1063:
	s_mov_b32 s74, s47
	v_add_u32_e32 v14, 0x10000, v168
	v_add_u32_e32 v30, 0x14000, v168
	ds_read_b128 v[2:5], v14
	ds_read_b128 v[6:9], v14 offset:1024
	ds_read_b128 v[10:13], v14 offset:2048
	ds_read_b128 v[14:17], v14 offset:3072
	ds_read_b128 v[18:21], v30
	ds_read_b128 v[22:25], v30 offset:1024
	ds_read_b128 v[26:29], v30 offset:2048
	ds_read_b128 v[30:33], v30 offset:3072
	ds_read_b128 v[170:173], v169
	ds_read_b128 v[174:177], v169 offset:1024
	ds_read_b128 v[178:181], v169 offset:2048
	ds_read_b128 v[182:185], v169 offset:3072
	ds_read_b128 v[186:189], v169 offset:4096
	ds_read_b128 v[190:193], v169 offset:5120
	ds_read_b128 v[194:197], v169 offset:6144
	ds_read_b128 v[198:201], v169 offset:7168
	s_add_i32 s30, s74, 0xc000
	s_mov_b32 m0, s30
	s_nop 0
	global_load_lds_dwordx4 v164, s[26:27]
	s_add_i32 s30, s74, 0xe000
	s_mov_b32 m0, s30
	s_nop 0
	global_load_lds_dwordx4 v165, s[26:27]
	s_waitcnt vmcnt(8)
	s_waitcnt lgkmcnt(0)
	s_barrier
	s_setprio 1
	s_waitcnt lgkmcnt(6)
	v_mfma_f32_16x16x128_f8f6f4 v[150:153], v[2:9], v[170:177], v[150:153]
	v_mfma_f32_16x16x128_f8f6f4 v[146:149], v[10:17], v[170:177], v[146:149]
	s_waitcnt lgkmcnt(4)
	v_mfma_f32_16x16x128_f8f6f4 v[134:137], v[2:9], v[178:185], v[134:137]
	v_mfma_f32_16x16x128_f8f6f4 v[130:133], v[10:17], v[178:185], v[130:133]
	s_waitcnt lgkmcnt(2)
	v_mfma_f32_16x16x128_f8f6f4 v[118:121], v[2:9], v[186:193], v[118:121]
	v_mfma_f32_16x16x128_f8f6f4 v[114:117], v[10:17], v[186:193], v[114:117]
	s_waitcnt lgkmcnt(0)
	v_mfma_f32_16x16x128_f8f6f4 v[102:105], v[2:9], v[194:201], v[102:105]
	v_mfma_f32_16x16x128_f8f6f4 v[98:101], v[10:17], v[194:201], v[98:101]
	v_mfma_f32_16x16x128_f8f6f4 v[158:161], v[18:25], v[170:177], v[158:161]
	v_mfma_f32_16x16x128_f8f6f4 v[154:157], v[26:33], v[170:177], v[154:157]
	v_mfma_f32_16x16x128_f8f6f4 v[142:145], v[18:25], v[178:185], v[142:145]
	v_mfma_f32_16x16x128_f8f6f4 v[138:141], v[26:33], v[178:185], v[138:141]
	v_mfma_f32_16x16x128_f8f6f4 v[126:129], v[18:25], v[186:193], v[126:129]
	v_mfma_f32_16x16x128_f8f6f4 v[122:125], v[26:33], v[186:193], v[122:125]
	v_mfma_f32_16x16x128_f8f6f4 v[110:113], v[18:25], v[194:201], v[110:113]
	v_mfma_f32_16x16x128_f8f6f4 v[106:109], v[26:33], v[194:201], v[106:109]
	s_setprio 0
	s_barrier
	s_cmp_lg_u32 s73, -2
	s_cselect_b64 s[30:31], -1, 0
	s_or_b64 s[30:31], s[30:31], s[28:29]
	s_and_b64 vcc, exec, s[30:31]
	s_cbranch_vccnz .LBB0_1062
	s_mov_b32 m0, s72
	s_nop 0
	global_load_lds_dword v1, s[2:3]
	s_branch .LBB0_1062
.Lmy_z8t:
	s_mov_b32 s74, s47
	v_add_u32_e32 v14, 0x10000, v168
	v_add_u32_e32 v30, 0x14000, v168
	ds_read_b128 v[2:5], v14
	ds_read_b128 v[6:9], v14 offset:1024
	ds_read_b128 v[10:13], v14 offset:2048
	ds_read_b128 v[14:17], v14 offset:3072
	ds_read_b128 v[18:21], v30
	ds_read_b128 v[22:25], v30 offset:1024
	ds_read_b128 v[26:29], v30 offset:2048
	ds_read_b128 v[30:33], v30 offset:3072
	ds_read_b128 v[170:173], v169
	ds_read_b128 v[174:177], v169 offset:1024
	ds_read_b128 v[178:181], v169 offset:2048
	ds_read_b128 v[182:185], v169 offset:3072
	ds_read_b128 v[186:189], v169 offset:4096
	ds_read_b128 v[190:193], v169 offset:5120
	ds_read_b128 v[194:197], v169 offset:6144
	ds_read_b128 v[198:201], v169 offset:7168
	s_add_i32 s30, s74, 0xc000
	s_mov_b32 m0, s30
	s_nop 0
	global_load_lds_dwordx4 v164, s[26:27]
	s_add_i32 s30, s74, 0xe000
	s_mov_b32 m0, s30
	s_nop 0
	global_load_lds_dwordx4 v165, s[26:27]
	s_waitcnt vmcnt(8)
	s_waitcnt lgkmcnt(0)
	s_barrier
	s_setprio 1
	s_waitcnt lgkmcnt(6)
	v_mfma_f32_16x16x128_f8f6f4 v[150:153], v[2:9], v[170:177], 0
	v_mfma_f32_16x16x128_f8f6f4 v[146:149], v[10:17], v[170:177], 0
	s_waitcnt lgkmcnt(4)
	v_mfma_f32_16x16x128_f8f6f4 v[134:137], v[2:9], v[178:185], 0
	v_mfma_f32_16x16x128_f8f6f4 v[130:133], v[10:17], v[178:185], 0
	s_waitcnt lgkmcnt(2)
	v_mfma_f32_16x16x128_f8f6f4 v[118:121], v[2:9], v[186:193], 0
	v_mfma_f32_16x16x128_f8f6f4 v[114:117], v[10:17], v[186:193], 0
	s_waitcnt lgkmcnt(0)
	v_mfma_f32_16x16x128_f8f6f4 v[102:105], v[2:9], v[194:201], 0
	v_mfma_f32_16x16x128_f8f6f4 v[98:101], v[10:17], v[194:201], 0
	v_mfma_f32_16x16x128_f8f6f4 v[158:161], v[18:25], v[170:177], 0
	v_mfma_f32_16x16x128_f8f6f4 v[154:157], v[26:33], v[170:177], 0
	v_mfma_f32_16x16x128_f8f6f4 v[142:145], v[18:25], v[178:185], 0
	v_mfma_f32_16x16x128_f8f6f4 v[138:141], v[26:33], v[178:185], 0
	v_mfma_f32_16x16x128_f8f6f4 v[126:129], v[18:25], v[186:193], 0
	v_mfma_f32_16x16x128_f8f6f4 v[122:125], v[26:33], v[186:193], 0
	v_mfma_f32_16x16x128_f8f6f4 v[110:113], v[18:25], v[194:201], 0
	v_mfma_f32_16x16x128_f8f6f4 v[106:109], v[26:33], v[194:201], 0
	s_setprio 0
	s_barrier
	s_cmp_lg_u32 s73, -2
	s_cselect_b64 s[30:31], -1, 0
	s_or_b64 s[30:31], s[30:31], s[28:29]
	s_and_b64 vcc, exec, s[30:31]
	s_cbranch_vccnz .Lmy_z8b
	s_mov_b32 m0, s72
	s_nop 0
	global_load_lds_dword v1, s[2:3]
	s_branch .Lmy_z8b
; #define PG8_STAGE(bufoff, gbase, voff) do { PG8_GLDS((const char*)(gbase), (voff)[0], ldsb + (bufoff)); PG8_GLDS((const char*)(gbase), (voff)[1], ldsb + (bufoff) + 8192u); } while (0)
; #define PG8_STAGEA(bufoff, gbase, o0, o1) do { PG8_GLDS((const char*)(gbase), (o0), ldsb + (bufoff)); PG8_GLDS((const char*)(gbase), (o1), ldsb + (bufoff) + 8192u); } while (0)
; #define PG8_STAGEA1(bufoff, gbase) do { if constexpr (Sched::GATHER) { PG8_STAGEA(bufoff, gbase, vA2, vA3); } else { PG8_STAGEA(bufoff, (gbase) + hstep, vA0, vA1); } } while (0)
; #define PG8_LDA(dst, b, h) do { if constexpr (F8) { _Pragma("unroll") for (int m = 0; m < 4; ++m) dst##8[m] = PG8_LD32(lds + PG8_SA(b, h) + aoff + m * 2048); } else { \
;         _Pragma("unroll") for (int m = 0; m < 4; ++m) _Pragma("unroll") for (int k = 0; k < 2; ++k) dst[m][k] = *(const LAS bf16x8*)(lds + PG8_SA(b, h) + aoff + m * 2048 + k * 1024); } } while (0)
; #define PG8_LDB(dst, b, h) do { if constexpr (F8) { _Pragma("unroll") for (int n = 0; n < 2; ++n) dst##8[n] = PG8_LD32(lds + PG8_SB(b, h) + boff + n * 2048); } else { \
;         _Pragma("unroll") for (int n = 0; n < 2; ++n) _Pragma("unroll") for (int k = 0; k < 2; ++k) dst[n][k] = *(const LAS bf16x8*)(lds + PG8_SB(b, h) + boff + n * 2048 + k * 1024); } } while (0)
; #define PG8_WAIT_VR() PG8_WAIT_V(8)
; template <class Epi, class Sched, bool F8 = false, bool PF = false, bool I8 = false, int PID = -1>
; __device__ __forceinline__ void gemm_phase(LAS unsigned char* lds, LAS unsigned char* xlds, const int RP, const int RPB, const int nt, const Sched& S, const Epi& E, const int stagger_ticks) {
;     ...
;             PG8_LDA(At, 0, 1); PG8_STAGE(PG8_SB(0, 0), b2, voffB); PG8_STAGE(PG8_SB(0, 1), b2 + hstepB, voffB); PG8_STAGEA(PG8_SA(0, 0), a2, vA0, vA1);
;             PG8_WAIT_VX(); PG8_WAIT_L(0); PG8_BAR; PG8_MMA(1, 0, At, B0); PG8_MMA(1, 1, At, B1); PG8_BAR; PG8_SCHED;
;             PG8_LDB(B0, 1, 0); PG8_LDB(B1, 1, 1); PG8_SCHED; PG8_LDA(At, 1, 0); PG8_STAGEA1(PG8_SA(0, 1), a2);
;             PG8_WAIT_VR(); PG8_WAIT_L(0); PG8_BAR; PG8_MMA(0, 0, At, B0); PG8_MMA(0, 1, At, B1); PG8_BAR; PG8_SCHED;
;             PG8_LDA(At, 1, 1); PG8_STAGE(PG8_SB(1, 0), b3, voffB); PG8_STAGE(PG8_SB(1, 1), b3 + hstepB, voffB); PG8_STAGEA(PG8_SA(1, 0), a3, vA0, vA1);
;             PG8_WAIT_VR(); PG8_WAIT_L(0); PG8_BAR; PG8_MMA(1, 0, At, B0); PG8_MMA(1, 1, At, B1); PG8_BAR; PG8_SCHED;
.Lmy_z8b:
	s_add_u32 s30, s26, 0xfffe0080
	s_addc_u32 s31, s27, -1
	s_cmp_eq_u32 s73, 4
	s_cselect_b32 s38, s6, s30
	s_cselect_b32 s39, s7, s31
	s_cselect_b32 s34, s8, s25
	s_cselect_b32 s35, s9, s71
	s_add_u32 s30, s38, 0x80
	s_addc_u32 s31, s39, 0
	s_add_u32 s36, s34, 0x80
	s_addc_u32 s37, s35, 0
	ds_read_b128 v[170:173], v169 offset:16384
	ds_read_b128 v[174:177], v169 offset:17408
	ds_read_b128 v[178:181], v169 offset:18432
	ds_read_b128 v[182:185], v169 offset:19456
	ds_read_b128 v[186:189], v169 offset:20480
	ds_read_b128 v[190:193], v169 offset:21504
	ds_read_b128 v[194:197], v169 offset:22528
	ds_read_b128 v[198:201], v169 offset:23552
	s_add_i32 s75, s74, 0x10000
	s_mov_b32 m0, s75
	s_nop 0
	global_load_lds_dwordx4 v166, s[34:35]
	s_add_i32 s75, s74, 0x12000
	s_mov_b32 m0, s75
	s_nop 0
	global_load_lds_dwordx4 v167, s[34:35]
	s_add_u32 s76, s34, 0x2000
	s_addc_u32 s77, s35, 0
	s_add_i32 s75, s74, 0x14000
	s_mov_b32 m0, s75
	s_nop 0
	global_load_lds_dwordx4 v166, s[76:77]
	s_add_i32 s75, s74, 0x16000
	s_mov_b32 m0, s75
	s_nop 0
	global_load_lds_dwordx4 v167, s[76:77]
	s_add_i32 s75, s74, 0x2000
	s_mov_b32 m0, s74
	s_nop 0
	global_load_lds_dwordx4 v164, s[38:39]
	s_nop 0
	s_mov_b32 m0, s75
	s_nop 0
	global_load_lds_dwordx4 v165, s[38:39]
	s_waitcnt vmcnt(8)
	s_waitcnt lgkmcnt(0)
	s_barrier
	s_setprio 1
	s_waitcnt lgkmcnt(6)
	v_mfma_f32_16x16x128_f8f6f4 v[86:89], v[2:9], v[170:177], 0
	v_mfma_f32_16x16x128_f8f6f4 v[82:85], v[10:17], v[170:177], 0
	s_waitcnt lgkmcnt(4)
	v_mfma_f32_16x16x128_f8f6f4 v[70:73], v[2:9], v[178:185], 0
	v_mfma_f32_16x16x128_f8f6f4 v[66:69], v[10:17], v[178:185], 0
	s_waitcnt lgkmcnt(2)
	v_mfma_f32_16x16x128_f8f6f4 v[202:205], v[2:9], v[186:193], 0
	v_mfma_f32_16x16x128_f8f6f4 v[206:209], v[10:17], v[186:193], 0
	s_waitcnt lgkmcnt(0)
	v_mfma_f32_16x16x128_f8f6f4 v[210:213], v[2:9], v[194:201], 0
	v_mfma_f32_16x16x128_f8f6f4 v[214:217], v[10:17], v[194:201], 0
	v_mfma_f32_16x16x128_f8f6f4 v[94:97], v[18:25], v[170:177], 0
	v_mfma_f32_16x16x128_f8f6f4 v[90:93], v[26:33], v[170:177], 0
	v_mfma_f32_16x16x128_f8f6f4 v[78:81], v[18:25], v[178:185], 0
	v_mfma_f32_16x16x128_f8f6f4 v[74:77], v[26:33], v[178:185], 0
	v_mfma_f32_16x16x128_f8f6f4 v[218:221], v[18:25], v[186:193], 0
	v_mfma_f32_16x16x128_f8f6f4 v[186:189], v[26:33], v[186:193], 0
	v_mfma_f32_16x16x128_f8f6f4 v[190:193], v[18:25], v[194:201], 0
	v_mfma_f32_16x16x128_f8f6f4 v[194:197], v[26:33], v[194:201], 0
	s_setprio 0
	s_barrier
	v_add_u32_e32 v14, 0x18000, v168
	v_add_u32_e32 v30, 0x1c000, v168
	ds_read_b128 v[2:5], v14
	ds_read_b128 v[6:9], v14 offset:1024
	ds_read_b128 v[10:13], v14 offset:2048
	ds_read_b128 v[14:17], v14 offset:3072
	ds_read_b128 v[18:21], v30
	ds_read_b128 v[22:25], v30 offset:1024
	ds_read_b128 v[26:29], v30 offset:2048
	ds_read_b128 v[30:33], v30 offset:3072
	ds_read_b128 v[34:37], v169 offset:32768
	ds_read_b128 v[38:41], v169 offset:33792
	ds_read_b128 v[42:45], v169 offset:34816
	ds_read_b128 v[46:49], v169 offset:35840
	ds_read_b128 v[50:53], v169 offset:36864
	ds_read_b128 v[54:57], v169 offset:37888
	ds_read_b128 v[58:61], v169 offset:38912
	ds_read_b128 v[62:65], v169 offset:39936
	s_add_u32 s38, s38, 0x20000
	s_addc_u32 s39, s39, 0
	s_add_i32 s75, s74, 0x4000
	s_mov_b32 m0, s75
	s_nop 0
	global_load_lds_dwordx4 v164, s[38:39]
	s_add_i32 s75, s74, 0x6000
	s_mov_b32 m0, s75
	s_nop 0
	global_load_lds_dwordx4 v165, s[38:39]
	s_waitcnt vmcnt(8)
	s_waitcnt lgkmcnt(0)
	s_barrier
; #define PG8_STAGE(bufoff, gbase, voff) do { PG8_GLDS((const char*)(gbase), (voff)[0], ldsb + (bufoff)); PG8_GLDS((const char*)(gbase), (voff)[1], ldsb + (bufoff) + 8192u); } while (0)
; #define PG8_STAGEA(bufoff, gbase, o0, o1) do { PG8_GLDS((const char*)(gbase), (o0), ldsb + (bufoff)); PG8_GLDS((const char*)(gbase), (o1), ldsb + (bufoff) + 8192u); } while (0)
; #define PG8_STAGEA1(bufoff, gbase) do { if constexpr (Sched::GATHER) { PG8_STAGEA(bufoff, gbase, vA2, vA3); } else { PG8_STAGEA(bufoff, (gbase) + hstep, vA0, vA1); } } while (0)
; #define PG8_LDA(dst, b, h) do { if constexpr (F8) { _Pragma("unroll") for (int m = 0; m < 4; ++m) dst##8[m] = PG8_LD32(lds + PG8_SA(b, h) + aoff + m * 2048); } else { \
;         _Pragma("unroll") for (int m = 0; m < 4; ++m) _Pragma("unroll") for (int k = 0; k < 2; ++k) dst[m][k] = *(const LAS bf16x8*)(lds + PG8_SA(b, h) + aoff + m * 2048 + k * 1024); } } while (0)
; #define PG8_LDB(dst, b, h) do { if constexpr (F8) { _Pragma("unroll") for (int n = 0; n < 2; ++n) dst##8[n] = PG8_LD32(lds + PG8_SB(b, h) + boff + n * 2048); } else { \
;         _Pragma("unroll") for (int n = 0; n < 2; ++n) _Pragma("unroll") for (int k = 0; k < 2; ++k) dst[n][k] = *(const LAS bf16x8*)(lds + PG8_SB(b, h) + boff + n * 2048 + k * 1024); } } while (0)
; #define PG8_WAIT_VR() PG8_WAIT_V(8)
; #define PG8_WAIT_L(n) asm volatile("s_waitcnt lgkmcnt(" #n ")" ::: "memory")
; #define PG8_BAR __builtin_amdgcn_s_barrier()
; #define PG8_SCHED __builtin_amdgcn_sched_barrier(0)
; template <class Epi, class Sched, bool F8 = false, bool PF = false, bool I8 = false, int PID = -1>
; __device__ __forceinline__ void gemm_phase(LAS unsigned char* lds, LAS unsigned char* xlds, const int RP, const int RPB, const int nt, const Sched& S, const Epi& E, const int stagger_ticks) {
;     ...
;             PG8_LDB(B0, 1, 0); PG8_LDB(B1, 1, 1); PG8_SCHED; PG8_LDA(At, 1, 0); PG8_STAGEA1(PG8_SA(0, 1), a2);
;             PG8_WAIT_VR(); PG8_WAIT_L(0); PG8_BAR; PG8_MMA(0, 0, At, B0); PG8_MMA(0, 1, At, B1); PG8_BAR; PG8_SCHED;
;             PG8_LDA(At, 1, 1); PG8_STAGE(PG8_SB(1, 0), b3, voffB); PG8_STAGE(PG8_SB(1, 1), b3 + hstepB, voffB); PG8_STAGEA(PG8_SA(1, 0), a3, vA0, vA1);
;             PG8_WAIT_VR(); PG8_WAIT_L(0); PG8_BAR; PG8_MMA(1, 0, At, B0); PG8_MMA(1, 1, At, B1); PG8_BAR; PG8_SCHED;
	s_setprio 1
	s_waitcnt lgkmcnt(6)
	v_mfma_f32_16x16x128_f8f6f4 v[150:153], v[2:9], v[34:41], v[150:153]
	v_mfma_f32_16x16x128_f8f6f4 v[146:149], v[10:17], v[34:41], v[146:149]
	s_waitcnt lgkmcnt(4)
	v_mfma_f32_16x16x128_f8f6f4 v[134:137], v[2:9], v[42:49], v[134:137]
	v_mfma_f32_16x16x128_f8f6f4 v[130:133], v[10:17], v[42:49], v[130:133]
	s_waitcnt lgkmcnt(2)
	v_mfma_f32_16x16x128_f8f6f4 v[118:121], v[2:9], v[50:57], v[118:121]
	v_mfma_f32_16x16x128_f8f6f4 v[114:117], v[10:17], v[50:57], v[114:117]
	s_waitcnt lgkmcnt(0)
	v_mfma_f32_16x16x128_f8f6f4 v[102:105], v[2:9], v[58:65], v[102:105]
	v_mfma_f32_16x16x128_f8f6f4 v[98:101], v[10:17], v[58:65], v[98:101]
	v_mfma_f32_16x16x128_f8f6f4 v[158:161], v[18:25], v[34:41], v[158:161]
	v_mfma_f32_16x16x128_f8f6f4 v[154:157], v[26:33], v[34:41], v[154:157]
	v_mfma_f32_16x16x128_f8f6f4 v[142:145], v[18:25], v[42:49], v[142:145]
	v_mfma_f32_16x16x128_f8f6f4 v[138:141], v[26:33], v[42:49], v[138:141]
	v_mfma_f32_16x16x128_f8f6f4 v[126:129], v[18:25], v[50:57], v[126:129]
	v_mfma_f32_16x16x128_f8f6f4 v[122:125], v[26:33], v[50:57], v[122:125]
	v_mfma_f32_16x16x128_f8f6f4 v[110:113], v[18:25], v[58:65], v[110:113]
	v_mfma_f32_16x16x128_f8f6f4 v[106:109], v[26:33], v[58:65], v[106:109]
	s_setprio 0
	s_barrier
	ds_read_b128 v[42:45], v169 offset:49152
	ds_read_b128 v[46:49], v169 offset:50176
	ds_read_b128 v[58:61], v169 offset:51200
	ds_read_b128 v[62:65], v169 offset:52224
	ds_read_b128 v[170:173], v169 offset:53248
	ds_read_b128 v[174:177], v169 offset:54272
	ds_read_b128 v[178:181], v169 offset:55296
	ds_read_b128 v[182:185], v169 offset:56320
	s_add_i32 s38, s74, 0x18000
	s_mov_b32 m0, s38
	s_nop 0
	global_load_lds_dwordx4 v166, s[36:37]
	s_add_i32 s38, s74, 0x1a000
	s_mov_b32 m0, s38
	s_nop 0
	global_load_lds_dwordx4 v167, s[36:37]
	s_add_u32 s34, s34, 0x2080
	s_addc_u32 s35, s35, 0
	s_add_i32 s36, s74, 0x1c000
	s_mov_b32 m0, s36
	s_nop 0
	global_load_lds_dwordx4 v166, s[34:35]
	s_add_i32 s36, s74, 0x1e000
	s_mov_b32 m0, s36
	s_nop 0
	global_load_lds_dwordx4 v167, s[34:35]
	s_add_i32 s34, s74, 0x8000
	s_mov_b32 m0, s34
	s_nop 0
	global_load_lds_dwordx4 v164, s[30:31]
	s_add_i32 s74, s74, 0xa000
	s_mov_b32 m0, s74
	s_nop 0
	global_load_lds_dwordx4 v165, s[30:31]
	s_waitcnt vmcnt(8)
	s_waitcnt lgkmcnt(0)
	s_barrier
	s_setprio 1
	s_waitcnt lgkmcnt(6)
	v_mfma_f32_16x16x128_f8f6f4 v[86:89], v[2:9], v[42:49], v[86:89]
	v_mfma_f32_16x16x128_f8f6f4 v[82:85], v[10:17], v[42:49], v[82:85]
	s_waitcnt lgkmcnt(4)
	v_mfma_f32_16x16x128_f8f6f4 v[70:73], v[2:9], v[58:65], v[70:73]
	v_mfma_f32_16x16x128_f8f6f4 v[66:69], v[10:17], v[58:65], v[66:69]
	s_waitcnt lgkmcnt(2)
	v_mfma_f32_16x16x128_f8f6f4 v[54:57], v[2:9], v[170:177], v[202:205]
	v_mfma_f32_16x16x128_f8f6f4 v[50:53], v[10:17], v[170:177], v[206:209]
	s_waitcnt lgkmcnt(0)
	v_mfma_f32_16x16x128_f8f6f4 v[38:41], v[2:9], v[178:185], v[210:213]
	v_mfma_f32_16x16x128_f8f6f4 v[34:37], v[10:17], v[178:185], v[214:217]
	v_mfma_f32_16x16x128_f8f6f4 v[94:97], v[18:25], v[42:49], v[94:97]
	v_mfma_f32_16x16x128_f8f6f4 v[90:93], v[26:33], v[42:49], v[90:93]
	v_mfma_f32_16x16x128_f8f6f4 v[78:81], v[18:25], v[58:65], v[78:81]
	v_mfma_f32_16x16x128_f8f6f4 v[74:77], v[26:33], v[58:65], v[74:77]
	v_mfma_f32_16x16x128_f8f6f4 v[62:65], v[18:25], v[170:177], v[218:221]
	v_mfma_f32_16x16x128_f8f6f4 v[58:61], v[26:33], v[170:177], v[186:189]
	v_mfma_f32_16x16x128_f8f6f4 v[46:49], v[18:25], v[178:185], v[190:193]
	v_mfma_f32_16x16x128_f8f6f4 v[42:45], v[26:33], v[178:185], v[194:197]
	s_setprio 0
	s_barrier
	s_add_i32 s73, s73, 2
	s_add_u32 s25, s25, 0x100
	s_addc_u32 s71, s71, 0
	s_add_u32 s26, s26, 0x100
	s_addc_u32 s27, s27, 0
	s_cmp_gt_u32 s73, 5
	s_branch .LBB0_1063
